# bf16 GEMM loops: pre-barrier LDS-read wait lgkmcnt(4) on 16-read segments only (8-read segments wait fully); fp8 loops as before (4 late reads under first 8 MFMAs)
# baseline (speedup 1.0000x reference)
.LBB0_219:
	s_waitcnt lgkmcnt(0)
	s_add_i32 s4, s92, 0x180
	s_add_i32 s5, s93, 0x180
	s_barrier
	s_setprio 1
	s_waitcnt lgkmcnt(7)
	v_mfma_f32_16x16x32_bf16 v[60:63], v[156:159], v[188:191], 0
	s_waitcnt lgkmcnt(6)
	v_mfma_f32_16x16x32_bf16 v[60:63], v[152:155], v[184:187], v[60:63]
	v_mfma_f32_16x16x32_bf16 v[56:59], v[148:151], v[188:191], 0
	s_nop 0
	v_mfma_f32_16x16x32_bf16 v[56:59], v[144:147], v[184:187], v[56:59]
	s_waitcnt lgkmcnt(5)
	v_mfma_f32_16x16x32_bf16 v[52:55], v[156:159], v[180:183], 0
	s_waitcnt lgkmcnt(4)
	v_mfma_f32_16x16x32_bf16 v[52:55], v[152:155], v[176:179], v[52:55]
	v_mfma_f32_16x16x32_bf16 v[48:51], v[148:151], v[180:183], 0
	s_nop 0
	v_mfma_f32_16x16x32_bf16 v[48:51], v[144:147], v[176:179], v[48:51]
	s_waitcnt lgkmcnt(3)
	v_mfma_f32_16x16x32_bf16 v[44:47], v[156:159], v[172:175], 0
	s_waitcnt lgkmcnt(2)
	v_mfma_f32_16x16x32_bf16 v[44:47], v[152:155], v[168:171], v[44:47]
	v_mfma_f32_16x16x32_bf16 v[40:43], v[148:151], v[172:175], 0
	s_nop 0
	v_mfma_f32_16x16x32_bf16 v[40:43], v[144:147], v[168:171], v[40:43]
	s_waitcnt lgkmcnt(1)
	v_mfma_f32_16x16x32_bf16 v[36:39], v[156:159], v[164:167], 0
	s_waitcnt lgkmcnt(0)
	v_mfma_f32_16x16x32_bf16 v[36:39], v[152:155], v[160:163], v[36:39]
	v_mfma_f32_16x16x32_bf16 v[32:35], v[148:151], v[164:167], 0
	s_nop 0
	v_mfma_f32_16x16x32_bf16 v[32:35], v[144:147], v[160:163], v[32:35]
	s_setprio 0
	s_setprio 1
	v_mfma_f32_16x16x32_bf16 v[28:31], v[140:143], v[188:191], 0
	s_nop 0
	v_mfma_f32_16x16x32_bf16 v[28:31], v[136:139], v[184:187], v[28:31]
	v_mfma_f32_16x16x32_bf16 v[24:27], v[132:135], v[188:191], 0
	s_nop 0
	v_mfma_f32_16x16x32_bf16 v[24:27], v[128:131], v[184:187], v[24:27]
	v_mfma_f32_16x16x32_bf16 v[20:23], v[140:143], v[180:183], 0
	s_nop 0
	v_mfma_f32_16x16x32_bf16 v[20:23], v[136:139], v[176:179], v[20:23]
	v_mfma_f32_16x16x32_bf16 v[16:19], v[132:135], v[180:183], 0
	s_nop 0
	v_mfma_f32_16x16x32_bf16 v[16:19], v[128:131], v[176:179], v[16:19]
	v_mfma_f32_16x16x32_bf16 v[12:15], v[140:143], v[172:175], 0
	s_nop 0
	v_mfma_f32_16x16x32_bf16 v[12:15], v[136:139], v[168:171], v[12:15]
	v_mfma_f32_16x16x32_bf16 v[8:11], v[132:135], v[172:175], 0
	s_nop 0
	v_mfma_f32_16x16x32_bf16 v[8:11], v[128:131], v[168:171], v[8:11]
	v_mfma_f32_16x16x32_bf16 v[4:7], v[140:143], v[164:167], 0
	s_nop 0
	v_mfma_f32_16x16x32_bf16 v[4:7], v[136:139], v[160:163], v[4:7]
	v_mfma_f32_16x16x32_bf16 v[0:3], v[132:135], v[164:167], 0
	s_nop 0
	v_mfma_f32_16x16x32_bf16 v[0:3], v[128:131], v[160:163], v[0:3]
	s_setprio 0
	s_barrier
	ds_read_b128 v[156:159], v211
	ds_read_b128 v[152:155], v212
	ds_read_b128 v[148:151], v213
	ds_read_b128 v[144:147], v214
	ds_read_b128 v[140:143], v215
	ds_read_b128 v[136:139], v216
	ds_read_b128 v[132:135], v217
	ds_read_b128 v[128:131], v218
	s_mov_b32 m0, s69
	s_add_i32 s14, s92, 0x20100
	buffer_load_dwordx4 v196, s[8:11], s14 offen lds
	s_add_i32 s14, s92, 0x30100
	s_mov_b32 m0, s70
	s_nop 0
	buffer_load_dwordx4 v196, s[8:11], s14 offen lds
	ds_read_b128 v[160:163], v219 offset:32768
	ds_read_b128 v[164:167], v219 offset:33792
	ds_read_b128 v[168:171], v219 offset:34816
	ds_read_b128 v[172:175], v219 offset:35840
	ds_read_b128 v[176:179], v219 offset:36864
	ds_read_b128 v[180:183], v219 offset:37888
	ds_read_b128 v[184:187], v219 offset:38912
	ds_read_b128 v[188:191], v219 offset:39936
	s_waitcnt vmcnt(8)
	s_waitcnt lgkmcnt(4)
	s_barrier
	s_setprio 1
	s_waitcnt lgkmcnt(7)
	v_mfma_f32_16x16x32_bf16 v[124:127], v[156:159], v[160:163], v[124:127]
	s_waitcnt lgkmcnt(6)
	v_mfma_f32_16x16x32_bf16 v[124:127], v[152:155], v[164:167], v[124:127]
	v_mfma_f32_16x16x32_bf16 v[120:123], v[148:151], v[160:163], v[120:123]
	s_nop 0
	v_mfma_f32_16x16x32_bf16 v[120:123], v[144:147], v[164:167], v[120:123]
	s_waitcnt lgkmcnt(5)
	v_mfma_f32_16x16x32_bf16 v[116:119], v[156:159], v[168:171], v[116:119]
	s_waitcnt lgkmcnt(4)
	v_mfma_f32_16x16x32_bf16 v[116:119], v[152:155], v[172:175], v[116:119]
	v_mfma_f32_16x16x32_bf16 v[112:115], v[148:151], v[168:171], v[112:115]
	s_nop 0
	v_mfma_f32_16x16x32_bf16 v[112:115], v[144:147], v[172:175], v[112:115]
	s_waitcnt lgkmcnt(3)
	v_mfma_f32_16x16x32_bf16 v[108:111], v[156:159], v[176:179], v[108:111]
	s_waitcnt lgkmcnt(2)
	v_mfma_f32_16x16x32_bf16 v[108:111], v[152:155], v[180:183], v[108:111]
	v_mfma_f32_16x16x32_bf16 v[104:107], v[148:151], v[176:179], v[104:107]
	s_nop 0
	v_mfma_f32_16x16x32_bf16 v[104:107], v[144:147], v[180:183], v[104:107]
	s_waitcnt lgkmcnt(1)
	v_mfma_f32_16x16x32_bf16 v[100:103], v[156:159], v[184:187], v[100:103]
	s_waitcnt lgkmcnt(0)
	v_mfma_f32_16x16x32_bf16 v[100:103], v[152:155], v[188:191], v[100:103]
	v_mfma_f32_16x16x32_bf16 v[96:99], v[148:151], v[184:187], v[96:99]
	s_nop 0
	v_mfma_f32_16x16x32_bf16 v[96:99], v[144:147], v[188:191], v[96:99]
	s_setprio 0
	s_setprio 1
	v_mfma_f32_16x16x32_bf16 v[92:95], v[140:143], v[160:163], v[92:95]
	s_nop 0
	v_mfma_f32_16x16x32_bf16 v[92:95], v[136:139], v[164:167], v[92:95]
	v_mfma_f32_16x16x32_bf16 v[88:91], v[132:135], v[160:163], v[88:91]
	s_nop 0
	v_mfma_f32_16x16x32_bf16 v[88:91], v[128:131], v[164:167], v[88:91]
	v_mfma_f32_16x16x32_bf16 v[84:87], v[140:143], v[168:171], v[84:87]
	s_nop 0
	v_mfma_f32_16x16x32_bf16 v[84:87], v[136:139], v[172:175], v[84:87]
	v_mfma_f32_16x16x32_bf16 v[80:83], v[132:135], v[168:171], v[80:83]
	s_nop 0
	v_mfma_f32_16x16x32_bf16 v[80:83], v[128:131], v[172:175], v[80:83]
	v_mfma_f32_16x16x32_bf16 v[76:79], v[140:143], v[176:179], v[76:79]
	s_nop 0
	v_mfma_f32_16x16x32_bf16 v[76:79], v[136:139], v[180:183], v[76:79]
	v_mfma_f32_16x16x32_bf16 v[72:75], v[132:135], v[176:179], v[72:75]
	s_nop 0
	v_mfma_f32_16x16x32_bf16 v[72:75], v[128:131], v[180:183], v[72:75]
	v_mfma_f32_16x16x32_bf16 v[68:71], v[140:143], v[184:187], v[68:71]
	s_nop 0
	v_mfma_f32_16x16x32_bf16 v[68:71], v[136:139], v[188:191], v[68:71]
	v_mfma_f32_16x16x32_bf16 v[64:67], v[132:135], v[184:187], v[64:67]
	s_nop 0
	v_mfma_f32_16x16x32_bf16 v[64:67], v[128:131], v[188:191], v[64:67]
	s_setprio 0
	s_barrier
	s_mov_b32 m0, s73
	s_mov_b32 s14, s10
	s_mov_b32 s15, s11
	buffer_load_dwordx4 v202, s[12:15], s5 offen lds
	s_add_i32 s5, s93, 0x80180
	s_mov_b32 m0, s74
	s_nop 0
	buffer_load_dwordx4 v202, s[12:15], s5 offen lds
	s_add_i32 s5, s93, 0x8180
	s_mov_b32 m0, s77
	s_nop 0
	buffer_load_dwordx4 v202, s[12:15], s5 offen lds
	s_add_i32 s5, s93, 0x88180
	s_mov_b32 m0, s78
	s_nop 0
	buffer_load_dwordx4 v202, s[12:15], s5 offen lds
	s_mov_b32 m0, s75
	s_nop 0
	buffer_load_dwordx4 v196, s[8:11], s4 offen lds
	s_add_i32 s4, s92, 0x10180
	s_mov_b32 m0, s76
	s_nop 0
	buffer_load_dwordx4 v196, s[8:11], s4 offen lds
	ds_read_b128 v[160:163], v219 offset:49152
	ds_read_b128 v[164:167], v219 offset:50176
	ds_read_b128 v[168:171], v219 offset:51200
	ds_read_b128 v[172:175], v219 offset:52224
	ds_read_b128 v[176:179], v219 offset:53248
	ds_read_b128 v[180:183], v219 offset:54272
	ds_read_b128 v[184:187], v219 offset:55296
	ds_read_b128 v[188:191], v219 offset:56320
	s_waitcnt vmcnt(8)
	s_waitcnt lgkmcnt(0)
	s_barrier
	s_setprio 1
	s_waitcnt lgkmcnt(7)
	v_mfma_f32_16x16x32_bf16 v[60:63], v[156:159], v[160:163], v[60:63]
	s_waitcnt lgkmcnt(6)
	v_mfma_f32_16x16x32_bf16 v[60:63], v[152:155], v[164:167], v[60:63]
	v_mfma_f32_16x16x32_bf16 v[56:59], v[148:151], v[160:163], v[56:59]
	s_nop 0
	v_mfma_f32_16x16x32_bf16 v[56:59], v[144:147], v[164:167], v[56:59]
	s_waitcnt lgkmcnt(5)
	v_mfma_f32_16x16x32_bf16 v[52:55], v[156:159], v[168:171], v[52:55]
	s_waitcnt lgkmcnt(4)
	v_mfma_f32_16x16x32_bf16 v[52:55], v[152:155], v[172:175], v[52:55]
	v_mfma_f32_16x16x32_bf16 v[48:51], v[148:151], v[168:171], v[48:51]
	s_nop 0
	v_mfma_f32_16x16x32_bf16 v[48:51], v[144:147], v[172:175], v[48:51]
	s_waitcnt lgkmcnt(3)
	v_mfma_f32_16x16x32_bf16 v[44:47], v[156:159], v[176:179], v[44:47]
	s_waitcnt lgkmcnt(2)
	v_mfma_f32_16x16x32_bf16 v[44:47], v[152:155], v[180:183], v[44:47]
	v_mfma_f32_16x16x32_bf16 v[40:43], v[148:151], v[176:179], v[40:43]
	s_nop 0
	v_mfma_f32_16x16x32_bf16 v[40:43], v[144:147], v[180:183], v[40:43]
	s_waitcnt lgkmcnt(1)
	v_mfma_f32_16x16x32_bf16 v[36:39], v[156:159], v[184:187], v[36:39]
	s_waitcnt lgkmcnt(0)
	v_mfma_f32_16x16x32_bf16 v[36:39], v[152:155], v[188:191], v[36:39]
	v_mfma_f32_16x16x32_bf16 v[32:35], v[148:151], v[184:187], v[32:35]
	s_nop 0
	v_mfma_f32_16x16x32_bf16 v[32:35], v[144:147], v[188:191], v[32:35]
	s_setprio 0
	s_setprio 1
	v_mfma_f32_16x16x32_bf16 v[28:31], v[140:143], v[160:163], v[28:31]
	s_nop 0
	v_mfma_f32_16x16x32_bf16 v[28:31], v[136:139], v[164:167], v[28:31]
	v_mfma_f32_16x16x32_bf16 v[24:27], v[132:135], v[160:163], v[24:27]
	s_nop 0
	v_mfma_f32_16x16x32_bf16 v[24:27], v[128:131], v[164:167], v[24:27]
	v_mfma_f32_16x16x32_bf16 v[20:23], v[140:143], v[168:171], v[20:23]
	s_nop 0
	v_mfma_f32_16x16x32_bf16 v[20:23], v[136:139], v[172:175], v[20:23]
	v_mfma_f32_16x16x32_bf16 v[16:19], v[132:135], v[168:171], v[16:19]
	s_nop 0
	v_mfma_f32_16x16x32_bf16 v[16:19], v[128:131], v[172:175], v[16:19]
	v_mfma_f32_16x16x32_bf16 v[12:15], v[140:143], v[176:179], v[12:15]
	s_nop 0
	v_mfma_f32_16x16x32_bf16 v[12:15], v[136:139], v[180:183], v[12:15]
	v_mfma_f32_16x16x32_bf16 v[8:11], v[132:135], v[176:179], v[8:11]
	s_nop 0
	v_mfma_f32_16x16x32_bf16 v[8:11], v[128:131], v[180:183], v[8:11]
	v_mfma_f32_16x16x32_bf16 v[4:7], v[140:143], v[184:187], v[4:7]
	s_nop 0
	v_mfma_f32_16x16x32_bf16 v[4:7], v[136:139], v[188:191], v[4:7]
	v_mfma_f32_16x16x32_bf16 v[0:3], v[132:135], v[184:187], v[0:3]
	s_nop 0
	v_mfma_f32_16x16x32_bf16 v[0:3], v[128:131], v[188:191], v[0:3]
	s_setprio 0
	s_barrier
	s_add_i32 s4, s92, 0x30180
	s_add_i32 s5, s93, 0x200
	s_mov_b32 s33, 0
.LBB0_220:
	ds_read_b128 v[128:131], v203
	ds_read_b128 v[132:135], v204
	ds_read_b128 v[136:139], v205
	ds_read_b128 v[140:143], v206
	ds_read_b128 v[144:147], v207
	ds_read_b128 v[148:151], v208
	ds_read_b128 v[152:155], v209
	ds_read_b128 v[156:159], v210
	s_add_i32 s66, s4, 0xfffd0080
	s_cmp_eq_u32 s33, 4
	s_cselect_b32 s66, s90, s66
	s_cselect_b32 s92, s91, s5
	s_add_i32 s67, s66, 0x80
	s_mov_b32 m0, s79
	s_add_i32 s93, s4, 0xffff0000
	buffer_load_dwordx4 v196, s[8:11], s93 offen lds
	s_mov_b32 m0, s81
	s_nop 0
	buffer_load_dwordx4 v196, s[8:11], s4 offen lds
	ds_read_b128 v[160:163], v219
	ds_read_b128 v[164:167], v219 offset:1024
	ds_read_b128 v[168:171], v219 offset:2048
	ds_read_b128 v[172:175], v219 offset:3072
	ds_read_b128 v[176:179], v219 offset:4096
	ds_read_b128 v[180:183], v219 offset:5120
	ds_read_b128 v[184:187], v219 offset:6144
	ds_read_b128 v[188:191], v219 offset:7168
	s_waitcnt vmcnt(8)
	s_waitcnt lgkmcnt(4)
	s_barrier
	s_setprio 1
	s_waitcnt lgkmcnt(7)
	v_mfma_f32_16x16x32_bf16 v[124:127], v[128:131], v[160:163], v[124:127]
	s_waitcnt lgkmcnt(6)
	v_mfma_f32_16x16x32_bf16 v[124:127], v[132:135], v[164:167], v[124:127]
	v_mfma_f32_16x16x32_bf16 v[120:123], v[136:139], v[160:163], v[120:123]
	s_nop 0
	v_mfma_f32_16x16x32_bf16 v[120:123], v[140:143], v[164:167], v[120:123]
	s_waitcnt lgkmcnt(5)
	v_mfma_f32_16x16x32_bf16 v[116:119], v[128:131], v[168:171], v[116:119]
	s_waitcnt lgkmcnt(4)
	v_mfma_f32_16x16x32_bf16 v[116:119], v[132:135], v[172:175], v[116:119]
	v_mfma_f32_16x16x32_bf16 v[112:115], v[136:139], v[168:171], v[112:115]
	s_nop 0
	v_mfma_f32_16x16x32_bf16 v[112:115], v[140:143], v[172:175], v[112:115]
	s_waitcnt lgkmcnt(3)
	v_mfma_f32_16x16x32_bf16 v[108:111], v[128:131], v[176:179], v[108:111]
	s_waitcnt lgkmcnt(2)
	v_mfma_f32_16x16x32_bf16 v[108:111], v[132:135], v[180:183], v[108:111]
	v_mfma_f32_16x16x32_bf16 v[104:107], v[136:139], v[176:179], v[104:107]
	s_nop 0
	v_mfma_f32_16x16x32_bf16 v[104:107], v[140:143], v[180:183], v[104:107]
	s_waitcnt lgkmcnt(1)
	v_mfma_f32_16x16x32_bf16 v[100:103], v[128:131], v[184:187], v[100:103]
	s_waitcnt lgkmcnt(0)
	v_mfma_f32_16x16x32_bf16 v[100:103], v[132:135], v[188:191], v[100:103]
	v_mfma_f32_16x16x32_bf16 v[96:99], v[136:139], v[184:187], v[96:99]
	s_nop 0
	v_mfma_f32_16x16x32_bf16 v[96:99], v[140:143], v[188:191], v[96:99]
	s_setprio 0
	s_setprio 1
	v_mfma_f32_16x16x32_bf16 v[92:95], v[144:147], v[160:163], v[92:95]
	s_nop 0
	v_mfma_f32_16x16x32_bf16 v[92:95], v[148:151], v[164:167], v[92:95]
	v_mfma_f32_16x16x32_bf16 v[88:91], v[152:155], v[160:163], v[88:91]
	s_nop 0
	v_mfma_f32_16x16x32_bf16 v[88:91], v[156:159], v[164:167], v[88:91]
	v_mfma_f32_16x16x32_bf16 v[84:87], v[144:147], v[168:171], v[84:87]
	s_nop 0
	v_mfma_f32_16x16x32_bf16 v[84:87], v[148:151], v[172:175], v[84:87]
	v_mfma_f32_16x16x32_bf16 v[80:83], v[152:155], v[168:171], v[80:83]
	s_nop 0
	v_mfma_f32_16x16x32_bf16 v[80:83], v[156:159], v[172:175], v[80:83]
	v_mfma_f32_16x16x32_bf16 v[76:79], v[144:147], v[176:179], v[76:79]
	s_nop 0
	v_mfma_f32_16x16x32_bf16 v[76:79], v[148:151], v[180:183], v[76:79]
	v_mfma_f32_16x16x32_bf16 v[72:75], v[152:155], v[176:179], v[72:75]
	s_nop 0
	v_mfma_f32_16x16x32_bf16 v[72:75], v[156:159], v[180:183], v[72:75]
	v_mfma_f32_16x16x32_bf16 v[68:71], v[144:147], v[184:187], v[68:71]
	s_nop 0
	v_mfma_f32_16x16x32_bf16 v[68:71], v[148:151], v[188:191], v[68:71]
	v_mfma_f32_16x16x32_bf16 v[64:67], v[152:155], v[184:187], v[64:67]
	s_nop 0
	v_mfma_f32_16x16x32_bf16 v[64:67], v[156:159], v[188:191], v[64:67]
	s_setprio 0
	s_barrier
	s_mov_b32 m0, s62
	s_add_i32 s93, s92, 0x80000
	buffer_load_dwordx4 v202, s[12:15], s92 offen lds
	s_mov_b32 m0, s63
	s_nop 0
	buffer_load_dwordx4 v202, s[12:15], s93 offen lds
	s_add_i32 s93, s92, 0x8000
	s_mov_b32 m0, s64
	s_nop 0
	buffer_load_dwordx4 v202, s[12:15], s93 offen lds
	s_add_i32 s93, s92, 0x88000
	s_mov_b32 m0, s65
	s_nop 0
	buffer_load_dwordx4 v202, s[12:15], s93 offen lds
	s_mov_b32 m0, s45
	s_add_i32 s93, s66, 0x10000
	buffer_load_dwordx4 v196, s[8:11], s66 offen lds
	s_mov_b32 m0, s68
	s_nop 0
	buffer_load_dwordx4 v196, s[8:11], s93 offen lds
	ds_read_b128 v[160:163], v219 offset:16384
	ds_read_b128 v[164:167], v219 offset:17408
	ds_read_b128 v[168:171], v219 offset:18432
	ds_read_b128 v[172:175], v219 offset:19456
	ds_read_b128 v[176:179], v219 offset:20480
	ds_read_b128 v[180:183], v219 offset:21504
	ds_read_b128 v[184:187], v219 offset:22528
	ds_read_b128 v[188:191], v219 offset:23552
	s_waitcnt vmcnt(8)
	s_waitcnt lgkmcnt(0)
	s_barrier
	s_setprio 1
	s_waitcnt lgkmcnt(7)
	v_mfma_f32_16x16x32_bf16 v[60:63], v[128:131], v[160:163], v[60:63]
	s_waitcnt lgkmcnt(6)
	v_mfma_f32_16x16x32_bf16 v[60:63], v[132:135], v[164:167], v[60:63]
	v_mfma_f32_16x16x32_bf16 v[56:59], v[136:139], v[160:163], v[56:59]
	s_nop 0
	v_mfma_f32_16x16x32_bf16 v[56:59], v[140:143], v[164:167], v[56:59]
	s_waitcnt lgkmcnt(5)
	v_mfma_f32_16x16x32_bf16 v[52:55], v[128:131], v[168:171], v[52:55]
	s_waitcnt lgkmcnt(4)
	v_mfma_f32_16x16x32_bf16 v[52:55], v[132:135], v[172:175], v[52:55]
	v_mfma_f32_16x16x32_bf16 v[48:51], v[136:139], v[168:171], v[48:51]
	s_nop 0
	v_mfma_f32_16x16x32_bf16 v[48:51], v[140:143], v[172:175], v[48:51]
	s_waitcnt lgkmcnt(3)
	v_mfma_f32_16x16x32_bf16 v[44:47], v[128:131], v[176:179], v[44:47]
	s_waitcnt lgkmcnt(2)
	v_mfma_f32_16x16x32_bf16 v[44:47], v[132:135], v[180:183], v[44:47]
	v_mfma_f32_16x16x32_bf16 v[40:43], v[136:139], v[176:179], v[40:43]
	s_nop 0
	v_mfma_f32_16x16x32_bf16 v[40:43], v[140:143], v[180:183], v[40:43]
	s_waitcnt lgkmcnt(1)
	v_mfma_f32_16x16x32_bf16 v[36:39], v[128:131], v[184:187], v[36:39]
	s_waitcnt lgkmcnt(0)
	v_mfma_f32_16x16x32_bf16 v[36:39], v[132:135], v[188:191], v[36:39]
	v_mfma_f32_16x16x32_bf16 v[32:35], v[136:139], v[184:187], v[32:35]
	s_nop 0
	v_mfma_f32_16x16x32_bf16 v[32:35], v[140:143], v[188:191], v[32:35]
	s_setprio 0
	s_setprio 1
	v_mfma_f32_16x16x32_bf16 v[28:31], v[144:147], v[160:163], v[28:31]
	s_nop 0
	v_mfma_f32_16x16x32_bf16 v[28:31], v[148:151], v[164:167], v[28:31]
	v_mfma_f32_16x16x32_bf16 v[24:27], v[152:155], v[160:163], v[24:27]
	s_nop 0
	v_mfma_f32_16x16x32_bf16 v[24:27], v[156:159], v[164:167], v[24:27]
	v_mfma_f32_16x16x32_bf16 v[20:23], v[144:147], v[168:171], v[20:23]
	s_nop 0
	v_mfma_f32_16x16x32_bf16 v[20:23], v[148:151], v[172:175], v[20:23]
	v_mfma_f32_16x16x32_bf16 v[16:19], v[152:155], v[168:171], v[16:19]
	s_nop 0
	v_mfma_f32_16x16x32_bf16 v[16:19], v[156:159], v[172:175], v[16:19]
	v_mfma_f32_16x16x32_bf16 v[12:15], v[144:147], v[176:179], v[12:15]
	s_nop 0
	v_mfma_f32_16x16x32_bf16 v[12:15], v[148:151], v[180:183], v[12:15]
	v_mfma_f32_16x16x32_bf16 v[8:11], v[152:155], v[176:179], v[8:11]
	s_nop 0
	v_mfma_f32_16x16x32_bf16 v[8:11], v[156:159], v[180:183], v[8:11]
	v_mfma_f32_16x16x32_bf16 v[4:7], v[144:147], v[184:187], v[4:7]
	s_nop 0
	v_mfma_f32_16x16x32_bf16 v[4:7], v[148:151], v[188:191], v[4:7]
	v_mfma_f32_16x16x32_bf16 v[0:3], v[152:155], v[184:187], v[0:3]
	s_nop 0
	v_mfma_f32_16x16x32_bf16 v[0:3], v[156:159], v[188:191], v[0:3]
	s_setprio 0
	s_barrier
	ds_read_b128 v[140:143], v211
	ds_read_b128 v[144:147], v212
	ds_read_b128 v[148:151], v213
	ds_read_b128 v[152:155], v214
	ds_read_b128 v[156:159], v215
	ds_read_b128 v[136:139], v216
	ds_read_b128 v[132:135], v217
	ds_read_b128 v[128:131], v218
	s_mov_b32 m0, s69
	s_add_i32 s93, s66, 0x20000
	buffer_load_dwordx4 v196, s[8:11], s93 offen lds
	s_add_i32 s93, s66, 0x30000
	s_mov_b32 m0, s70
	s_nop 0
	buffer_load_dwordx4 v196, s[8:11], s93 offen lds
	ds_read_b128 v[160:163], v219 offset:32768
	ds_read_b128 v[164:167], v219 offset:33792
	ds_read_b128 v[168:171], v219 offset:34816
	ds_read_b128 v[172:175], v219 offset:35840
	ds_read_b128 v[176:179], v219 offset:36864
	ds_read_b128 v[180:183], v219 offset:37888
	ds_read_b128 v[184:187], v219 offset:38912
	ds_read_b128 v[188:191], v219 offset:39936
	s_waitcnt vmcnt(8)
	s_waitcnt lgkmcnt(4)
	s_barrier
	s_setprio 1
	s_waitcnt lgkmcnt(7)
	v_mfma_f32_16x16x32_bf16 v[124:127], v[140:143], v[160:163], v[124:127]
	s_waitcnt lgkmcnt(6)
	v_mfma_f32_16x16x32_bf16 v[124:127], v[144:147], v[164:167], v[124:127]
	v_mfma_f32_16x16x32_bf16 v[120:123], v[148:151], v[160:163], v[120:123]
	s_nop 0
	v_mfma_f32_16x16x32_bf16 v[120:123], v[152:155], v[164:167], v[120:123]
	s_waitcnt lgkmcnt(5)
	v_mfma_f32_16x16x32_bf16 v[116:119], v[140:143], v[168:171], v[116:119]
	s_waitcnt lgkmcnt(4)
	v_mfma_f32_16x16x32_bf16 v[116:119], v[144:147], v[172:175], v[116:119]
	v_mfma_f32_16x16x32_bf16 v[112:115], v[148:151], v[168:171], v[112:115]
	s_nop 0
	v_mfma_f32_16x16x32_bf16 v[112:115], v[152:155], v[172:175], v[112:115]
	s_waitcnt lgkmcnt(3)
	v_mfma_f32_16x16x32_bf16 v[108:111], v[140:143], v[176:179], v[108:111]
	s_waitcnt lgkmcnt(2)
	v_mfma_f32_16x16x32_bf16 v[108:111], v[144:147], v[180:183], v[108:111]
	v_mfma_f32_16x16x32_bf16 v[104:107], v[148:151], v[176:179], v[104:107]
	s_nop 0
	v_mfma_f32_16x16x32_bf16 v[104:107], v[152:155], v[180:183], v[104:107]
	s_waitcnt lgkmcnt(1)
	v_mfma_f32_16x16x32_bf16 v[100:103], v[140:143], v[184:187], v[100:103]
	s_waitcnt lgkmcnt(0)
	v_mfma_f32_16x16x32_bf16 v[100:103], v[144:147], v[188:191], v[100:103]
	v_mfma_f32_16x16x32_bf16 v[96:99], v[148:151], v[184:187], v[96:99]
	s_nop 0
	v_mfma_f32_16x16x32_bf16 v[96:99], v[152:155], v[188:191], v[96:99]
	s_setprio 0
	s_setprio 1
	v_mfma_f32_16x16x32_bf16 v[92:95], v[156:159], v[160:163], v[92:95]
	s_nop 0
	v_mfma_f32_16x16x32_bf16 v[92:95], v[136:139], v[164:167], v[92:95]
	v_mfma_f32_16x16x32_bf16 v[88:91], v[132:135], v[160:163], v[88:91]
	s_nop 0
	v_mfma_f32_16x16x32_bf16 v[88:91], v[128:131], v[164:167], v[88:91]
	v_mfma_f32_16x16x32_bf16 v[84:87], v[156:159], v[168:171], v[84:87]
	s_nop 0
	v_mfma_f32_16x16x32_bf16 v[84:87], v[136:139], v[172:175], v[84:87]
	v_mfma_f32_16x16x32_bf16 v[80:83], v[132:135], v[168:171], v[80:83]
	s_nop 0
	v_mfma_f32_16x16x32_bf16 v[80:83], v[128:131], v[172:175], v[80:83]
	v_mfma_f32_16x16x32_bf16 v[76:79], v[156:159], v[176:179], v[76:79]
	s_nop 0
	v_mfma_f32_16x16x32_bf16 v[76:79], v[136:139], v[180:183], v[76:79]
	v_mfma_f32_16x16x32_bf16 v[72:75], v[132:135], v[176:179], v[72:75]
	s_nop 0
	v_mfma_f32_16x16x32_bf16 v[72:75], v[128:131], v[180:183], v[72:75]
	v_mfma_f32_16x16x32_bf16 v[68:71], v[156:159], v[184:187], v[68:71]
	s_nop 0
	v_mfma_f32_16x16x32_bf16 v[68:71], v[136:139], v[188:191], v[68:71]
	v_mfma_f32_16x16x32_bf16 v[64:67], v[132:135], v[184:187], v[64:67]
	s_nop 0
	v_mfma_f32_16x16x32_bf16 v[64:67], v[128:131], v[188:191], v[64:67]
	s_setprio 0
	s_barrier
	s_mov_b32 m0, s73
	s_add_i32 s93, s92, 0x80
	buffer_load_dwordx4 v202, s[12:15], s93 offen lds
	s_add_i32 s93, s92, 0x80080
	s_mov_b32 m0, s74
	s_add_i32 s66, s66, 0x10080
	buffer_load_dwordx4 v202, s[12:15], s93 offen lds
	s_add_i32 s93, s92, 0x8080
	s_mov_b32 m0, s77
	s_add_i32 s92, s92, 0x88080
	buffer_load_dwordx4 v202, s[12:15], s93 offen lds
	s_mov_b32 m0, s78
	s_nop 0
	buffer_load_dwordx4 v202, s[12:15], s92 offen lds
	s_mov_b32 m0, s75
	s_nop 0
	buffer_load_dwordx4 v196, s[8:11], s67 offen lds
	s_mov_b32 m0, s76
	s_nop 0
	buffer_load_dwordx4 v196, s[8:11], s66 offen lds
	ds_read_b128 v[160:163], v219 offset:49152
	ds_read_b128 v[164:167], v219 offset:50176
	ds_read_b128 v[168:171], v219 offset:51200
	ds_read_b128 v[172:175], v219 offset:52224
	ds_read_b128 v[176:179], v219 offset:53248
	ds_read_b128 v[180:183], v219 offset:54272
	ds_read_b128 v[184:187], v219 offset:55296
	ds_read_b128 v[188:191], v219 offset:56320
	s_waitcnt vmcnt(8)
	s_waitcnt lgkmcnt(0)
	s_barrier
	s_setprio 1
	s_waitcnt lgkmcnt(7)
	v_mfma_f32_16x16x32_bf16 v[60:63], v[140:143], v[160:163], v[60:63]
	s_waitcnt lgkmcnt(6)
	v_mfma_f32_16x16x32_bf16 v[60:63], v[144:147], v[164:167], v[60:63]
	v_mfma_f32_16x16x32_bf16 v[56:59], v[148:151], v[160:163], v[56:59]
	s_nop 0
	v_mfma_f32_16x16x32_bf16 v[56:59], v[152:155], v[164:167], v[56:59]
	s_waitcnt lgkmcnt(5)
	v_mfma_f32_16x16x32_bf16 v[52:55], v[140:143], v[168:171], v[52:55]
	s_waitcnt lgkmcnt(4)
	v_mfma_f32_16x16x32_bf16 v[52:55], v[144:147], v[172:175], v[52:55]
	v_mfma_f32_16x16x32_bf16 v[48:51], v[148:151], v[168:171], v[48:51]
	s_nop 0
	v_mfma_f32_16x16x32_bf16 v[48:51], v[152:155], v[172:175], v[48:51]
	s_waitcnt lgkmcnt(3)
	v_mfma_f32_16x16x32_bf16 v[44:47], v[140:143], v[176:179], v[44:47]
	s_waitcnt lgkmcnt(2)
	v_mfma_f32_16x16x32_bf16 v[44:47], v[144:147], v[180:183], v[44:47]
	v_mfma_f32_16x16x32_bf16 v[40:43], v[148:151], v[176:179], v[40:43]
	s_nop 0
	v_mfma_f32_16x16x32_bf16 v[40:43], v[152:155], v[180:183], v[40:43]
	s_waitcnt lgkmcnt(1)
	v_mfma_f32_16x16x32_bf16 v[36:39], v[140:143], v[184:187], v[36:39]
	s_waitcnt lgkmcnt(0)
	v_mfma_f32_16x16x32_bf16 v[36:39], v[144:147], v[188:191], v[36:39]
	v_mfma_f32_16x16x32_bf16 v[32:35], v[148:151], v[184:187], v[32:35]
	s_nop 0
	v_mfma_f32_16x16x32_bf16 v[32:35], v[152:155], v[188:191], v[32:35]
	s_setprio 0
	s_setprio 1
	v_mfma_f32_16x16x32_bf16 v[28:31], v[156:159], v[160:163], v[28:31]
	s_nop 0
	v_mfma_f32_16x16x32_bf16 v[28:31], v[136:139], v[164:167], v[28:31]
	v_mfma_f32_16x16x32_bf16 v[24:27], v[132:135], v[160:163], v[24:27]
	s_nop 0
	v_mfma_f32_16x16x32_bf16 v[24:27], v[128:131], v[164:167], v[24:27]
	v_mfma_f32_16x16x32_bf16 v[20:23], v[156:159], v[168:171], v[20:23]
	s_nop 0
	v_mfma_f32_16x16x32_bf16 v[20:23], v[136:139], v[172:175], v[20:23]
	v_mfma_f32_16x16x32_bf16 v[16:19], v[132:135], v[168:171], v[16:19]
	s_nop 0
	v_mfma_f32_16x16x32_bf16 v[16:19], v[128:131], v[172:175], v[16:19]
	v_mfma_f32_16x16x32_bf16 v[12:15], v[156:159], v[176:179], v[12:15]
	s_nop 0
	v_mfma_f32_16x16x32_bf16 v[12:15], v[136:139], v[180:183], v[12:15]
	v_mfma_f32_16x16x32_bf16 v[8:11], v[132:135], v[176:179], v[8:11]
	s_nop 0
	v_mfma_f32_16x16x32_bf16 v[8:11], v[128:131], v[180:183], v[8:11]
	v_mfma_f32_16x16x32_bf16 v[4:7], v[156:159], v[184:187], v[4:7]
	s_nop 0
	v_mfma_f32_16x16x32_bf16 v[4:7], v[136:139], v[188:191], v[4:7]
	v_mfma_f32_16x16x32_bf16 v[0:3], v[132:135], v[184:187], v[0:3]
	s_nop 0
	v_mfma_f32_16x16x32_bf16 v[0:3], v[128:131], v[188:191], v[0:3]
	s_setprio 0
	s_barrier
	s_add_i32 s33, s33, 2
	s_addk_i32 s4, 0x100
	s_addk_i32 s5, 0x100
	s_cmp_gt_u32 s33, 5
	s_cbranch_scc0 .LBB0_220
	s_and_b64 vcc, exec, s[16:17]
	s_cbranch_vccz .LBB0_223
	s_barrier

.LBB0_253:
	s_waitcnt lgkmcnt(0)
	s_add_i32 s33, s91, 0x180
	s_add_i32 s42, s90, 0x180
	s_barrier
	s_setprio 1
	s_waitcnt lgkmcnt(7)
	v_mfma_f32_16x16x32_bf16 v[60:63], v[156:159], v[188:191], 0
	s_waitcnt lgkmcnt(6)
	v_mfma_f32_16x16x32_bf16 v[60:63], v[152:155], v[184:187], v[60:63]
	v_mfma_f32_16x16x32_bf16 v[56:59], v[148:151], v[188:191], 0
	s_nop 0
	v_mfma_f32_16x16x32_bf16 v[56:59], v[144:147], v[184:187], v[56:59]
	s_waitcnt lgkmcnt(5)
	v_mfma_f32_16x16x32_bf16 v[52:55], v[156:159], v[180:183], 0
	s_waitcnt lgkmcnt(4)
	v_mfma_f32_16x16x32_bf16 v[52:55], v[152:155], v[176:179], v[52:55]
	v_mfma_f32_16x16x32_bf16 v[48:51], v[148:151], v[180:183], 0
	s_nop 0
	v_mfma_f32_16x16x32_bf16 v[48:51], v[144:147], v[176:179], v[48:51]
	s_waitcnt lgkmcnt(3)
	v_mfma_f32_16x16x32_bf16 v[44:47], v[156:159], v[172:175], 0
	s_waitcnt lgkmcnt(2)
	v_mfma_f32_16x16x32_bf16 v[44:47], v[152:155], v[168:171], v[44:47]
	v_mfma_f32_16x16x32_bf16 v[40:43], v[148:151], v[172:175], 0
	s_nop 0
	v_mfma_f32_16x16x32_bf16 v[40:43], v[144:147], v[168:171], v[40:43]
	s_waitcnt lgkmcnt(1)
	v_mfma_f32_16x16x32_bf16 v[36:39], v[156:159], v[164:167], 0
	s_waitcnt lgkmcnt(0)
	v_mfma_f32_16x16x32_bf16 v[36:39], v[152:155], v[160:163], v[36:39]
	v_mfma_f32_16x16x32_bf16 v[32:35], v[148:151], v[164:167], 0
	s_nop 0
	v_mfma_f32_16x16x32_bf16 v[32:35], v[144:147], v[160:163], v[32:35]
	s_setprio 0
	s_setprio 1
	v_mfma_f32_16x16x32_bf16 v[28:31], v[140:143], v[188:191], 0
	s_nop 0
	v_mfma_f32_16x16x32_bf16 v[28:31], v[136:139], v[184:187], v[28:31]
	v_mfma_f32_16x16x32_bf16 v[24:27], v[132:135], v[188:191], 0
	s_nop 0
	v_mfma_f32_16x16x32_bf16 v[24:27], v[128:131], v[184:187], v[24:27]
	v_mfma_f32_16x16x32_bf16 v[20:23], v[140:143], v[180:183], 0
	s_nop 0
	v_mfma_f32_16x16x32_bf16 v[20:23], v[136:139], v[176:179], v[20:23]
	v_mfma_f32_16x16x32_bf16 v[16:19], v[132:135], v[180:183], 0
	s_nop 0
	v_mfma_f32_16x16x32_bf16 v[16:19], v[128:131], v[176:179], v[16:19]
	v_mfma_f32_16x16x32_bf16 v[12:15], v[140:143], v[172:175], 0
	s_nop 0
	v_mfma_f32_16x16x32_bf16 v[12:15], v[136:139], v[168:171], v[12:15]
	v_mfma_f32_16x16x32_bf16 v[8:11], v[132:135], v[172:175], 0
	s_nop 0
	v_mfma_f32_16x16x32_bf16 v[8:11], v[128:131], v[168:171], v[8:11]
	v_mfma_f32_16x16x32_bf16 v[4:7], v[140:143], v[164:167], 0
	s_nop 0
	v_mfma_f32_16x16x32_bf16 v[4:7], v[136:139], v[160:163], v[4:7]
	v_mfma_f32_16x16x32_bf16 v[0:3], v[132:135], v[164:167], 0
	s_nop 0
	v_mfma_f32_16x16x32_bf16 v[0:3], v[128:131], v[160:163], v[0:3]
	s_setprio 0
	s_barrier
	ds_read_b128 v[156:159], v203
	ds_read_b128 v[152:155], v204
	ds_read_b128 v[148:151], v205
	ds_read_b128 v[144:147], v206
	ds_read_b128 v[140:143], v207
	ds_read_b128 v[136:139], v208
	ds_read_b128 v[132:135], v209
	ds_read_b128 v[128:131], v210
	s_mov_b32 m0, s69
	s_add_i32 s10, s91, 0x20100
	buffer_load_dwordx4 v196, s[4:7], s10 offen lds
	s_add_i32 s10, s91, 0x30100
	s_mov_b32 m0, s70
	s_nop 0
	buffer_load_dwordx4 v196, s[4:7], s10 offen lds
	ds_read_b128 v[160:163], v197 offset:32768
	ds_read_b128 v[164:167], v197 offset:33792
	ds_read_b128 v[168:171], v197 offset:34816
	ds_read_b128 v[172:175], v197 offset:35840
	ds_read_b128 v[176:179], v197 offset:36864
	ds_read_b128 v[180:183], v197 offset:37888
	ds_read_b128 v[184:187], v197 offset:38912
	ds_read_b128 v[188:191], v197 offset:39936
	s_waitcnt vmcnt(8)
	s_waitcnt lgkmcnt(4)
	s_barrier
	s_setprio 1
	s_waitcnt lgkmcnt(7)
	v_mfma_f32_16x16x32_bf16 v[124:127], v[156:159], v[160:163], v[124:127]
	s_waitcnt lgkmcnt(6)
	v_mfma_f32_16x16x32_bf16 v[124:127], v[152:155], v[164:167], v[124:127]
	v_mfma_f32_16x16x32_bf16 v[120:123], v[148:151], v[160:163], v[120:123]
	s_nop 0
	v_mfma_f32_16x16x32_bf16 v[120:123], v[144:147], v[164:167], v[120:123]
	s_waitcnt lgkmcnt(5)
	v_mfma_f32_16x16x32_bf16 v[116:119], v[156:159], v[168:171], v[116:119]
	s_waitcnt lgkmcnt(4)
	v_mfma_f32_16x16x32_bf16 v[116:119], v[152:155], v[172:175], v[116:119]
	v_mfma_f32_16x16x32_bf16 v[112:115], v[148:151], v[168:171], v[112:115]
	s_nop 0
	v_mfma_f32_16x16x32_bf16 v[112:115], v[144:147], v[172:175], v[112:115]
	s_waitcnt lgkmcnt(3)
	v_mfma_f32_16x16x32_bf16 v[108:111], v[156:159], v[176:179], v[108:111]
	s_waitcnt lgkmcnt(2)
	v_mfma_f32_16x16x32_bf16 v[108:111], v[152:155], v[180:183], v[108:111]
	v_mfma_f32_16x16x32_bf16 v[104:107], v[148:151], v[176:179], v[104:107]
	s_nop 0
	v_mfma_f32_16x16x32_bf16 v[104:107], v[144:147], v[180:183], v[104:107]
	s_waitcnt lgkmcnt(1)
	v_mfma_f32_16x16x32_bf16 v[100:103], v[156:159], v[184:187], v[100:103]
	s_waitcnt lgkmcnt(0)
	v_mfma_f32_16x16x32_bf16 v[100:103], v[152:155], v[188:191], v[100:103]
	v_mfma_f32_16x16x32_bf16 v[96:99], v[148:151], v[184:187], v[96:99]
	s_nop 0
	v_mfma_f32_16x16x32_bf16 v[96:99], v[144:147], v[188:191], v[96:99]
	s_setprio 0
	s_setprio 1
	v_mfma_f32_16x16x32_bf16 v[92:95], v[140:143], v[160:163], v[92:95]
	s_nop 0
	v_mfma_f32_16x16x32_bf16 v[92:95], v[136:139], v[164:167], v[92:95]
	v_mfma_f32_16x16x32_bf16 v[88:91], v[132:135], v[160:163], v[88:91]
	s_nop 0
	v_mfma_f32_16x16x32_bf16 v[88:91], v[128:131], v[164:167], v[88:91]
	v_mfma_f32_16x16x32_bf16 v[84:87], v[140:143], v[168:171], v[84:87]
	s_nop 0
	v_mfma_f32_16x16x32_bf16 v[84:87], v[136:139], v[172:175], v[84:87]
	v_mfma_f32_16x16x32_bf16 v[80:83], v[132:135], v[168:171], v[80:83]
	s_nop 0
	v_mfma_f32_16x16x32_bf16 v[80:83], v[128:131], v[172:175], v[80:83]
	v_mfma_f32_16x16x32_bf16 v[76:79], v[140:143], v[176:179], v[76:79]
	s_nop 0
	v_mfma_f32_16x16x32_bf16 v[76:79], v[136:139], v[180:183], v[76:79]
	v_mfma_f32_16x16x32_bf16 v[72:75], v[132:135], v[176:179], v[72:75]
	s_nop 0
	v_mfma_f32_16x16x32_bf16 v[72:75], v[128:131], v[180:183], v[72:75]
	v_mfma_f32_16x16x32_bf16 v[68:71], v[140:143], v[184:187], v[68:71]
	s_nop 0
	v_mfma_f32_16x16x32_bf16 v[68:71], v[136:139], v[188:191], v[68:71]
	v_mfma_f32_16x16x32_bf16 v[64:67], v[132:135], v[184:187], v[64:67]
	s_nop 0
	v_mfma_f32_16x16x32_bf16 v[64:67], v[128:131], v[188:191], v[64:67]
	s_setprio 0
	s_barrier
	s_mov_b32 m0, s72
	s_mov_b32 s10, s6
	s_mov_b32 s11, s7
	buffer_load_dwordx4 v192, s[8:11], s42 offen lds
	s_add_i32 s42, s90, 0x20180
	s_mov_b32 m0, s73
	s_nop 0
	buffer_load_dwordx4 v192, s[8:11], s42 offen lds
	s_add_i32 s42, s90, 0x2180
	s_mov_b32 m0, s76
	s_nop 0
	buffer_load_dwordx4 v192, s[8:11], s42 offen lds
	s_add_i32 s42, s90, 0x22180
	s_mov_b32 m0, s77
	s_nop 0
	buffer_load_dwordx4 v192, s[8:11], s42 offen lds
	s_mov_b32 m0, s74
	s_nop 0
	buffer_load_dwordx4 v196, s[4:7], s33 offen lds
	s_add_i32 s33, s91, 0x10180
	s_mov_b32 m0, s75
	s_nop 0
	buffer_load_dwordx4 v196, s[4:7], s33 offen lds
	ds_read_b128 v[160:163], v197 offset:49152
	ds_read_b128 v[164:167], v197 offset:50176
	ds_read_b128 v[168:171], v197 offset:51200
	ds_read_b128 v[172:175], v197 offset:52224
	ds_read_b128 v[176:179], v197 offset:53248
	ds_read_b128 v[180:183], v197 offset:54272
	ds_read_b128 v[184:187], v197 offset:55296
	ds_read_b128 v[188:191], v197 offset:56320
	s_waitcnt vmcnt(8)
	s_waitcnt lgkmcnt(0)
	s_barrier
	s_setprio 1
	s_waitcnt lgkmcnt(7)
	v_mfma_f32_16x16x32_bf16 v[60:63], v[156:159], v[160:163], v[60:63]
	s_waitcnt lgkmcnt(6)
	v_mfma_f32_16x16x32_bf16 v[60:63], v[152:155], v[164:167], v[60:63]
	v_mfma_f32_16x16x32_bf16 v[56:59], v[148:151], v[160:163], v[56:59]
	s_nop 0
	v_mfma_f32_16x16x32_bf16 v[56:59], v[144:147], v[164:167], v[56:59]
	s_waitcnt lgkmcnt(5)
	v_mfma_f32_16x16x32_bf16 v[52:55], v[156:159], v[168:171], v[52:55]
	s_waitcnt lgkmcnt(4)
	v_mfma_f32_16x16x32_bf16 v[52:55], v[152:155], v[172:175], v[52:55]
	v_mfma_f32_16x16x32_bf16 v[48:51], v[148:151], v[168:171], v[48:51]
	s_nop 0
	v_mfma_f32_16x16x32_bf16 v[48:51], v[144:147], v[172:175], v[48:51]
	s_waitcnt lgkmcnt(3)
	v_mfma_f32_16x16x32_bf16 v[44:47], v[156:159], v[176:179], v[44:47]
	s_waitcnt lgkmcnt(2)
	v_mfma_f32_16x16x32_bf16 v[44:47], v[152:155], v[180:183], v[44:47]
	v_mfma_f32_16x16x32_bf16 v[40:43], v[148:151], v[176:179], v[40:43]
	s_nop 0
	v_mfma_f32_16x16x32_bf16 v[40:43], v[144:147], v[180:183], v[40:43]
	s_waitcnt lgkmcnt(1)
	v_mfma_f32_16x16x32_bf16 v[36:39], v[156:159], v[184:187], v[36:39]
	s_waitcnt lgkmcnt(0)
	v_mfma_f32_16x16x32_bf16 v[36:39], v[152:155], v[188:191], v[36:39]
	v_mfma_f32_16x16x32_bf16 v[32:35], v[148:151], v[184:187], v[32:35]
	s_nop 0
	v_mfma_f32_16x16x32_bf16 v[32:35], v[144:147], v[188:191], v[32:35]
	s_setprio 0
	s_setprio 1
	v_mfma_f32_16x16x32_bf16 v[28:31], v[140:143], v[160:163], v[28:31]
	s_nop 0
	v_mfma_f32_16x16x32_bf16 v[28:31], v[136:139], v[164:167], v[28:31]
	v_mfma_f32_16x16x32_bf16 v[24:27], v[132:135], v[160:163], v[24:27]
	s_nop 0
	v_mfma_f32_16x16x32_bf16 v[24:27], v[128:131], v[164:167], v[24:27]
	v_mfma_f32_16x16x32_bf16 v[20:23], v[140:143], v[168:171], v[20:23]
	s_nop 0
	v_mfma_f32_16x16x32_bf16 v[20:23], v[136:139], v[172:175], v[20:23]
	v_mfma_f32_16x16x32_bf16 v[16:19], v[132:135], v[168:171], v[16:19]
	s_nop 0
	v_mfma_f32_16x16x32_bf16 v[16:19], v[128:131], v[172:175], v[16:19]
	v_mfma_f32_16x16x32_bf16 v[12:15], v[140:143], v[176:179], v[12:15]
	s_nop 0
	v_mfma_f32_16x16x32_bf16 v[12:15], v[136:139], v[180:183], v[12:15]
	v_mfma_f32_16x16x32_bf16 v[8:11], v[132:135], v[176:179], v[8:11]
	s_nop 0
	v_mfma_f32_16x16x32_bf16 v[8:11], v[128:131], v[180:183], v[8:11]
	v_mfma_f32_16x16x32_bf16 v[4:7], v[140:143], v[184:187], v[4:7]
	s_nop 0
	v_mfma_f32_16x16x32_bf16 v[4:7], v[136:139], v[188:191], v[4:7]
	v_mfma_f32_16x16x32_bf16 v[0:3], v[132:135], v[184:187], v[0:3]
	s_nop 0
	v_mfma_f32_16x16x32_bf16 v[0:3], v[128:131], v[188:191], v[0:3]
	s_setprio 0
	s_barrier
	s_add_i32 s33, s91, 0x30180
	s_add_i32 s42, s90, 0x200
	s_mov_b32 s43, 0
.LBB0_254:
	ds_read_b128 v[128:131], v193
	ds_read_b128 v[132:135], v194
	ds_read_b128 v[136:139], v195
	ds_read_b128 v[140:143], v198
	ds_read_b128 v[144:147], v199
	ds_read_b128 v[148:151], v200
	ds_read_b128 v[152:155], v201
	ds_read_b128 v[156:159], v202
	s_add_i32 s66, s33, 0xfffd0080
	s_cmp_eq_u32 s43, 4
	s_cselect_b32 s66, s88, s66
	s_cselect_b32 s90, s89, s42
	s_add_i32 s67, s66, 0x80
	s_mov_b32 m0, s78
	s_add_i32 s91, s33, 0xffff0000
	buffer_load_dwordx4 v196, s[4:7], s91 offen lds
	s_mov_b32 m0, s79
	s_nop 0
	buffer_load_dwordx4 v196, s[4:7], s33 offen lds
	ds_read_b128 v[160:163], v197
	ds_read_b128 v[164:167], v197 offset:1024
	ds_read_b128 v[168:171], v197 offset:2048
	ds_read_b128 v[172:175], v197 offset:3072
	ds_read_b128 v[176:179], v197 offset:4096
	ds_read_b128 v[180:183], v197 offset:5120
	ds_read_b128 v[184:187], v197 offset:6144
	ds_read_b128 v[188:191], v197 offset:7168
	s_waitcnt vmcnt(8)
	s_waitcnt lgkmcnt(4)
	s_barrier
	s_setprio 1
	s_waitcnt lgkmcnt(7)
	v_mfma_f32_16x16x32_bf16 v[124:127], v[128:131], v[160:163], v[124:127]
	s_waitcnt lgkmcnt(6)
	v_mfma_f32_16x16x32_bf16 v[124:127], v[132:135], v[164:167], v[124:127]
	v_mfma_f32_16x16x32_bf16 v[120:123], v[136:139], v[160:163], v[120:123]
	s_nop 0
	v_mfma_f32_16x16x32_bf16 v[120:123], v[140:143], v[164:167], v[120:123]
	s_waitcnt lgkmcnt(5)
	v_mfma_f32_16x16x32_bf16 v[116:119], v[128:131], v[168:171], v[116:119]
	s_waitcnt lgkmcnt(4)
	v_mfma_f32_16x16x32_bf16 v[116:119], v[132:135], v[172:175], v[116:119]
	v_mfma_f32_16x16x32_bf16 v[112:115], v[136:139], v[168:171], v[112:115]
	s_nop 0
	v_mfma_f32_16x16x32_bf16 v[112:115], v[140:143], v[172:175], v[112:115]
	s_waitcnt lgkmcnt(3)
	v_mfma_f32_16x16x32_bf16 v[108:111], v[128:131], v[176:179], v[108:111]
	s_waitcnt lgkmcnt(2)
	v_mfma_f32_16x16x32_bf16 v[108:111], v[132:135], v[180:183], v[108:111]
	v_mfma_f32_16x16x32_bf16 v[104:107], v[136:139], v[176:179], v[104:107]
	s_nop 0
	v_mfma_f32_16x16x32_bf16 v[104:107], v[140:143], v[180:183], v[104:107]
	s_waitcnt lgkmcnt(1)
	v_mfma_f32_16x16x32_bf16 v[100:103], v[128:131], v[184:187], v[100:103]
	s_waitcnt lgkmcnt(0)
	v_mfma_f32_16x16x32_bf16 v[100:103], v[132:135], v[188:191], v[100:103]
	v_mfma_f32_16x16x32_bf16 v[96:99], v[136:139], v[184:187], v[96:99]
	s_nop 0
	v_mfma_f32_16x16x32_bf16 v[96:99], v[140:143], v[188:191], v[96:99]
	s_setprio 0
	s_setprio 1
	v_mfma_f32_16x16x32_bf16 v[92:95], v[144:147], v[160:163], v[92:95]
	s_nop 0
	v_mfma_f32_16x16x32_bf16 v[92:95], v[148:151], v[164:167], v[92:95]
	v_mfma_f32_16x16x32_bf16 v[88:91], v[152:155], v[160:163], v[88:91]
	s_nop 0
	v_mfma_f32_16x16x32_bf16 v[88:91], v[156:159], v[164:167], v[88:91]
	v_mfma_f32_16x16x32_bf16 v[84:87], v[144:147], v[168:171], v[84:87]
	s_nop 0
	v_mfma_f32_16x16x32_bf16 v[84:87], v[148:151], v[172:175], v[84:87]
	v_mfma_f32_16x16x32_bf16 v[80:83], v[152:155], v[168:171], v[80:83]
	s_nop 0
	v_mfma_f32_16x16x32_bf16 v[80:83], v[156:159], v[172:175], v[80:83]
	v_mfma_f32_16x16x32_bf16 v[76:79], v[144:147], v[176:179], v[76:79]
	s_nop 0
	v_mfma_f32_16x16x32_bf16 v[76:79], v[148:151], v[180:183], v[76:79]
	v_mfma_f32_16x16x32_bf16 v[72:75], v[152:155], v[176:179], v[72:75]
	s_nop 0
	v_mfma_f32_16x16x32_bf16 v[72:75], v[156:159], v[180:183], v[72:75]
	v_mfma_f32_16x16x32_bf16 v[68:71], v[144:147], v[184:187], v[68:71]
	s_nop 0
	v_mfma_f32_16x16x32_bf16 v[68:71], v[148:151], v[188:191], v[68:71]
	v_mfma_f32_16x16x32_bf16 v[64:67], v[152:155], v[184:187], v[64:67]
	s_nop 0
	v_mfma_f32_16x16x32_bf16 v[64:67], v[156:159], v[188:191], v[64:67]
	s_setprio 0
	s_barrier
	s_mov_b32 m0, s62
	s_add_i32 s91, s90, 0x20000
	buffer_load_dwordx4 v192, s[8:11], s90 offen lds
	s_mov_b32 m0, s63
	s_nop 0
	buffer_load_dwordx4 v192, s[8:11], s91 offen lds
	s_add_i32 s91, s90, 0x2000
	s_mov_b32 m0, s64
	s_nop 0
	buffer_load_dwordx4 v192, s[8:11], s91 offen lds
	s_add_i32 s91, s90, 0x22000
	s_mov_b32 m0, s65
	s_nop 0
	buffer_load_dwordx4 v192, s[8:11], s91 offen lds
	s_mov_b32 m0, s47
	s_add_i32 s91, s66, 0x10000
	buffer_load_dwordx4 v196, s[4:7], s66 offen lds
	s_mov_b32 m0, s68
	s_nop 0
	buffer_load_dwordx4 v196, s[4:7], s91 offen lds
	ds_read_b128 v[160:163], v197 offset:16384
	ds_read_b128 v[164:167], v197 offset:17408
	ds_read_b128 v[168:171], v197 offset:18432
	ds_read_b128 v[172:175], v197 offset:19456
	ds_read_b128 v[176:179], v197 offset:20480
	ds_read_b128 v[180:183], v197 offset:21504
	ds_read_b128 v[184:187], v197 offset:22528
	ds_read_b128 v[188:191], v197 offset:23552
	s_waitcnt vmcnt(8)
	s_waitcnt lgkmcnt(0)
	s_barrier
	s_setprio 1
	s_waitcnt lgkmcnt(7)
	v_mfma_f32_16x16x32_bf16 v[60:63], v[128:131], v[160:163], v[60:63]
	s_waitcnt lgkmcnt(6)
	v_mfma_f32_16x16x32_bf16 v[60:63], v[132:135], v[164:167], v[60:63]
	v_mfma_f32_16x16x32_bf16 v[56:59], v[136:139], v[160:163], v[56:59]
	s_nop 0
	v_mfma_f32_16x16x32_bf16 v[56:59], v[140:143], v[164:167], v[56:59]
	s_waitcnt lgkmcnt(5)
	v_mfma_f32_16x16x32_bf16 v[52:55], v[128:131], v[168:171], v[52:55]
	s_waitcnt lgkmcnt(4)
	v_mfma_f32_16x16x32_bf16 v[52:55], v[132:135], v[172:175], v[52:55]
	v_mfma_f32_16x16x32_bf16 v[48:51], v[136:139], v[168:171], v[48:51]
	s_nop 0
	v_mfma_f32_16x16x32_bf16 v[48:51], v[140:143], v[172:175], v[48:51]
	s_waitcnt lgkmcnt(3)
	v_mfma_f32_16x16x32_bf16 v[44:47], v[128:131], v[176:179], v[44:47]
	s_waitcnt lgkmcnt(2)
	v_mfma_f32_16x16x32_bf16 v[44:47], v[132:135], v[180:183], v[44:47]
	v_mfma_f32_16x16x32_bf16 v[40:43], v[136:139], v[176:179], v[40:43]
	s_nop 0
	v_mfma_f32_16x16x32_bf16 v[40:43], v[140:143], v[180:183], v[40:43]
	s_waitcnt lgkmcnt(1)
	v_mfma_f32_16x16x32_bf16 v[36:39], v[128:131], v[184:187], v[36:39]
	s_waitcnt lgkmcnt(0)
	v_mfma_f32_16x16x32_bf16 v[36:39], v[132:135], v[188:191], v[36:39]
	v_mfma_f32_16x16x32_bf16 v[32:35], v[136:139], v[184:187], v[32:35]
	s_nop 0
	v_mfma_f32_16x16x32_bf16 v[32:35], v[140:143], v[188:191], v[32:35]
	s_setprio 0
	s_setprio 1
	v_mfma_f32_16x16x32_bf16 v[28:31], v[144:147], v[160:163], v[28:31]
	s_nop 0
	v_mfma_f32_16x16x32_bf16 v[28:31], v[148:151], v[164:167], v[28:31]
	v_mfma_f32_16x16x32_bf16 v[24:27], v[152:155], v[160:163], v[24:27]
	s_nop 0
	v_mfma_f32_16x16x32_bf16 v[24:27], v[156:159], v[164:167], v[24:27]
	v_mfma_f32_16x16x32_bf16 v[20:23], v[144:147], v[168:171], v[20:23]
	s_nop 0
	v_mfma_f32_16x16x32_bf16 v[20:23], v[148:151], v[172:175], v[20:23]
	v_mfma_f32_16x16x32_bf16 v[16:19], v[152:155], v[168:171], v[16:19]
	s_nop 0
	v_mfma_f32_16x16x32_bf16 v[16:19], v[156:159], v[172:175], v[16:19]
	v_mfma_f32_16x16x32_bf16 v[12:15], v[144:147], v[176:179], v[12:15]
	s_nop 0
	v_mfma_f32_16x16x32_bf16 v[12:15], v[148:151], v[180:183], v[12:15]
	v_mfma_f32_16x16x32_bf16 v[8:11], v[152:155], v[176:179], v[8:11]
	s_nop 0
	v_mfma_f32_16x16x32_bf16 v[8:11], v[156:159], v[180:183], v[8:11]
	v_mfma_f32_16x16x32_bf16 v[4:7], v[144:147], v[184:187], v[4:7]
	s_nop 0
	v_mfma_f32_16x16x32_bf16 v[4:7], v[148:151], v[188:191], v[4:7]
	v_mfma_f32_16x16x32_bf16 v[0:3], v[152:155], v[184:187], v[0:3]
	s_nop 0
	v_mfma_f32_16x16x32_bf16 v[0:3], v[156:159], v[188:191], v[0:3]
	s_setprio 0
	s_barrier
	ds_read_b128 v[140:143], v203
	ds_read_b128 v[144:147], v204
	ds_read_b128 v[148:151], v205
	ds_read_b128 v[152:155], v206
	ds_read_b128 v[156:159], v207
	ds_read_b128 v[136:139], v208
	ds_read_b128 v[132:135], v209
	ds_read_b128 v[128:131], v210
	s_mov_b32 m0, s69
	s_add_i32 s91, s66, 0x20000
	buffer_load_dwordx4 v196, s[4:7], s91 offen lds
	s_add_i32 s91, s66, 0x30000
	s_mov_b32 m0, s70
	s_nop 0
	buffer_load_dwordx4 v196, s[4:7], s91 offen lds
	ds_read_b128 v[160:163], v197 offset:32768
	ds_read_b128 v[164:167], v197 offset:33792
	ds_read_b128 v[168:171], v197 offset:34816
	ds_read_b128 v[172:175], v197 offset:35840
	ds_read_b128 v[176:179], v197 offset:36864
	ds_read_b128 v[180:183], v197 offset:37888
	ds_read_b128 v[184:187], v197 offset:38912
	ds_read_b128 v[188:191], v197 offset:39936
	s_waitcnt vmcnt(8)
	s_waitcnt lgkmcnt(4)
	s_barrier
	s_setprio 1
	s_waitcnt lgkmcnt(7)
	v_mfma_f32_16x16x32_bf16 v[124:127], v[140:143], v[160:163], v[124:127]
	s_waitcnt lgkmcnt(6)
	v_mfma_f32_16x16x32_bf16 v[124:127], v[144:147], v[164:167], v[124:127]
	v_mfma_f32_16x16x32_bf16 v[120:123], v[148:151], v[160:163], v[120:123]
	s_nop 0
	v_mfma_f32_16x16x32_bf16 v[120:123], v[152:155], v[164:167], v[120:123]
	s_waitcnt lgkmcnt(5)
	v_mfma_f32_16x16x32_bf16 v[116:119], v[140:143], v[168:171], v[116:119]
	s_waitcnt lgkmcnt(4)
	v_mfma_f32_16x16x32_bf16 v[116:119], v[144:147], v[172:175], v[116:119]
	v_mfma_f32_16x16x32_bf16 v[112:115], v[148:151], v[168:171], v[112:115]
	s_nop 0
	v_mfma_f32_16x16x32_bf16 v[112:115], v[152:155], v[172:175], v[112:115]
	s_waitcnt lgkmcnt(3)
	v_mfma_f32_16x16x32_bf16 v[108:111], v[140:143], v[176:179], v[108:111]
	s_waitcnt lgkmcnt(2)
	v_mfma_f32_16x16x32_bf16 v[108:111], v[144:147], v[180:183], v[108:111]
	v_mfma_f32_16x16x32_bf16 v[104:107], v[148:151], v[176:179], v[104:107]
	s_nop 0
	v_mfma_f32_16x16x32_bf16 v[104:107], v[152:155], v[180:183], v[104:107]
	s_waitcnt lgkmcnt(1)
	v_mfma_f32_16x16x32_bf16 v[100:103], v[140:143], v[184:187], v[100:103]
	s_waitcnt lgkmcnt(0)
	v_mfma_f32_16x16x32_bf16 v[100:103], v[144:147], v[188:191], v[100:103]
	v_mfma_f32_16x16x32_bf16 v[96:99], v[148:151], v[184:187], v[96:99]
	s_nop 0
	v_mfma_f32_16x16x32_bf16 v[96:99], v[152:155], v[188:191], v[96:99]
	s_setprio 0
	s_setprio 1
	v_mfma_f32_16x16x32_bf16 v[92:95], v[156:159], v[160:163], v[92:95]
	s_nop 0
	v_mfma_f32_16x16x32_bf16 v[92:95], v[136:139], v[164:167], v[92:95]
	v_mfma_f32_16x16x32_bf16 v[88:91], v[132:135], v[160:163], v[88:91]
	s_nop 0
	v_mfma_f32_16x16x32_bf16 v[88:91], v[128:131], v[164:167], v[88:91]
	v_mfma_f32_16x16x32_bf16 v[84:87], v[156:159], v[168:171], v[84:87]
	s_nop 0
	v_mfma_f32_16x16x32_bf16 v[84:87], v[136:139], v[172:175], v[84:87]
	v_mfma_f32_16x16x32_bf16 v[80:83], v[132:135], v[168:171], v[80:83]
	s_nop 0
	v_mfma_f32_16x16x32_bf16 v[80:83], v[128:131], v[172:175], v[80:83]
	v_mfma_f32_16x16x32_bf16 v[76:79], v[156:159], v[176:179], v[76:79]
	s_nop 0
	v_mfma_f32_16x16x32_bf16 v[76:79], v[136:139], v[180:183], v[76:79]
	v_mfma_f32_16x16x32_bf16 v[72:75], v[132:135], v[176:179], v[72:75]
	s_nop 0
	v_mfma_f32_16x16x32_bf16 v[72:75], v[128:131], v[180:183], v[72:75]
	v_mfma_f32_16x16x32_bf16 v[68:71], v[156:159], v[184:187], v[68:71]
	s_nop 0
	v_mfma_f32_16x16x32_bf16 v[68:71], v[136:139], v[188:191], v[68:71]
	v_mfma_f32_16x16x32_bf16 v[64:67], v[132:135], v[184:187], v[64:67]
	s_nop 0
	v_mfma_f32_16x16x32_bf16 v[64:67], v[128:131], v[188:191], v[64:67]
	s_setprio 0
	s_barrier
	s_mov_b32 m0, s72
	s_add_i32 s91, s90, 0x80
	buffer_load_dwordx4 v192, s[8:11], s91 offen lds
	s_add_i32 s91, s90, 0x20080
	s_mov_b32 m0, s73
	s_add_i32 s66, s66, 0x10080
	buffer_load_dwordx4 v192, s[8:11], s91 offen lds
	s_add_i32 s91, s90, 0x2080
	s_mov_b32 m0, s76
	s_add_i32 s90, s90, 0x22080
	buffer_load_dwordx4 v192, s[8:11], s91 offen lds
	s_mov_b32 m0, s77
	s_nop 0
	buffer_load_dwordx4 v192, s[8:11], s90 offen lds
	s_mov_b32 m0, s74
	s_nop 0
	buffer_load_dwordx4 v196, s[4:7], s67 offen lds
	s_mov_b32 m0, s75
	s_nop 0
	buffer_load_dwordx4 v196, s[4:7], s66 offen lds
	ds_read_b128 v[160:163], v197 offset:49152
	ds_read_b128 v[164:167], v197 offset:50176
	ds_read_b128 v[168:171], v197 offset:51200
	ds_read_b128 v[172:175], v197 offset:52224
	ds_read_b128 v[176:179], v197 offset:53248
	ds_read_b128 v[180:183], v197 offset:54272
	ds_read_b128 v[184:187], v197 offset:55296
	ds_read_b128 v[188:191], v197 offset:56320
	s_waitcnt vmcnt(8)
	s_waitcnt lgkmcnt(0)
	s_barrier
	s_setprio 1
	s_waitcnt lgkmcnt(7)
	v_mfma_f32_16x16x32_bf16 v[60:63], v[140:143], v[160:163], v[60:63]
	s_waitcnt lgkmcnt(6)
	v_mfma_f32_16x16x32_bf16 v[60:63], v[144:147], v[164:167], v[60:63]
	v_mfma_f32_16x16x32_bf16 v[56:59], v[148:151], v[160:163], v[56:59]
	s_nop 0
	v_mfma_f32_16x16x32_bf16 v[56:59], v[152:155], v[164:167], v[56:59]
	s_waitcnt lgkmcnt(5)
	v_mfma_f32_16x16x32_bf16 v[52:55], v[140:143], v[168:171], v[52:55]
	s_waitcnt lgkmcnt(4)
	v_mfma_f32_16x16x32_bf16 v[52:55], v[144:147], v[172:175], v[52:55]
	v_mfma_f32_16x16x32_bf16 v[48:51], v[148:151], v[168:171], v[48:51]
	s_nop 0
	v_mfma_f32_16x16x32_bf16 v[48:51], v[152:155], v[172:175], v[48:51]
	s_waitcnt lgkmcnt(3)
	v_mfma_f32_16x16x32_bf16 v[44:47], v[140:143], v[176:179], v[44:47]
	s_waitcnt lgkmcnt(2)
	v_mfma_f32_16x16x32_bf16 v[44:47], v[144:147], v[180:183], v[44:47]
	v_mfma_f32_16x16x32_bf16 v[40:43], v[148:151], v[176:179], v[40:43]
	s_nop 0
	v_mfma_f32_16x16x32_bf16 v[40:43], v[152:155], v[180:183], v[40:43]
	s_waitcnt lgkmcnt(1)
	v_mfma_f32_16x16x32_bf16 v[36:39], v[140:143], v[184:187], v[36:39]
	s_waitcnt lgkmcnt(0)
	v_mfma_f32_16x16x32_bf16 v[36:39], v[144:147], v[188:191], v[36:39]
	v_mfma_f32_16x16x32_bf16 v[32:35], v[148:151], v[184:187], v[32:35]
	s_nop 0
	v_mfma_f32_16x16x32_bf16 v[32:35], v[152:155], v[188:191], v[32:35]
	s_setprio 0
	s_setprio 1
	v_mfma_f32_16x16x32_bf16 v[28:31], v[156:159], v[160:163], v[28:31]
	s_nop 0
	v_mfma_f32_16x16x32_bf16 v[28:31], v[136:139], v[164:167], v[28:31]
	v_mfma_f32_16x16x32_bf16 v[24:27], v[132:135], v[160:163], v[24:27]
	s_nop 0
	v_mfma_f32_16x16x32_bf16 v[24:27], v[128:131], v[164:167], v[24:27]
	v_mfma_f32_16x16x32_bf16 v[20:23], v[156:159], v[168:171], v[20:23]
	s_nop 0
	v_mfma_f32_16x16x32_bf16 v[20:23], v[136:139], v[172:175], v[20:23]
	v_mfma_f32_16x16x32_bf16 v[16:19], v[132:135], v[168:171], v[16:19]
	s_nop 0
	v_mfma_f32_16x16x32_bf16 v[16:19], v[128:131], v[172:175], v[16:19]
	v_mfma_f32_16x16x32_bf16 v[12:15], v[156:159], v[176:179], v[12:15]
	s_nop 0
	v_mfma_f32_16x16x32_bf16 v[12:15], v[136:139], v[180:183], v[12:15]
	v_mfma_f32_16x16x32_bf16 v[8:11], v[132:135], v[176:179], v[8:11]
	s_nop 0
	v_mfma_f32_16x16x32_bf16 v[8:11], v[128:131], v[180:183], v[8:11]
	v_mfma_f32_16x16x32_bf16 v[4:7], v[156:159], v[184:187], v[4:7]
	s_nop 0
	v_mfma_f32_16x16x32_bf16 v[4:7], v[136:139], v[188:191], v[4:7]
	v_mfma_f32_16x16x32_bf16 v[0:3], v[132:135], v[184:187], v[0:3]
	s_nop 0
	v_mfma_f32_16x16x32_bf16 v[0:3], v[128:131], v[188:191], v[0:3]
	s_setprio 0
	s_barrier
	s_add_i32 s43, s43, 2
	s_addk_i32 s33, 0x100
	s_addk_i32 s42, 0x100
	s_cmp_gt_u32 s43, 5
	s_cbranch_scc0 .LBB0_254
	s_and_b64 vcc, exec, s[14:15]
	s_cbranch_vccz .LBB0_257
	s_barrier

.LBB0_344:
	s_waitcnt lgkmcnt(0)
	s_add_i32 s4, s60, 0x180
	s_add_i32 s5, s36, 0x180
	s_barrier
	s_setprio 1
	s_waitcnt lgkmcnt(7)
	v_mfma_f32_16x16x32_bf16 v[60:63], v[164:167], v[196:199], 0
	s_waitcnt lgkmcnt(6)
	v_mfma_f32_16x16x32_bf16 v[60:63], v[160:163], v[192:195], v[60:63]
	v_mfma_f32_16x16x32_bf16 v[56:59], v[156:159], v[196:199], 0
	s_nop 0
	v_mfma_f32_16x16x32_bf16 v[56:59], v[152:155], v[192:195], v[56:59]
	s_waitcnt lgkmcnt(5)
	v_mfma_f32_16x16x32_bf16 v[52:55], v[164:167], v[188:191], 0
	s_waitcnt lgkmcnt(4)
	v_mfma_f32_16x16x32_bf16 v[52:55], v[160:163], v[184:187], v[52:55]
	v_mfma_f32_16x16x32_bf16 v[48:51], v[156:159], v[188:191], 0
	s_nop 0
	v_mfma_f32_16x16x32_bf16 v[48:51], v[152:155], v[184:187], v[48:51]
	s_waitcnt lgkmcnt(3)
	v_mfma_f32_16x16x32_bf16 v[44:47], v[164:167], v[180:183], 0
	s_waitcnt lgkmcnt(2)
	v_mfma_f32_16x16x32_bf16 v[44:47], v[160:163], v[176:179], v[44:47]
	v_mfma_f32_16x16x32_bf16 v[40:43], v[156:159], v[180:183], 0
	s_nop 0
	v_mfma_f32_16x16x32_bf16 v[40:43], v[152:155], v[176:179], v[40:43]
	s_waitcnt lgkmcnt(1)
	v_mfma_f32_16x16x32_bf16 v[36:39], v[164:167], v[172:175], 0
	s_waitcnt lgkmcnt(0)
	v_mfma_f32_16x16x32_bf16 v[36:39], v[160:163], v[168:171], v[36:39]
	v_mfma_f32_16x16x32_bf16 v[32:35], v[156:159], v[172:175], 0
	s_nop 0
	v_mfma_f32_16x16x32_bf16 v[32:35], v[152:155], v[168:171], v[32:35]
	s_setprio 0
	s_setprio 1
	v_mfma_f32_16x16x32_bf16 v[28:31], v[148:151], v[196:199], 0
	s_nop 0
	v_mfma_f32_16x16x32_bf16 v[28:31], v[144:147], v[192:195], v[28:31]
	v_mfma_f32_16x16x32_bf16 v[24:27], v[140:143], v[196:199], 0
	s_nop 0
	v_mfma_f32_16x16x32_bf16 v[24:27], v[136:139], v[192:195], v[24:27]
	v_mfma_f32_16x16x32_bf16 v[20:23], v[148:151], v[188:191], 0
	s_nop 0
	v_mfma_f32_16x16x32_bf16 v[20:23], v[144:147], v[184:187], v[20:23]
	v_mfma_f32_16x16x32_bf16 v[16:19], v[140:143], v[188:191], 0
	s_nop 0
	v_mfma_f32_16x16x32_bf16 v[16:19], v[136:139], v[184:187], v[16:19]
	v_mfma_f32_16x16x32_bf16 v[12:15], v[148:151], v[180:183], 0
	s_nop 0
	v_mfma_f32_16x16x32_bf16 v[12:15], v[144:147], v[176:179], v[12:15]
	v_mfma_f32_16x16x32_bf16 v[8:11], v[140:143], v[180:183], 0
	s_nop 0
	v_mfma_f32_16x16x32_bf16 v[8:11], v[136:139], v[176:179], v[8:11]
	v_mfma_f32_16x16x32_bf16 v[4:7], v[148:151], v[172:175], 0
	s_nop 0
	v_mfma_f32_16x16x32_bf16 v[4:7], v[144:147], v[168:171], v[4:7]
	v_mfma_f32_16x16x32_bf16 v[0:3], v[140:143], v[172:175], 0
	s_nop 0
	v_mfma_f32_16x16x32_bf16 v[0:3], v[136:139], v[168:171], v[0:3]
	s_setprio 0
	s_barrier
	ds_read_b128 v[164:167], v225
	ds_read_b128 v[160:163], v226
	ds_read_b128 v[156:159], v227
	ds_read_b128 v[152:155], v228
	ds_read_b128 v[148:151], v229
	ds_read_b128 v[144:147], v230
	ds_read_b128 v[140:143], v231
	ds_read_b128 v[136:139], v232
	s_mov_b32 m0, s72
	s_add_i32 s14, s60, 0x100100
	buffer_load_dwordx4 v214, s[8:11], s14 offen lds
	s_add_i32 s14, s60, 0x180100
	s_mov_b32 m0, s73
	s_nop 0
	buffer_load_dwordx4 v214, s[8:11], s14 offen lds
	ds_read_b128 v[168:171], v233 offset:32768
	ds_read_b128 v[172:175], v233 offset:33792
	ds_read_b128 v[176:179], v233 offset:34816
	ds_read_b128 v[180:183], v233 offset:35840
	ds_read_b128 v[184:187], v233 offset:36864
	ds_read_b128 v[188:191], v233 offset:37888
	ds_read_b128 v[192:195], v233 offset:38912
	ds_read_b128 v[196:199], v233 offset:39936
	s_waitcnt vmcnt(10)
	s_waitcnt lgkmcnt(4)
	s_barrier
	s_setprio 1
	s_waitcnt lgkmcnt(7)
	v_mfma_f32_16x16x32_bf16 v[124:127], v[164:167], v[168:171], v[124:127]
	s_waitcnt lgkmcnt(6)
	v_mfma_f32_16x16x32_bf16 v[124:127], v[160:163], v[172:175], v[124:127]
	v_mfma_f32_16x16x32_bf16 v[120:123], v[156:159], v[168:171], v[120:123]
	s_nop 0
	v_mfma_f32_16x16x32_bf16 v[120:123], v[152:155], v[172:175], v[120:123]
	s_waitcnt lgkmcnt(5)
	v_mfma_f32_16x16x32_bf16 v[116:119], v[164:167], v[176:179], v[116:119]
	s_waitcnt lgkmcnt(4)
	v_mfma_f32_16x16x32_bf16 v[116:119], v[160:163], v[180:183], v[116:119]
	v_mfma_f32_16x16x32_bf16 v[112:115], v[156:159], v[176:179], v[112:115]
	s_nop 0
	v_mfma_f32_16x16x32_bf16 v[112:115], v[152:155], v[180:183], v[112:115]
	s_waitcnt lgkmcnt(3)
	v_mfma_f32_16x16x32_bf16 v[108:111], v[164:167], v[184:187], v[108:111]
	s_waitcnt lgkmcnt(2)
	v_mfma_f32_16x16x32_bf16 v[108:111], v[160:163], v[188:191], v[108:111]
	v_mfma_f32_16x16x32_bf16 v[104:107], v[156:159], v[184:187], v[104:107]
	s_nop 0
	v_mfma_f32_16x16x32_bf16 v[104:107], v[152:155], v[188:191], v[104:107]
	s_waitcnt lgkmcnt(1)
	v_mfma_f32_16x16x32_bf16 v[100:103], v[164:167], v[192:195], v[100:103]
	s_waitcnt lgkmcnt(0)
	v_mfma_f32_16x16x32_bf16 v[100:103], v[160:163], v[196:199], v[100:103]
	v_mfma_f32_16x16x32_bf16 v[96:99], v[156:159], v[192:195], v[96:99]
	s_nop 0
	v_mfma_f32_16x16x32_bf16 v[96:99], v[152:155], v[196:199], v[96:99]
	s_setprio 0
	s_setprio 1
	v_mfma_f32_16x16x32_bf16 v[92:95], v[148:151], v[168:171], v[92:95]
	s_nop 0
	v_mfma_f32_16x16x32_bf16 v[92:95], v[144:147], v[172:175], v[92:95]
	v_mfma_f32_16x16x32_bf16 v[88:91], v[140:143], v[168:171], v[88:91]
	s_nop 0
	v_mfma_f32_16x16x32_bf16 v[88:91], v[136:139], v[172:175], v[88:91]
	v_mfma_f32_16x16x32_bf16 v[84:87], v[148:151], v[176:179], v[84:87]
	s_nop 0
	v_mfma_f32_16x16x32_bf16 v[84:87], v[144:147], v[180:183], v[84:87]
	v_mfma_f32_16x16x32_bf16 v[80:83], v[140:143], v[176:179], v[80:83]
	s_nop 0
	v_mfma_f32_16x16x32_bf16 v[80:83], v[136:139], v[180:183], v[80:83]
	v_mfma_f32_16x16x32_bf16 v[76:79], v[148:151], v[184:187], v[76:79]
	s_nop 0
	v_mfma_f32_16x16x32_bf16 v[76:79], v[144:147], v[188:191], v[76:79]
	v_mfma_f32_16x16x32_bf16 v[72:75], v[140:143], v[184:187], v[72:75]
	s_nop 0
	v_mfma_f32_16x16x32_bf16 v[72:75], v[136:139], v[188:191], v[72:75]
	v_mfma_f32_16x16x32_bf16 v[68:71], v[148:151], v[192:195], v[68:71]
	s_nop 0
	v_mfma_f32_16x16x32_bf16 v[68:71], v[144:147], v[196:199], v[68:71]
	v_mfma_f32_16x16x32_bf16 v[64:67], v[140:143], v[192:195], v[64:67]
	s_nop 0
	v_mfma_f32_16x16x32_bf16 v[64:67], v[136:139], v[196:199], v[64:67]
	s_setprio 0
	s_barrier
	s_mov_b32 m0, s76
	s_mov_b32 s14, s10
	s_mov_b32 s15, s11
	buffer_load_dwordx4 v215, s[12:15], s5 offen lds
	s_add_i32 s5, s36, 0x100180
	s_mov_b32 m0, s77
	s_nop 0
	buffer_load_dwordx4 v215, s[12:15], s5 offen lds
	s_add_i32 s5, s36, 0x10180
	s_mov_b32 m0, s80
	s_nop 0
	buffer_load_dwordx4 v215, s[12:15], s5 offen lds
	s_add_i32 s5, s36, 0x110180
	s_mov_b32 m0, s81
	s_nop 0
	buffer_load_dwordx4 v215, s[12:15], s5 offen lds
	s_mov_b32 m0, s78
	s_nop 0
	buffer_load_dwordx4 v214, s[8:11], s4 offen lds
	s_add_i32 s4, s60, 0x80180
	s_mov_b32 m0, s79
	s_nop 0
	buffer_load_dwordx4 v214, s[8:11], s4 offen lds
	ds_read_b128 v[168:171], v233 offset:49152
	ds_read_b128 v[172:175], v233 offset:50176
	ds_read_b128 v[176:179], v233 offset:51200
	ds_read_b128 v[180:183], v233 offset:52224
	ds_read_b128 v[184:187], v233 offset:53248
	ds_read_b128 v[188:191], v233 offset:54272
	ds_read_b128 v[192:195], v233 offset:55296
	ds_read_b128 v[196:199], v233 offset:56320
	s_waitcnt vmcnt(8)
	s_waitcnt lgkmcnt(0)
	s_barrier
	s_setprio 1
	s_waitcnt lgkmcnt(7)
	v_mfma_f32_16x16x32_bf16 v[60:63], v[164:167], v[168:171], v[60:63]
	s_waitcnt lgkmcnt(6)
	v_mfma_f32_16x16x32_bf16 v[60:63], v[160:163], v[172:175], v[60:63]
	v_mfma_f32_16x16x32_bf16 v[56:59], v[156:159], v[168:171], v[56:59]
	s_nop 0
	v_mfma_f32_16x16x32_bf16 v[56:59], v[152:155], v[172:175], v[56:59]
	s_waitcnt lgkmcnt(5)
	v_mfma_f32_16x16x32_bf16 v[52:55], v[164:167], v[176:179], v[52:55]
	s_waitcnt lgkmcnt(4)
	v_mfma_f32_16x16x32_bf16 v[52:55], v[160:163], v[180:183], v[52:55]
	v_mfma_f32_16x16x32_bf16 v[48:51], v[156:159], v[176:179], v[48:51]
	s_nop 0
	v_mfma_f32_16x16x32_bf16 v[48:51], v[152:155], v[180:183], v[48:51]
	s_waitcnt lgkmcnt(3)
	v_mfma_f32_16x16x32_bf16 v[44:47], v[164:167], v[184:187], v[44:47]
	s_waitcnt lgkmcnt(2)
	v_mfma_f32_16x16x32_bf16 v[44:47], v[160:163], v[188:191], v[44:47]
	v_mfma_f32_16x16x32_bf16 v[40:43], v[156:159], v[184:187], v[40:43]
	s_nop 0
	v_mfma_f32_16x16x32_bf16 v[40:43], v[152:155], v[188:191], v[40:43]
	s_waitcnt lgkmcnt(1)
	v_mfma_f32_16x16x32_bf16 v[36:39], v[164:167], v[192:195], v[36:39]
	s_waitcnt lgkmcnt(0)
	v_mfma_f32_16x16x32_bf16 v[36:39], v[160:163], v[196:199], v[36:39]
	v_mfma_f32_16x16x32_bf16 v[32:35], v[156:159], v[192:195], v[32:35]
	s_nop 0
	v_mfma_f32_16x16x32_bf16 v[32:35], v[152:155], v[196:199], v[32:35]
	s_setprio 0
	s_setprio 1
	v_mfma_f32_16x16x32_bf16 v[28:31], v[148:151], v[168:171], v[28:31]
	s_nop 0
	v_mfma_f32_16x16x32_bf16 v[28:31], v[144:147], v[172:175], v[28:31]
	v_mfma_f32_16x16x32_bf16 v[24:27], v[140:143], v[168:171], v[24:27]
	s_nop 0
	v_mfma_f32_16x16x32_bf16 v[24:27], v[136:139], v[172:175], v[24:27]
	v_mfma_f32_16x16x32_bf16 v[20:23], v[148:151], v[176:179], v[20:23]
	s_nop 0
	v_mfma_f32_16x16x32_bf16 v[20:23], v[144:147], v[180:183], v[20:23]
	v_mfma_f32_16x16x32_bf16 v[16:19], v[140:143], v[176:179], v[16:19]
	s_nop 0
	v_mfma_f32_16x16x32_bf16 v[16:19], v[136:139], v[180:183], v[16:19]
	v_mfma_f32_16x16x32_bf16 v[12:15], v[148:151], v[184:187], v[12:15]
	s_nop 0
	v_mfma_f32_16x16x32_bf16 v[12:15], v[144:147], v[188:191], v[12:15]
	v_mfma_f32_16x16x32_bf16 v[8:11], v[140:143], v[184:187], v[8:11]
	s_nop 0
	v_mfma_f32_16x16x32_bf16 v[8:11], v[136:139], v[188:191], v[8:11]
	v_mfma_f32_16x16x32_bf16 v[4:7], v[148:151], v[192:195], v[4:7]
	s_nop 0
	v_mfma_f32_16x16x32_bf16 v[4:7], v[144:147], v[196:199], v[4:7]
	v_mfma_f32_16x16x32_bf16 v[0:3], v[140:143], v[192:195], v[0:3]
	s_nop 0
	v_mfma_f32_16x16x32_bf16 v[0:3], v[136:139], v[196:199], v[0:3]
	s_setprio 0
	s_barrier
	s_waitcnt vmcnt(14)
	v_mul_f32_e32 v132, 0x42800000, v132
	v_mul_f32_e32 v128, 0x42800000, v128
	v_mul_f32_e32 v133, 0x42800000, v133
	v_mul_f32_e32 v129, 0x42800000, v129
	v_mul_f32_e32 v134, 0x42800000, v134
	v_mul_f32_e32 v130, 0x42800000, v130
	v_mul_f32_e32 v135, 0x42800000, v135
	v_mul_f32_e32 v131, 0x42800000, v131
	v_cvt_pk_fp8_f32 v204, v128, v132
	v_cvt_pk_fp8_f32 v234, v129, v133
	v_cvt_pk_fp8_f32 v235, v130, v134
	v_cvt_pk_fp8_f32 v236, v131, v135
	s_add_i32 s33, s36, 0x200
	s_mov_b32 s61, 0
	s_mov_b32 s66, s75
	s_mov_b32 s94, s86
	s_branch .LBB0_347

.LBB0_347:
	v_mov_b32_e32 v152, v204
	v_mov_b32_e32 v153, v234
	v_mov_b32_e32 v154, v235
	v_mov_b32_e32 v155, v236
	ds_read_b128 v[158:161], v217
	ds_read_b128 v[162:165], v218
	ds_read_b128 v[166:169], v219
	ds_read_b128 v[170:173], v220
	ds_read_b128 v[148:151], v221
	ds_read_b128 v[144:147], v222
	ds_read_b128 v[140:143], v223
	ds_read_b128 v[136:139], v224
	s_add_i32 s4, s60, s61
	s_mov_b32 s46, s94
	s_add_i32 s94, s94, 1
	s_add_i32 s5, s4, 0x200
	s_add_i32 s16, s33, s61
	s_cmpk_eq_i32 s61, 0x1e00
	s_cselect_b32 s47, s90, s5
	s_cselect_b32 s97, s91, s16
	s_add_i32 s96, s47, 0x80
	s_mov_b32 m0, s82
	s_add_i32 s5, s4, 0x100180
	buffer_load_dwordx4 v214, s[8:11], s5 offen lds
	s_add_i32 s4, s4, 0x180180
	s_mov_b32 m0, s85
	s_add_i32 vcc_lo, s97, 0x80
	buffer_load_dwordx4 v214, s[8:11], s4 offen lds
	s_lshr_b32 s4, s94, 2
	s_mul_i32 s5, s4, s34
	s_add_i32 s16, s5, s2
	s_cmp_lt_i32 s4, s3
	s_cselect_b64 s[4:5], -1, 0
	s_and_b64 s[44:45], s[4:5], exec
	s_cselect_b32 s16, s16, 0
	s_bfe_u32 s17, s94, 0x10001
	s_or_b32 s17, s17, s83
	s_bfe_u32 s67, s16, 0x50007
	s_bfe_u32 s36, s16, 0x50002
	s_and_b32 s95, s16, 3
	s_cmpk_gt_i32 s16, 0xfff
	s_cselect_b64 s[44:45], -1, 0
	v_lshl_or_b32 v156, s17, 3, v216
	s_and_b64 s[16:17], s[44:45], exec
	s_cselect_b32 s16, s25, s21
	s_cselect_b32 s17, s24, s20
	s_lshl_b32 vcc_hi, s67, 23
	s_add_u32 s17, s17, vcc_hi
	s_addc_u32 s16, s16, 0
	s_lshl_b32 vcc_hi, s36, 18
	s_add_u32 s17, s17, vcc_hi
	s_addc_u32 vcc_hi, s16, 0
	s_lshl_b32 s16, s95, 9
	s_add_u32 s16, s17, s16
	v_and_or_b32 v204, s66, 2, v200
	s_addc_u32 s17, vcc_hi, 0
	v_lshlrev_b64 v[128:129], 11, v[204:205]
	v_lshl_add_u64 v[128:129], s[16:17], 0, v[128:129]
	v_lshlrev_b32_e32 v204, 4, v156
	v_lshl_add_u64 v[132:133], v[128:129], 0, v[204:205]
	global_load_dwordx4 v[128:131], v[132:133], off nt
	s_nop 0
	global_load_dwordx4 v[132:135], v[132:133], off offset:2048 nt
	ds_read_b128 v[174:177], v233
	ds_read_b128 v[178:181], v233 offset:1024
	ds_read_b128 v[182:185], v233 offset:2048
	ds_read_b128 v[186:189], v233 offset:3072
	ds_read_b128 v[190:193], v233 offset:4096
	ds_read_b128 v[194:197], v233 offset:5120
	ds_read_b128 v[234:237], v233 offset:6144
	ds_read_b128 v[238:241], v233 offset:7168
	s_waitcnt vmcnt(10)
	s_waitcnt lgkmcnt(4)
	s_barrier
	s_setprio 1
	s_waitcnt lgkmcnt(7)
	v_mfma_f32_16x16x32_bf16 v[124:127], v[158:161], v[174:177], v[124:127]
	s_waitcnt lgkmcnt(6)
	v_mfma_f32_16x16x32_bf16 v[124:127], v[162:165], v[178:181], v[124:127]
	v_mfma_f32_16x16x32_bf16 v[120:123], v[166:169], v[174:177], v[120:123]
	s_nop 0
	v_mfma_f32_16x16x32_bf16 v[120:123], v[170:173], v[178:181], v[120:123]
	s_waitcnt lgkmcnt(5)
	v_mfma_f32_16x16x32_bf16 v[116:119], v[158:161], v[182:185], v[116:119]
	s_waitcnt lgkmcnt(4)
	v_mfma_f32_16x16x32_bf16 v[116:119], v[162:165], v[186:189], v[116:119]
	v_mfma_f32_16x16x32_bf16 v[112:115], v[166:169], v[182:185], v[112:115]
	s_nop 0
	v_mfma_f32_16x16x32_bf16 v[112:115], v[170:173], v[186:189], v[112:115]
	s_waitcnt lgkmcnt(3)
	v_mfma_f32_16x16x32_bf16 v[108:111], v[158:161], v[190:193], v[108:111]
	s_waitcnt lgkmcnt(2)
	v_mfma_f32_16x16x32_bf16 v[108:111], v[162:165], v[194:197], v[108:111]
	v_mfma_f32_16x16x32_bf16 v[104:107], v[166:169], v[190:193], v[104:107]
	s_nop 0
	v_mfma_f32_16x16x32_bf16 v[104:107], v[170:173], v[194:197], v[104:107]
	s_waitcnt lgkmcnt(1)
	v_mfma_f32_16x16x32_bf16 v[100:103], v[158:161], v[234:237], v[100:103]
	s_waitcnt lgkmcnt(0)
	v_mfma_f32_16x16x32_bf16 v[100:103], v[162:165], v[238:241], v[100:103]
	v_mfma_f32_16x16x32_bf16 v[96:99], v[166:169], v[234:237], v[96:99]
	s_nop 0
	v_mfma_f32_16x16x32_bf16 v[96:99], v[170:173], v[238:241], v[96:99]
	s_setprio 0
	s_setprio 1
	v_mfma_f32_16x16x32_bf16 v[92:95], v[148:151], v[174:177], v[92:95]
	s_nop 0
	v_mfma_f32_16x16x32_bf16 v[92:95], v[144:147], v[178:181], v[92:95]
	v_mfma_f32_16x16x32_bf16 v[88:91], v[140:143], v[174:177], v[88:91]
	s_nop 0
	v_mfma_f32_16x16x32_bf16 v[88:91], v[136:139], v[178:181], v[88:91]
	v_mfma_f32_16x16x32_bf16 v[84:87], v[148:151], v[182:185], v[84:87]
	s_nop 0
	v_mfma_f32_16x16x32_bf16 v[84:87], v[144:147], v[186:189], v[84:87]
	v_mfma_f32_16x16x32_bf16 v[80:83], v[140:143], v[182:185], v[80:83]
	s_nop 0
	v_mfma_f32_16x16x32_bf16 v[80:83], v[136:139], v[186:189], v[80:83]
	v_mfma_f32_16x16x32_bf16 v[76:79], v[148:151], v[190:193], v[76:79]
	s_nop 0
	v_mfma_f32_16x16x32_bf16 v[76:79], v[144:147], v[194:197], v[76:79]
	v_mfma_f32_16x16x32_bf16 v[72:75], v[140:143], v[190:193], v[72:75]
	s_nop 0
	v_mfma_f32_16x16x32_bf16 v[72:75], v[136:139], v[194:197], v[72:75]
	v_mfma_f32_16x16x32_bf16 v[68:71], v[148:151], v[234:237], v[68:71]
	s_nop 0
	v_mfma_f32_16x16x32_bf16 v[68:71], v[144:147], v[238:241], v[68:71]
	v_mfma_f32_16x16x32_bf16 v[64:67], v[140:143], v[234:237], v[64:67]
	s_nop 0
	v_mfma_f32_16x16x32_bf16 v[64:67], v[136:139], v[238:241], v[64:67]
	s_setprio 0
	s_barrier
	s_mov_b32 m0, s65
	s_add_i32 s16, s97, 0x100000
	buffer_load_dwordx4 v215, s[12:15], s97 offen lds
	s_mov_b32 m0, s68
	s_nop 0
	buffer_load_dwordx4 v215, s[12:15], s16 offen lds
	s_add_i32 s16, s97, 0x10000
	s_mov_b32 m0, s69
	s_nop 0
	buffer_load_dwordx4 v215, s[12:15], s16 offen lds
	s_add_i32 s16, s97, 0x110000
	s_mov_b32 m0, s70
	s_nop 0
	buffer_load_dwordx4 v215, s[12:15], s16 offen lds
	s_mov_b32 m0, s64
	s_add_i32 s16, s47, 0x80000
	buffer_load_dwordx4 v214, s[8:11], s47 offen lds
	s_mov_b32 m0, s71
	s_nop 0
	buffer_load_dwordx4 v214, s[8:11], s16 offen lds
	ds_read_b128 v[174:177], v233 offset:16384
	ds_read_b128 v[178:181], v233 offset:17408
	ds_read_b128 v[182:185], v233 offset:18432
	ds_read_b128 v[186:189], v233 offset:19456
	ds_read_b128 v[190:193], v233 offset:20480
	ds_read_b128 v[194:197], v233 offset:21504
	ds_read_b128 v[234:237], v233 offset:22528
	ds_read_b128 v[238:241], v233 offset:23552
	s_waitcnt vmcnt(10)
	s_waitcnt lgkmcnt(0)
	s_barrier
	s_setprio 1
	s_waitcnt lgkmcnt(7)
	v_mfma_f32_16x16x32_bf16 v[60:63], v[158:161], v[174:177], v[60:63]
	s_waitcnt lgkmcnt(6)
	v_mfma_f32_16x16x32_bf16 v[60:63], v[162:165], v[178:181], v[60:63]
	v_mfma_f32_16x16x32_bf16 v[56:59], v[166:169], v[174:177], v[56:59]
	s_nop 0
	v_mfma_f32_16x16x32_bf16 v[56:59], v[170:173], v[178:181], v[56:59]
	s_waitcnt lgkmcnt(5)
	v_mfma_f32_16x16x32_bf16 v[52:55], v[158:161], v[182:185], v[52:55]
	s_waitcnt lgkmcnt(4)
	v_mfma_f32_16x16x32_bf16 v[52:55], v[162:165], v[186:189], v[52:55]
	v_mfma_f32_16x16x32_bf16 v[48:51], v[166:169], v[182:185], v[48:51]
	s_nop 0
	v_mfma_f32_16x16x32_bf16 v[48:51], v[170:173], v[186:189], v[48:51]
	s_waitcnt lgkmcnt(3)
	v_mfma_f32_16x16x32_bf16 v[44:47], v[158:161], v[190:193], v[44:47]
	s_waitcnt lgkmcnt(2)
	v_mfma_f32_16x16x32_bf16 v[44:47], v[162:165], v[194:197], v[44:47]
	v_mfma_f32_16x16x32_bf16 v[40:43], v[166:169], v[190:193], v[40:43]
	s_nop 0
	v_mfma_f32_16x16x32_bf16 v[40:43], v[170:173], v[194:197], v[40:43]
	s_waitcnt lgkmcnt(1)
	v_mfma_f32_16x16x32_bf16 v[36:39], v[158:161], v[234:237], v[36:39]
	s_waitcnt lgkmcnt(0)
	v_mfma_f32_16x16x32_bf16 v[36:39], v[162:165], v[238:241], v[36:39]
	v_mfma_f32_16x16x32_bf16 v[32:35], v[166:169], v[234:237], v[32:35]
	s_nop 0
	v_mfma_f32_16x16x32_bf16 v[32:35], v[170:173], v[238:241], v[32:35]
	s_setprio 0
	s_setprio 1
	v_mfma_f32_16x16x32_bf16 v[28:31], v[148:151], v[174:177], v[28:31]
	s_nop 0
	v_mfma_f32_16x16x32_bf16 v[28:31], v[144:147], v[178:181], v[28:31]
	v_mfma_f32_16x16x32_bf16 v[24:27], v[140:143], v[174:177], v[24:27]
	s_nop 0
	v_mfma_f32_16x16x32_bf16 v[24:27], v[136:139], v[178:181], v[24:27]
	v_mfma_f32_16x16x32_bf16 v[20:23], v[148:151], v[182:185], v[20:23]
	s_nop 0
	v_mfma_f32_16x16x32_bf16 v[20:23], v[144:147], v[186:189], v[20:23]
	v_mfma_f32_16x16x32_bf16 v[16:19], v[140:143], v[182:185], v[16:19]
	s_nop 0
	v_mfma_f32_16x16x32_bf16 v[16:19], v[136:139], v[186:189], v[16:19]
	v_mfma_f32_16x16x32_bf16 v[12:15], v[148:151], v[190:193], v[12:15]
	s_nop 0
	v_mfma_f32_16x16x32_bf16 v[12:15], v[144:147], v[194:197], v[12:15]
	v_mfma_f32_16x16x32_bf16 v[8:11], v[140:143], v[190:193], v[8:11]
	s_nop 0
	v_mfma_f32_16x16x32_bf16 v[8:11], v[136:139], v[194:197], v[8:11]
	v_mfma_f32_16x16x32_bf16 v[4:7], v[148:151], v[234:237], v[4:7]
	s_nop 0
	v_mfma_f32_16x16x32_bf16 v[4:7], v[144:147], v[238:241], v[4:7]
	v_mfma_f32_16x16x32_bf16 v[0:3], v[140:143], v[234:237], v[0:3]
	s_nop 0
	v_mfma_f32_16x16x32_bf16 v[0:3], v[136:139], v[238:241], v[0:3]
	s_setprio 0
	s_barrier
	ds_read_b128 v[136:139], v225
	ds_read_b128 v[140:143], v226
	ds_read_b128 v[144:147], v227
	ds_read_b128 v[148:151], v228
	ds_read_b128 v[158:161], v229
	ds_read_b128 v[162:165], v230
	ds_read_b128 v[166:169], v231
	ds_read_b128 v[170:173], v232
	s_mov_b32 m0, s72
	s_add_i32 s16, s47, 0x100000
	buffer_load_dwordx4 v214, s[8:11], s16 offen lds
	s_add_i32 s16, s47, 0x180000
	s_mov_b32 m0, s73
	s_nop 0
	buffer_load_dwordx4 v214, s[8:11], s16 offen lds
	ds_read_b128 v[174:177], v233 offset:32768
	ds_read_b128 v[178:181], v233 offset:33792
	ds_read_b128 v[182:185], v233 offset:34816
	ds_read_b128 v[186:189], v233 offset:35840
	ds_read_b128 v[190:193], v233 offset:36864
	ds_read_b128 v[194:197], v233 offset:37888
	ds_read_b128 v[234:237], v233 offset:38912
	ds_read_b128 v[238:241], v233 offset:39936
	s_waitcnt vmcnt(10)
	s_waitcnt lgkmcnt(4)
	s_barrier
	s_setprio 1
	s_waitcnt lgkmcnt(7)
	v_mfma_f32_16x16x32_bf16 v[124:127], v[136:139], v[174:177], v[124:127]
	s_waitcnt lgkmcnt(6)
	v_mfma_f32_16x16x32_bf16 v[124:127], v[140:143], v[178:181], v[124:127]
	v_mfma_f32_16x16x32_bf16 v[120:123], v[144:147], v[174:177], v[120:123]
	s_nop 0
	v_mfma_f32_16x16x32_bf16 v[120:123], v[148:151], v[178:181], v[120:123]
	s_waitcnt lgkmcnt(5)
	v_mfma_f32_16x16x32_bf16 v[116:119], v[136:139], v[182:185], v[116:119]
	s_waitcnt lgkmcnt(4)
	v_mfma_f32_16x16x32_bf16 v[116:119], v[140:143], v[186:189], v[116:119]
	v_mfma_f32_16x16x32_bf16 v[112:115], v[144:147], v[182:185], v[112:115]
	s_nop 0
	v_mfma_f32_16x16x32_bf16 v[112:115], v[148:151], v[186:189], v[112:115]
	s_waitcnt lgkmcnt(3)
	v_mfma_f32_16x16x32_bf16 v[108:111], v[136:139], v[190:193], v[108:111]
	s_waitcnt lgkmcnt(2)
	v_mfma_f32_16x16x32_bf16 v[108:111], v[140:143], v[194:197], v[108:111]
	v_mfma_f32_16x16x32_bf16 v[104:107], v[144:147], v[190:193], v[104:107]
	s_nop 0
	v_mfma_f32_16x16x32_bf16 v[104:107], v[148:151], v[194:197], v[104:107]
	s_waitcnt lgkmcnt(1)
	v_mfma_f32_16x16x32_bf16 v[100:103], v[136:139], v[234:237], v[100:103]
	s_waitcnt lgkmcnt(0)
	v_mfma_f32_16x16x32_bf16 v[100:103], v[140:143], v[238:241], v[100:103]
	v_mfma_f32_16x16x32_bf16 v[96:99], v[144:147], v[234:237], v[96:99]
	s_nop 0
	v_mfma_f32_16x16x32_bf16 v[96:99], v[148:151], v[238:241], v[96:99]
	s_setprio 0
	s_setprio 1
	v_mfma_f32_16x16x32_bf16 v[92:95], v[158:161], v[174:177], v[92:95]
	s_nop 0
	v_mfma_f32_16x16x32_bf16 v[92:95], v[162:165], v[178:181], v[92:95]
	v_mfma_f32_16x16x32_bf16 v[88:91], v[166:169], v[174:177], v[88:91]
	s_nop 0
	v_mfma_f32_16x16x32_bf16 v[88:91], v[170:173], v[178:181], v[88:91]
	v_mfma_f32_16x16x32_bf16 v[84:87], v[158:161], v[182:185], v[84:87]
	s_nop 0
	v_mfma_f32_16x16x32_bf16 v[84:87], v[162:165], v[186:189], v[84:87]
	v_mfma_f32_16x16x32_bf16 v[80:83], v[166:169], v[182:185], v[80:83]
	s_nop 0
	v_mfma_f32_16x16x32_bf16 v[80:83], v[170:173], v[186:189], v[80:83]
	v_mfma_f32_16x16x32_bf16 v[76:79], v[158:161], v[190:193], v[76:79]
	s_nop 0
	v_mfma_f32_16x16x32_bf16 v[76:79], v[162:165], v[194:197], v[76:79]
	v_mfma_f32_16x16x32_bf16 v[72:75], v[166:169], v[190:193], v[72:75]
	s_nop 0
	v_mfma_f32_16x16x32_bf16 v[72:75], v[170:173], v[194:197], v[72:75]
	v_mfma_f32_16x16x32_bf16 v[68:71], v[158:161], v[234:237], v[68:71]
	s_nop 0
	v_mfma_f32_16x16x32_bf16 v[68:71], v[162:165], v[238:241], v[68:71]
	v_mfma_f32_16x16x32_bf16 v[64:67], v[166:169], v[234:237], v[64:67]
	s_nop 0
	v_mfma_f32_16x16x32_bf16 v[64:67], v[170:173], v[238:241], v[64:67]
	s_setprio 0
	s_barrier
	s_mov_b32 m0, s76
	s_add_i32 s16, s97, 0x100080
	buffer_load_dwordx4 v215, s[12:15], vcc_lo offen lds
	s_mov_b32 m0, s77
	s_add_i32 s47, s47, 0x80080
	buffer_load_dwordx4 v215, s[12:15], s16 offen lds
	s_add_i32 s16, s97, 0x10080
	s_mov_b32 m0, s80
	s_add_i32 s97, s97, 0x110080
	buffer_load_dwordx4 v215, s[12:15], s16 offen lds
	s_mov_b32 m0, s81
	s_nop 0
	buffer_load_dwordx4 v215, s[12:15], s97 offen lds
	s_mov_b32 m0, s78
	s_nop 0
	buffer_load_dwordx4 v214, s[8:11], s96 offen lds
	s_mov_b32 m0, s79
	s_nop 0
	buffer_load_dwordx4 v214, s[8:11], s47 offen lds
	ds_read_b128 v[174:177], v233 offset:49152
	ds_read_b128 v[178:181], v233 offset:50176
	ds_read_b128 v[182:185], v233 offset:51200
	ds_read_b128 v[186:189], v233 offset:52224
	ds_read_b128 v[190:193], v233 offset:53248
	ds_read_b128 v[194:197], v233 offset:54272
	ds_read_b128 v[234:237], v233 offset:55296
	ds_read_b128 v[238:241], v233 offset:56320
	s_waitcnt vmcnt(8)
	s_waitcnt lgkmcnt(0)
	s_barrier
	s_setprio 1
	s_waitcnt lgkmcnt(7)
	v_mfma_f32_16x16x32_bf16 v[60:63], v[136:139], v[174:177], v[60:63]
	s_waitcnt lgkmcnt(6)
	v_mfma_f32_16x16x32_bf16 v[60:63], v[140:143], v[178:181], v[60:63]
	v_mfma_f32_16x16x32_bf16 v[56:59], v[144:147], v[174:177], v[56:59]
	s_nop 0
	v_mfma_f32_16x16x32_bf16 v[56:59], v[148:151], v[178:181], v[56:59]
	s_waitcnt lgkmcnt(5)
	v_mfma_f32_16x16x32_bf16 v[52:55], v[136:139], v[182:185], v[52:55]
	s_waitcnt lgkmcnt(4)
	v_mfma_f32_16x16x32_bf16 v[52:55], v[140:143], v[186:189], v[52:55]
	v_mfma_f32_16x16x32_bf16 v[48:51], v[144:147], v[182:185], v[48:51]
	s_nop 0
	v_mfma_f32_16x16x32_bf16 v[48:51], v[148:151], v[186:189], v[48:51]
	s_waitcnt lgkmcnt(3)
	v_mfma_f32_16x16x32_bf16 v[44:47], v[136:139], v[190:193], v[44:47]
	s_waitcnt lgkmcnt(2)
	v_mfma_f32_16x16x32_bf16 v[44:47], v[140:143], v[194:197], v[44:47]
	v_mfma_f32_16x16x32_bf16 v[40:43], v[144:147], v[190:193], v[40:43]
	s_nop 0
	v_mfma_f32_16x16x32_bf16 v[40:43], v[148:151], v[194:197], v[40:43]
	s_waitcnt lgkmcnt(1)
	v_mfma_f32_16x16x32_bf16 v[36:39], v[136:139], v[234:237], v[36:39]
	s_waitcnt lgkmcnt(0)
	v_mfma_f32_16x16x32_bf16 v[36:39], v[140:143], v[238:241], v[36:39]
	v_mfma_f32_16x16x32_bf16 v[32:35], v[144:147], v[234:237], v[32:35]
	s_nop 0
	v_mfma_f32_16x16x32_bf16 v[32:35], v[148:151], v[238:241], v[32:35]
	s_setprio 0
	s_setprio 1
	v_mfma_f32_16x16x32_bf16 v[28:31], v[158:161], v[174:177], v[28:31]
	s_nop 0
	v_mfma_f32_16x16x32_bf16 v[28:31], v[162:165], v[178:181], v[28:31]
	v_mfma_f32_16x16x32_bf16 v[24:27], v[166:169], v[174:177], v[24:27]
	s_nop 0
	v_mfma_f32_16x16x32_bf16 v[24:27], v[170:173], v[178:181], v[24:27]
	v_mfma_f32_16x16x32_bf16 v[20:23], v[158:161], v[182:185], v[20:23]
	s_nop 0
	v_mfma_f32_16x16x32_bf16 v[20:23], v[162:165], v[186:189], v[20:23]
	v_mfma_f32_16x16x32_bf16 v[16:19], v[166:169], v[182:185], v[16:19]
	s_nop 0
	v_mfma_f32_16x16x32_bf16 v[16:19], v[170:173], v[186:189], v[16:19]
	v_mfma_f32_16x16x32_bf16 v[12:15], v[158:161], v[190:193], v[12:15]
	s_nop 0
	v_mfma_f32_16x16x32_bf16 v[12:15], v[162:165], v[194:197], v[12:15]
	v_mfma_f32_16x16x32_bf16 v[8:11], v[166:169], v[190:193], v[8:11]
	s_nop 0
	v_mfma_f32_16x16x32_bf16 v[8:11], v[170:173], v[194:197], v[8:11]
	v_mfma_f32_16x16x32_bf16 v[4:7], v[158:161], v[234:237], v[4:7]
	s_nop 0
	v_mfma_f32_16x16x32_bf16 v[4:7], v[162:165], v[238:241], v[4:7]
	v_mfma_f32_16x16x32_bf16 v[0:3], v[166:169], v[234:237], v[0:3]
	s_nop 0
	v_mfma_f32_16x16x32_bf16 v[0:3], v[170:173], v[238:241], v[0:3]
	s_setprio 0
	s_barrier
	s_bitcmp0_b32 s46, 0
	s_waitcnt vmcnt(15)
	v_mul_f32_e32 v128, 0x42800000, v128
	s_waitcnt vmcnt(14)
	v_mul_f32_e32 v132, 0x42800000, v132
	v_mul_f32_e32 v129, 0x42800000, v129
	v_mul_f32_e32 v133, 0x42800000, v133
	v_mul_f32_e32 v130, 0x42800000, v130
	v_mul_f32_e32 v134, 0x42800000, v134
	v_mul_f32_e32 v131, 0x42800000, v131
	v_mul_f32_e32 v135, 0x42800000, v135
	s_mov_b64 s[46:47], -1
	s_cbranch_scc0 .LBB0_350
	s_andn2_b64 vcc, exec, s[46:47]
	s_cbranch_vccnz .LBB0_346
	s_branch .LBB0_351

.LBB0_592:
	s_waitcnt lgkmcnt(0)
	s_add_i32 s4, s60, 0x180
	s_add_i32 s5, s42, 0x180
	s_barrier
	s_setprio 1
	s_waitcnt lgkmcnt(7)
	v_mfma_f32_16x16x32_bf16 v[60:63], v[164:167], v[196:199], 0
	s_waitcnt lgkmcnt(6)
	v_mfma_f32_16x16x32_bf16 v[60:63], v[160:163], v[192:195], v[60:63]
	v_mfma_f32_16x16x32_bf16 v[56:59], v[156:159], v[196:199], 0
	s_nop 0
	v_mfma_f32_16x16x32_bf16 v[56:59], v[152:155], v[192:195], v[56:59]
	s_waitcnt lgkmcnt(5)
	v_mfma_f32_16x16x32_bf16 v[52:55], v[164:167], v[188:191], 0
	s_waitcnt lgkmcnt(4)
	v_mfma_f32_16x16x32_bf16 v[52:55], v[160:163], v[184:187], v[52:55]
	v_mfma_f32_16x16x32_bf16 v[48:51], v[156:159], v[188:191], 0
	s_nop 0
	v_mfma_f32_16x16x32_bf16 v[48:51], v[152:155], v[184:187], v[48:51]
	s_waitcnt lgkmcnt(3)
	v_mfma_f32_16x16x32_bf16 v[44:47], v[164:167], v[180:183], 0
	s_waitcnt lgkmcnt(2)
	v_mfma_f32_16x16x32_bf16 v[44:47], v[160:163], v[176:179], v[44:47]
	v_mfma_f32_16x16x32_bf16 v[40:43], v[156:159], v[180:183], 0
	s_nop 0
	v_mfma_f32_16x16x32_bf16 v[40:43], v[152:155], v[176:179], v[40:43]
	s_waitcnt lgkmcnt(1)
	v_mfma_f32_16x16x32_bf16 v[36:39], v[164:167], v[172:175], 0
	s_waitcnt lgkmcnt(0)
	v_mfma_f32_16x16x32_bf16 v[36:39], v[160:163], v[168:171], v[36:39]
	v_mfma_f32_16x16x32_bf16 v[32:35], v[156:159], v[172:175], 0
	s_nop 0
	v_mfma_f32_16x16x32_bf16 v[32:35], v[152:155], v[168:171], v[32:35]
	s_setprio 0
	s_setprio 1
	v_mfma_f32_16x16x32_bf16 v[28:31], v[148:151], v[196:199], 0
	s_nop 0
	v_mfma_f32_16x16x32_bf16 v[28:31], v[144:147], v[192:195], v[28:31]
	v_mfma_f32_16x16x32_bf16 v[24:27], v[140:143], v[196:199], 0
	s_nop 0
	v_mfma_f32_16x16x32_bf16 v[24:27], v[136:139], v[192:195], v[24:27]
	v_mfma_f32_16x16x32_bf16 v[20:23], v[148:151], v[188:191], 0
	s_nop 0
	v_mfma_f32_16x16x32_bf16 v[20:23], v[144:147], v[184:187], v[20:23]
	v_mfma_f32_16x16x32_bf16 v[16:19], v[140:143], v[188:191], 0
	s_nop 0
	v_mfma_f32_16x16x32_bf16 v[16:19], v[136:139], v[184:187], v[16:19]
	v_mfma_f32_16x16x32_bf16 v[12:15], v[148:151], v[180:183], 0
	s_nop 0
	v_mfma_f32_16x16x32_bf16 v[12:15], v[144:147], v[176:179], v[12:15]
	v_mfma_f32_16x16x32_bf16 v[8:11], v[140:143], v[180:183], 0
	s_nop 0
	v_mfma_f32_16x16x32_bf16 v[8:11], v[136:139], v[176:179], v[8:11]
	v_mfma_f32_16x16x32_bf16 v[4:7], v[148:151], v[172:175], 0
	s_nop 0
	v_mfma_f32_16x16x32_bf16 v[4:7], v[144:147], v[168:171], v[4:7]
	v_mfma_f32_16x16x32_bf16 v[0:3], v[140:143], v[172:175], 0
	s_nop 0
	v_mfma_f32_16x16x32_bf16 v[0:3], v[136:139], v[168:171], v[0:3]
	s_setprio 0
	s_barrier
	ds_read_b128 v[164:167], v224
	ds_read_b128 v[160:163], v225
	ds_read_b128 v[156:159], v226
	ds_read_b128 v[152:155], v227
	ds_read_b128 v[148:151], v228
	ds_read_b128 v[144:147], v229
	ds_read_b128 v[140:143], v230
	ds_read_b128 v[136:139], v231
	s_mov_b32 m0, s68
	s_add_i32 s10, s60, 0x100100
	buffer_load_dwordx4 v213, s[12:15], s10 offen lds
	s_add_i32 s10, s60, 0x180100
	s_mov_b32 m0, s69
	s_nop 0
	buffer_load_dwordx4 v213, s[12:15], s10 offen lds
	ds_read_b128 v[168:171], v232 offset:32768
	ds_read_b128 v[172:175], v232 offset:33792
	ds_read_b128 v[176:179], v232 offset:34816
	ds_read_b128 v[180:183], v232 offset:35840
	ds_read_b128 v[184:187], v232 offset:36864
	ds_read_b128 v[188:191], v232 offset:37888
	ds_read_b128 v[192:195], v232 offset:38912
	ds_read_b128 v[196:199], v232 offset:39936
	s_waitcnt vmcnt(10)
	s_waitcnt lgkmcnt(4)
	s_barrier
	s_setprio 1
	s_waitcnt lgkmcnt(7)
	v_mfma_f32_16x16x32_bf16 v[124:127], v[164:167], v[168:171], v[124:127]
	s_waitcnt lgkmcnt(6)
	v_mfma_f32_16x16x32_bf16 v[124:127], v[160:163], v[172:175], v[124:127]
	v_mfma_f32_16x16x32_bf16 v[120:123], v[156:159], v[168:171], v[120:123]
	s_nop 0
	v_mfma_f32_16x16x32_bf16 v[120:123], v[152:155], v[172:175], v[120:123]
	s_waitcnt lgkmcnt(5)
	v_mfma_f32_16x16x32_bf16 v[116:119], v[164:167], v[176:179], v[116:119]
	s_waitcnt lgkmcnt(4)
	v_mfma_f32_16x16x32_bf16 v[116:119], v[160:163], v[180:183], v[116:119]
	v_mfma_f32_16x16x32_bf16 v[112:115], v[156:159], v[176:179], v[112:115]
	s_nop 0
	v_mfma_f32_16x16x32_bf16 v[112:115], v[152:155], v[180:183], v[112:115]
	s_waitcnt lgkmcnt(3)
	v_mfma_f32_16x16x32_bf16 v[108:111], v[164:167], v[184:187], v[108:111]
	s_waitcnt lgkmcnt(2)
	v_mfma_f32_16x16x32_bf16 v[108:111], v[160:163], v[188:191], v[108:111]
	v_mfma_f32_16x16x32_bf16 v[104:107], v[156:159], v[184:187], v[104:107]
	s_nop 0
	v_mfma_f32_16x16x32_bf16 v[104:107], v[152:155], v[188:191], v[104:107]
	s_waitcnt lgkmcnt(1)
	v_mfma_f32_16x16x32_bf16 v[100:103], v[164:167], v[192:195], v[100:103]
	s_waitcnt lgkmcnt(0)
	v_mfma_f32_16x16x32_bf16 v[100:103], v[160:163], v[196:199], v[100:103]
	v_mfma_f32_16x16x32_bf16 v[96:99], v[156:159], v[192:195], v[96:99]
	s_nop 0
	v_mfma_f32_16x16x32_bf16 v[96:99], v[152:155], v[196:199], v[96:99]
	s_setprio 0
	s_setprio 1
	v_mfma_f32_16x16x32_bf16 v[92:95], v[148:151], v[168:171], v[92:95]
	s_nop 0
	v_mfma_f32_16x16x32_bf16 v[92:95], v[144:147], v[172:175], v[92:95]
	v_mfma_f32_16x16x32_bf16 v[88:91], v[140:143], v[168:171], v[88:91]
	s_nop 0
	v_mfma_f32_16x16x32_bf16 v[88:91], v[136:139], v[172:175], v[88:91]
	v_mfma_f32_16x16x32_bf16 v[84:87], v[148:151], v[176:179], v[84:87]
	s_nop 0
	v_mfma_f32_16x16x32_bf16 v[84:87], v[144:147], v[180:183], v[84:87]
	v_mfma_f32_16x16x32_bf16 v[80:83], v[140:143], v[176:179], v[80:83]
	s_nop 0
	v_mfma_f32_16x16x32_bf16 v[80:83], v[136:139], v[180:183], v[80:83]
	v_mfma_f32_16x16x32_bf16 v[76:79], v[148:151], v[184:187], v[76:79]
	s_nop 0
	v_mfma_f32_16x16x32_bf16 v[76:79], v[144:147], v[188:191], v[76:79]
	v_mfma_f32_16x16x32_bf16 v[72:75], v[140:143], v[184:187], v[72:75]
	s_nop 0
	v_mfma_f32_16x16x32_bf16 v[72:75], v[136:139], v[188:191], v[72:75]
	v_mfma_f32_16x16x32_bf16 v[68:71], v[148:151], v[192:195], v[68:71]
	s_nop 0
	v_mfma_f32_16x16x32_bf16 v[68:71], v[144:147], v[196:199], v[68:71]
	v_mfma_f32_16x16x32_bf16 v[64:67], v[140:143], v[192:195], v[64:67]
	s_nop 0
	v_mfma_f32_16x16x32_bf16 v[64:67], v[136:139], v[196:199], v[64:67]
	s_setprio 0
	s_barrier
	s_mov_b32 m0, s72
	s_mov_b32 s10, s14
	s_mov_b32 s11, s15
	buffer_load_dwordx4 v214, s[8:11], s5 offen lds
	s_add_i32 s5, s42, 0x40180
	s_mov_b32 m0, s73
	s_nop 0
	buffer_load_dwordx4 v214, s[8:11], s5 offen lds
	s_add_i32 s5, s42, 0x4180
	s_mov_b32 m0, s76
	s_nop 0
	buffer_load_dwordx4 v214, s[8:11], s5 offen lds
	s_add_i32 s5, s42, 0x44180
	s_mov_b32 m0, s77
	s_nop 0
	buffer_load_dwordx4 v214, s[8:11], s5 offen lds
	s_mov_b32 m0, s74
	s_nop 0
	buffer_load_dwordx4 v213, s[12:15], s4 offen lds
	s_add_i32 s4, s60, 0x80180
	s_mov_b32 m0, s75
	s_nop 0
	buffer_load_dwordx4 v213, s[12:15], s4 offen lds
	ds_read_b128 v[168:171], v232 offset:49152
	ds_read_b128 v[172:175], v232 offset:50176
	ds_read_b128 v[176:179], v232 offset:51200
	ds_read_b128 v[180:183], v232 offset:52224
	ds_read_b128 v[184:187], v232 offset:53248
	ds_read_b128 v[188:191], v232 offset:54272
	ds_read_b128 v[192:195], v232 offset:55296
	ds_read_b128 v[196:199], v232 offset:56320
	s_waitcnt vmcnt(8)
	s_waitcnt lgkmcnt(0)
	s_barrier
	s_setprio 1
	s_waitcnt lgkmcnt(7)
	v_mfma_f32_16x16x32_bf16 v[60:63], v[164:167], v[168:171], v[60:63]
	s_waitcnt lgkmcnt(6)
	v_mfma_f32_16x16x32_bf16 v[60:63], v[160:163], v[172:175], v[60:63]
	v_mfma_f32_16x16x32_bf16 v[56:59], v[156:159], v[168:171], v[56:59]
	s_nop 0
	v_mfma_f32_16x16x32_bf16 v[56:59], v[152:155], v[172:175], v[56:59]
	s_waitcnt lgkmcnt(5)
	v_mfma_f32_16x16x32_bf16 v[52:55], v[164:167], v[176:179], v[52:55]
	s_waitcnt lgkmcnt(4)
	v_mfma_f32_16x16x32_bf16 v[52:55], v[160:163], v[180:183], v[52:55]
	v_mfma_f32_16x16x32_bf16 v[48:51], v[156:159], v[176:179], v[48:51]
	s_nop 0
	v_mfma_f32_16x16x32_bf16 v[48:51], v[152:155], v[180:183], v[48:51]
	s_waitcnt lgkmcnt(3)
	v_mfma_f32_16x16x32_bf16 v[44:47], v[164:167], v[184:187], v[44:47]
	s_waitcnt lgkmcnt(2)
	v_mfma_f32_16x16x32_bf16 v[44:47], v[160:163], v[188:191], v[44:47]
	v_mfma_f32_16x16x32_bf16 v[40:43], v[156:159], v[184:187], v[40:43]
	s_nop 0
	v_mfma_f32_16x16x32_bf16 v[40:43], v[152:155], v[188:191], v[40:43]
	s_waitcnt lgkmcnt(1)
	v_mfma_f32_16x16x32_bf16 v[36:39], v[164:167], v[192:195], v[36:39]
	s_waitcnt lgkmcnt(0)
	v_mfma_f32_16x16x32_bf16 v[36:39], v[160:163], v[196:199], v[36:39]
	v_mfma_f32_16x16x32_bf16 v[32:35], v[156:159], v[192:195], v[32:35]
	s_nop 0
	v_mfma_f32_16x16x32_bf16 v[32:35], v[152:155], v[196:199], v[32:35]
	s_setprio 0
	s_setprio 1
	v_mfma_f32_16x16x32_bf16 v[28:31], v[148:151], v[168:171], v[28:31]
	s_nop 0
	v_mfma_f32_16x16x32_bf16 v[28:31], v[144:147], v[172:175], v[28:31]
	v_mfma_f32_16x16x32_bf16 v[24:27], v[140:143], v[168:171], v[24:27]
	s_nop 0
	v_mfma_f32_16x16x32_bf16 v[24:27], v[136:139], v[172:175], v[24:27]
	v_mfma_f32_16x16x32_bf16 v[20:23], v[148:151], v[176:179], v[20:23]
	s_nop 0
	v_mfma_f32_16x16x32_bf16 v[20:23], v[144:147], v[180:183], v[20:23]
	v_mfma_f32_16x16x32_bf16 v[16:19], v[140:143], v[176:179], v[16:19]
	s_nop 0
	v_mfma_f32_16x16x32_bf16 v[16:19], v[136:139], v[180:183], v[16:19]
	v_mfma_f32_16x16x32_bf16 v[12:15], v[148:151], v[184:187], v[12:15]
	s_nop 0
	v_mfma_f32_16x16x32_bf16 v[12:15], v[144:147], v[188:191], v[12:15]
	v_mfma_f32_16x16x32_bf16 v[8:11], v[140:143], v[184:187], v[8:11]
	s_nop 0
	v_mfma_f32_16x16x32_bf16 v[8:11], v[136:139], v[188:191], v[8:11]
	v_mfma_f32_16x16x32_bf16 v[4:7], v[148:151], v[192:195], v[4:7]
	s_nop 0
	v_mfma_f32_16x16x32_bf16 v[4:7], v[144:147], v[196:199], v[4:7]
	v_mfma_f32_16x16x32_bf16 v[0:3], v[140:143], v[192:195], v[0:3]
	s_nop 0
	v_mfma_f32_16x16x32_bf16 v[0:3], v[136:139], v[196:199], v[0:3]
	s_setprio 0
	s_barrier
	s_waitcnt vmcnt(14)
	v_mul_f32_e32 v132, 0x42800000, v132
	v_mul_f32_e32 v128, 0x42800000, v128
	v_mul_f32_e32 v133, 0x42800000, v133
	v_mul_f32_e32 v129, 0x42800000, v129
	v_mul_f32_e32 v134, 0x42800000, v134
	v_mul_f32_e32 v130, 0x42800000, v130
	v_mul_f32_e32 v135, 0x42800000, v135
	v_mul_f32_e32 v131, 0x42800000, v131
	v_cvt_pk_fp8_f32 v202, v128, v132
	v_cvt_pk_fp8_f32 v233, v129, v133
	v_cvt_pk_fp8_f32 v234, v130, v134
	v_cvt_pk_fp8_f32 v235, v131, v135
	s_add_i32 s33, s42, 0x200
	s_mov_b32 s66, 0
	s_mov_b32 s89, s70
	s_mov_b32 s90, s71
	s_branch .LBB0_595

.LBB0_595:
	v_mov_b32_e32 v152, v202
	v_mov_b32_e32 v153, v233
	v_mov_b32_e32 v154, v234
	v_mov_b32_e32 v155, v235
	ds_read_b128 v[158:161], v216
	ds_read_b128 v[162:165], v217
	ds_read_b128 v[166:169], v218
	ds_read_b128 v[170:173], v219
	ds_read_b128 v[148:151], v220
	ds_read_b128 v[144:147], v221
	ds_read_b128 v[140:143], v222
	ds_read_b128 v[136:139], v223
	s_add_i32 s4, s60, s66
	s_mov_b32 s42, s90
	s_add_i32 s90, s90, 1
	s_add_i32 s5, s4, 0x200
	s_add_i32 s67, s33, s66
	s_cmpk_eq_i32 s66, 0x200
	s_cselect_b32 s43, s87, s5
	s_cselect_b32 s93, s88, s67
	s_add_i32 s92, s43, 0x80
	s_mov_b32 m0, s78
	s_add_i32 s5, s4, 0x100180
	buffer_load_dwordx4 v213, s[12:15], s5 offen lds
	s_add_i32 s4, s4, 0x180180
	s_mov_b32 m0, s81
	s_add_i32 s94, s93, 0x80
	buffer_load_dwordx4 v213, s[12:15], s4 offen lds
	s_lshr_b32 s4, s90, 2
	s_mul_i32 s67, s4, s34
	s_add_i32 s67, s67, s2
	s_cmp_lt_i32 s4, s3
	s_cselect_b64 s[4:5], -1, 0
	s_and_b64 s[96:97], s[4:5], exec
	s_cselect_b32 s91, s67, 0
	s_ashr_i32 s96, s91, 7
	s_bfe_u32 s95, s90, 0x10001
	s_ashr_i32 s97, s96, 31
	s_or_b32 s95, s95, s79
	s_lshl_b64 s[96:97], s[96:97], 23
	s_add_u32 s96, s48, s96
	s_addc_u32 s97, s49, s97
	s_lshl_b32 vcc_lo, s91, 16
	s_and_b32 vcc_lo, vcc_lo, 0x600000
	s_add_u32 s96, s96, vcc_lo
	s_addc_u32 s97, s97, 0
	s_lshl_b32 s91, s91, 7
	s_and_b32 s91, s91, 0xf80
	s_lshl_b32 vcc_lo, s91, 2
	s_add_u32 s96, s96, vcc_lo
	v_and_or_b32 v202, s89, 2, v200
	s_addc_u32 s97, s97, 0
	v_lshl_or_b32 v156, s95, 5, v215
	v_lshlrev_b64 v[128:129], 14, v[202:203]
	v_lshl_add_u64 v[128:129], s[96:97], 0, v[128:129]
	v_lshlrev_b32_e32 v202, 2, v156
	v_lshl_add_u64 v[128:129], v[128:129], 0, v[202:203]
	s_movk_i32 s95, 0x4000
	v_add_co_u32_e32 v132, vcc, s95, v128
	s_nop 1
	v_addc_co_u32_e32 v133, vcc, 0, v129, vcc
	global_load_dwordx4 v[128:131], v[128:129], off nt
	s_nop 0
	global_load_dwordx4 v[132:135], v[132:133], off nt
	ds_read_b128 v[174:177], v232
	ds_read_b128 v[178:181], v232 offset:1024
	ds_read_b128 v[182:185], v232 offset:2048
	ds_read_b128 v[186:189], v232 offset:3072
	ds_read_b128 v[190:193], v232 offset:4096
	ds_read_b128 v[194:197], v232 offset:5120
	ds_read_b128 v[234:237], v232 offset:6144
	ds_read_b128 v[238:241], v232 offset:7168
	s_waitcnt vmcnt(10)
	s_waitcnt lgkmcnt(4)
	s_barrier
	s_setprio 1
	s_waitcnt lgkmcnt(7)
	v_mfma_f32_16x16x32_bf16 v[124:127], v[158:161], v[174:177], v[124:127]
	s_waitcnt lgkmcnt(6)
	v_mfma_f32_16x16x32_bf16 v[124:127], v[162:165], v[178:181], v[124:127]
	v_mfma_f32_16x16x32_bf16 v[120:123], v[166:169], v[174:177], v[120:123]
	s_nop 0
	v_mfma_f32_16x16x32_bf16 v[120:123], v[170:173], v[178:181], v[120:123]
	s_waitcnt lgkmcnt(5)
	v_mfma_f32_16x16x32_bf16 v[116:119], v[158:161], v[182:185], v[116:119]
	s_waitcnt lgkmcnt(4)
	v_mfma_f32_16x16x32_bf16 v[116:119], v[162:165], v[186:189], v[116:119]
	v_mfma_f32_16x16x32_bf16 v[112:115], v[166:169], v[182:185], v[112:115]
	s_nop 0
	v_mfma_f32_16x16x32_bf16 v[112:115], v[170:173], v[186:189], v[112:115]
	s_waitcnt lgkmcnt(3)
	v_mfma_f32_16x16x32_bf16 v[108:111], v[158:161], v[190:193], v[108:111]
	s_waitcnt lgkmcnt(2)
	v_mfma_f32_16x16x32_bf16 v[108:111], v[162:165], v[194:197], v[108:111]
	v_mfma_f32_16x16x32_bf16 v[104:107], v[166:169], v[190:193], v[104:107]
	s_nop 0
	v_mfma_f32_16x16x32_bf16 v[104:107], v[170:173], v[194:197], v[104:107]
	s_waitcnt lgkmcnt(1)
	v_mfma_f32_16x16x32_bf16 v[100:103], v[158:161], v[234:237], v[100:103]
	s_waitcnt lgkmcnt(0)
	v_mfma_f32_16x16x32_bf16 v[100:103], v[162:165], v[238:241], v[100:103]
	v_mfma_f32_16x16x32_bf16 v[96:99], v[166:169], v[234:237], v[96:99]
	s_nop 0
	v_mfma_f32_16x16x32_bf16 v[96:99], v[170:173], v[238:241], v[96:99]
	s_setprio 0
	s_setprio 1
	v_mfma_f32_16x16x32_bf16 v[92:95], v[148:151], v[174:177], v[92:95]
	s_nop 0
	v_mfma_f32_16x16x32_bf16 v[92:95], v[144:147], v[178:181], v[92:95]
	v_mfma_f32_16x16x32_bf16 v[88:91], v[140:143], v[174:177], v[88:91]
	s_nop 0
	v_mfma_f32_16x16x32_bf16 v[88:91], v[136:139], v[178:181], v[88:91]
	v_mfma_f32_16x16x32_bf16 v[84:87], v[148:151], v[182:185], v[84:87]
	s_nop 0
	v_mfma_f32_16x16x32_bf16 v[84:87], v[144:147], v[186:189], v[84:87]
	v_mfma_f32_16x16x32_bf16 v[80:83], v[140:143], v[182:185], v[80:83]
	s_nop 0
	v_mfma_f32_16x16x32_bf16 v[80:83], v[136:139], v[186:189], v[80:83]
	v_mfma_f32_16x16x32_bf16 v[76:79], v[148:151], v[190:193], v[76:79]
	s_nop 0
	v_mfma_f32_16x16x32_bf16 v[76:79], v[144:147], v[194:197], v[76:79]
	v_mfma_f32_16x16x32_bf16 v[72:75], v[140:143], v[190:193], v[72:75]
	s_nop 0
	v_mfma_f32_16x16x32_bf16 v[72:75], v[136:139], v[194:197], v[72:75]
	v_mfma_f32_16x16x32_bf16 v[68:71], v[148:151], v[234:237], v[68:71]
	s_nop 0
	v_mfma_f32_16x16x32_bf16 v[68:71], v[144:147], v[238:241], v[68:71]
	v_mfma_f32_16x16x32_bf16 v[64:67], v[140:143], v[234:237], v[64:67]
	s_nop 0
	v_mfma_f32_16x16x32_bf16 v[64:67], v[136:139], v[238:241], v[64:67]
	s_setprio 0
	s_barrier
	s_mov_b32 m0, s47
	s_add_i32 s95, s93, 0x40000
	buffer_load_dwordx4 v214, s[8:11], s93 offen lds
	s_mov_b32 m0, s62
	s_nop 0
	buffer_load_dwordx4 v214, s[8:11], s95 offen lds
	s_add_i32 s95, s93, 0x4000
	s_mov_b32 m0, s63
	s_nop 0
	buffer_load_dwordx4 v214, s[8:11], s95 offen lds
	s_add_i32 s95, s93, 0x44000
	s_mov_b32 m0, s64
	s_nop 0
	buffer_load_dwordx4 v214, s[8:11], s95 offen lds
	s_mov_b32 m0, s46
	s_add_i32 s95, s43, 0x80000
	buffer_load_dwordx4 v213, s[12:15], s43 offen lds
	s_mov_b32 m0, s65
	s_nop 0
	buffer_load_dwordx4 v213, s[12:15], s95 offen lds
	ds_read_b128 v[174:177], v232 offset:16384
	ds_read_b128 v[178:181], v232 offset:17408
	ds_read_b128 v[182:185], v232 offset:18432
	ds_read_b128 v[186:189], v232 offset:19456
	ds_read_b128 v[190:193], v232 offset:20480
	ds_read_b128 v[194:197], v232 offset:21504
	ds_read_b128 v[234:237], v232 offset:22528
	ds_read_b128 v[238:241], v232 offset:23552
	s_waitcnt vmcnt(10)
	s_waitcnt lgkmcnt(0)
	s_barrier
	s_setprio 1
	s_waitcnt lgkmcnt(7)
	v_mfma_f32_16x16x32_bf16 v[60:63], v[158:161], v[174:177], v[60:63]
	s_waitcnt lgkmcnt(6)
	v_mfma_f32_16x16x32_bf16 v[60:63], v[162:165], v[178:181], v[60:63]
	v_mfma_f32_16x16x32_bf16 v[56:59], v[166:169], v[174:177], v[56:59]
	s_nop 0
	v_mfma_f32_16x16x32_bf16 v[56:59], v[170:173], v[178:181], v[56:59]
	s_waitcnt lgkmcnt(5)
	v_mfma_f32_16x16x32_bf16 v[52:55], v[158:161], v[182:185], v[52:55]
	s_waitcnt lgkmcnt(4)
	v_mfma_f32_16x16x32_bf16 v[52:55], v[162:165], v[186:189], v[52:55]
	v_mfma_f32_16x16x32_bf16 v[48:51], v[166:169], v[182:185], v[48:51]
	s_nop 0
	v_mfma_f32_16x16x32_bf16 v[48:51], v[170:173], v[186:189], v[48:51]
	s_waitcnt lgkmcnt(3)
	v_mfma_f32_16x16x32_bf16 v[44:47], v[158:161], v[190:193], v[44:47]
	s_waitcnt lgkmcnt(2)
	v_mfma_f32_16x16x32_bf16 v[44:47], v[162:165], v[194:197], v[44:47]
	v_mfma_f32_16x16x32_bf16 v[40:43], v[166:169], v[190:193], v[40:43]
	s_nop 0
	v_mfma_f32_16x16x32_bf16 v[40:43], v[170:173], v[194:197], v[40:43]
	s_waitcnt lgkmcnt(1)
	v_mfma_f32_16x16x32_bf16 v[36:39], v[158:161], v[234:237], v[36:39]
	s_waitcnt lgkmcnt(0)
	v_mfma_f32_16x16x32_bf16 v[36:39], v[162:165], v[238:241], v[36:39]
	v_mfma_f32_16x16x32_bf16 v[32:35], v[166:169], v[234:237], v[32:35]
	s_nop 0
	v_mfma_f32_16x16x32_bf16 v[32:35], v[170:173], v[238:241], v[32:35]
	s_setprio 0
	s_setprio 1
	v_mfma_f32_16x16x32_bf16 v[28:31], v[148:151], v[174:177], v[28:31]
	s_nop 0
	v_mfma_f32_16x16x32_bf16 v[28:31], v[144:147], v[178:181], v[28:31]
	v_mfma_f32_16x16x32_bf16 v[24:27], v[140:143], v[174:177], v[24:27]
	s_nop 0
	v_mfma_f32_16x16x32_bf16 v[24:27], v[136:139], v[178:181], v[24:27]
	v_mfma_f32_16x16x32_bf16 v[20:23], v[148:151], v[182:185], v[20:23]
	s_nop 0
	v_mfma_f32_16x16x32_bf16 v[20:23], v[144:147], v[186:189], v[20:23]
	v_mfma_f32_16x16x32_bf16 v[16:19], v[140:143], v[182:185], v[16:19]
	s_nop 0
	v_mfma_f32_16x16x32_bf16 v[16:19], v[136:139], v[186:189], v[16:19]
	v_mfma_f32_16x16x32_bf16 v[12:15], v[148:151], v[190:193], v[12:15]
	s_nop 0
	v_mfma_f32_16x16x32_bf16 v[12:15], v[144:147], v[194:197], v[12:15]
	v_mfma_f32_16x16x32_bf16 v[8:11], v[140:143], v[190:193], v[8:11]
	s_nop 0
	v_mfma_f32_16x16x32_bf16 v[8:11], v[136:139], v[194:197], v[8:11]
	v_mfma_f32_16x16x32_bf16 v[4:7], v[148:151], v[234:237], v[4:7]
	s_nop 0
	v_mfma_f32_16x16x32_bf16 v[4:7], v[144:147], v[238:241], v[4:7]
	v_mfma_f32_16x16x32_bf16 v[0:3], v[140:143], v[234:237], v[0:3]
	s_nop 0
	v_mfma_f32_16x16x32_bf16 v[0:3], v[136:139], v[238:241], v[0:3]
	s_setprio 0
	s_barrier
	ds_read_b128 v[136:139], v224
	ds_read_b128 v[140:143], v225
	ds_read_b128 v[144:147], v226
	ds_read_b128 v[148:151], v227
	ds_read_b128 v[158:161], v228
	ds_read_b128 v[162:165], v229
	ds_read_b128 v[166:169], v230
	ds_read_b128 v[170:173], v231
	s_mov_b32 m0, s68
	s_add_i32 s95, s43, 0x100000
	buffer_load_dwordx4 v213, s[12:15], s95 offen lds
	s_add_i32 s95, s43, 0x180000
	s_mov_b32 m0, s69
	s_nop 0
	buffer_load_dwordx4 v213, s[12:15], s95 offen lds
	ds_read_b128 v[174:177], v232 offset:32768
	ds_read_b128 v[178:181], v232 offset:33792
	ds_read_b128 v[182:185], v232 offset:34816
	ds_read_b128 v[186:189], v232 offset:35840
	ds_read_b128 v[190:193], v232 offset:36864
	ds_read_b128 v[194:197], v232 offset:37888
	ds_read_b128 v[234:237], v232 offset:38912
	ds_read_b128 v[238:241], v232 offset:39936
	s_waitcnt vmcnt(10)
	s_waitcnt lgkmcnt(4)
	s_barrier
	s_setprio 1
	s_waitcnt lgkmcnt(7)
	v_mfma_f32_16x16x32_bf16 v[124:127], v[136:139], v[174:177], v[124:127]
	s_waitcnt lgkmcnt(6)
	v_mfma_f32_16x16x32_bf16 v[124:127], v[140:143], v[178:181], v[124:127]
	v_mfma_f32_16x16x32_bf16 v[120:123], v[144:147], v[174:177], v[120:123]
	s_nop 0
	v_mfma_f32_16x16x32_bf16 v[120:123], v[148:151], v[178:181], v[120:123]
	s_waitcnt lgkmcnt(5)
	v_mfma_f32_16x16x32_bf16 v[116:119], v[136:139], v[182:185], v[116:119]
	s_waitcnt lgkmcnt(4)
	v_mfma_f32_16x16x32_bf16 v[116:119], v[140:143], v[186:189], v[116:119]
	v_mfma_f32_16x16x32_bf16 v[112:115], v[144:147], v[182:185], v[112:115]
	s_nop 0
	v_mfma_f32_16x16x32_bf16 v[112:115], v[148:151], v[186:189], v[112:115]
	s_waitcnt lgkmcnt(3)
	v_mfma_f32_16x16x32_bf16 v[108:111], v[136:139], v[190:193], v[108:111]
	s_waitcnt lgkmcnt(2)
	v_mfma_f32_16x16x32_bf16 v[108:111], v[140:143], v[194:197], v[108:111]
	v_mfma_f32_16x16x32_bf16 v[104:107], v[144:147], v[190:193], v[104:107]
	s_nop 0
	v_mfma_f32_16x16x32_bf16 v[104:107], v[148:151], v[194:197], v[104:107]
	s_waitcnt lgkmcnt(1)
	v_mfma_f32_16x16x32_bf16 v[100:103], v[136:139], v[234:237], v[100:103]
	s_waitcnt lgkmcnt(0)
	v_mfma_f32_16x16x32_bf16 v[100:103], v[140:143], v[238:241], v[100:103]
	v_mfma_f32_16x16x32_bf16 v[96:99], v[144:147], v[234:237], v[96:99]
	s_nop 0
	v_mfma_f32_16x16x32_bf16 v[96:99], v[148:151], v[238:241], v[96:99]
	s_setprio 0
	s_setprio 1
	v_mfma_f32_16x16x32_bf16 v[92:95], v[158:161], v[174:177], v[92:95]
	s_nop 0
	v_mfma_f32_16x16x32_bf16 v[92:95], v[162:165], v[178:181], v[92:95]
	v_mfma_f32_16x16x32_bf16 v[88:91], v[166:169], v[174:177], v[88:91]
	s_nop 0
	v_mfma_f32_16x16x32_bf16 v[88:91], v[170:173], v[178:181], v[88:91]
	v_mfma_f32_16x16x32_bf16 v[84:87], v[158:161], v[182:185], v[84:87]
	s_nop 0
	v_mfma_f32_16x16x32_bf16 v[84:87], v[162:165], v[186:189], v[84:87]
	v_mfma_f32_16x16x32_bf16 v[80:83], v[166:169], v[182:185], v[80:83]
	s_nop 0
	v_mfma_f32_16x16x32_bf16 v[80:83], v[170:173], v[186:189], v[80:83]
	v_mfma_f32_16x16x32_bf16 v[76:79], v[158:161], v[190:193], v[76:79]
	s_nop 0
	v_mfma_f32_16x16x32_bf16 v[76:79], v[162:165], v[194:197], v[76:79]
	v_mfma_f32_16x16x32_bf16 v[72:75], v[166:169], v[190:193], v[72:75]
	s_nop 0
	v_mfma_f32_16x16x32_bf16 v[72:75], v[170:173], v[194:197], v[72:75]
	v_mfma_f32_16x16x32_bf16 v[68:71], v[158:161], v[234:237], v[68:71]
	s_nop 0
	v_mfma_f32_16x16x32_bf16 v[68:71], v[162:165], v[238:241], v[68:71]
	v_mfma_f32_16x16x32_bf16 v[64:67], v[166:169], v[234:237], v[64:67]
	s_nop 0
	v_mfma_f32_16x16x32_bf16 v[64:67], v[170:173], v[238:241], v[64:67]
	s_setprio 0
	s_barrier
	s_mov_b32 m0, s72
	s_add_i32 s43, s43, 0x80080
	buffer_load_dwordx4 v214, s[8:11], s94 offen lds
	s_add_i32 s94, s93, 0x40080
	s_mov_b32 m0, s73
	s_nop 0
	buffer_load_dwordx4 v214, s[8:11], s94 offen lds
	s_add_i32 s94, s93, 0x4080
	s_mov_b32 m0, s76
	s_add_i32 s93, s93, 0x44080
	buffer_load_dwordx4 v214, s[8:11], s94 offen lds
	s_mov_b32 m0, s77
	s_nop 0
	buffer_load_dwordx4 v214, s[8:11], s93 offen lds
	s_mov_b32 m0, s74
	s_nop 0
	buffer_load_dwordx4 v213, s[12:15], s92 offen lds
	s_mov_b32 m0, s75
	s_nop 0
	buffer_load_dwordx4 v213, s[12:15], s43 offen lds
	ds_read_b128 v[174:177], v232 offset:49152
	ds_read_b128 v[178:181], v232 offset:50176
	ds_read_b128 v[182:185], v232 offset:51200
	ds_read_b128 v[186:189], v232 offset:52224
	ds_read_b128 v[190:193], v232 offset:53248
	ds_read_b128 v[194:197], v232 offset:54272
	ds_read_b128 v[234:237], v232 offset:55296
	ds_read_b128 v[238:241], v232 offset:56320
	s_waitcnt vmcnt(8)
	s_waitcnt lgkmcnt(0)
	s_barrier
	s_setprio 1
	s_waitcnt lgkmcnt(7)
	v_mfma_f32_16x16x32_bf16 v[60:63], v[136:139], v[174:177], v[60:63]
	s_waitcnt lgkmcnt(6)
	v_mfma_f32_16x16x32_bf16 v[60:63], v[140:143], v[178:181], v[60:63]
	v_mfma_f32_16x16x32_bf16 v[56:59], v[144:147], v[174:177], v[56:59]
	s_nop 0
	v_mfma_f32_16x16x32_bf16 v[56:59], v[148:151], v[178:181], v[56:59]
	s_waitcnt lgkmcnt(5)
	v_mfma_f32_16x16x32_bf16 v[52:55], v[136:139], v[182:185], v[52:55]
	s_waitcnt lgkmcnt(4)
	v_mfma_f32_16x16x32_bf16 v[52:55], v[140:143], v[186:189], v[52:55]
	v_mfma_f32_16x16x32_bf16 v[48:51], v[144:147], v[182:185], v[48:51]
	s_nop 0
	v_mfma_f32_16x16x32_bf16 v[48:51], v[148:151], v[186:189], v[48:51]
	s_waitcnt lgkmcnt(3)
	v_mfma_f32_16x16x32_bf16 v[44:47], v[136:139], v[190:193], v[44:47]
	s_waitcnt lgkmcnt(2)
	v_mfma_f32_16x16x32_bf16 v[44:47], v[140:143], v[194:197], v[44:47]
	v_mfma_f32_16x16x32_bf16 v[40:43], v[144:147], v[190:193], v[40:43]
	s_nop 0
	v_mfma_f32_16x16x32_bf16 v[40:43], v[148:151], v[194:197], v[40:43]
	s_waitcnt lgkmcnt(1)
	v_mfma_f32_16x16x32_bf16 v[36:39], v[136:139], v[234:237], v[36:39]
	s_waitcnt lgkmcnt(0)
	v_mfma_f32_16x16x32_bf16 v[36:39], v[140:143], v[238:241], v[36:39]
	v_mfma_f32_16x16x32_bf16 v[32:35], v[144:147], v[234:237], v[32:35]
	s_nop 0
	v_mfma_f32_16x16x32_bf16 v[32:35], v[148:151], v[238:241], v[32:35]
	s_setprio 0
	s_setprio 1
	v_mfma_f32_16x16x32_bf16 v[28:31], v[158:161], v[174:177], v[28:31]
	s_nop 0
	v_mfma_f32_16x16x32_bf16 v[28:31], v[162:165], v[178:181], v[28:31]
	v_mfma_f32_16x16x32_bf16 v[24:27], v[166:169], v[174:177], v[24:27]
	s_nop 0
	v_mfma_f32_16x16x32_bf16 v[24:27], v[170:173], v[178:181], v[24:27]
	v_mfma_f32_16x16x32_bf16 v[20:23], v[158:161], v[182:185], v[20:23]
	s_nop 0
	v_mfma_f32_16x16x32_bf16 v[20:23], v[162:165], v[186:189], v[20:23]
	v_mfma_f32_16x16x32_bf16 v[16:19], v[166:169], v[182:185], v[16:19]
	s_nop 0
	v_mfma_f32_16x16x32_bf16 v[16:19], v[170:173], v[186:189], v[16:19]
	v_mfma_f32_16x16x32_bf16 v[12:15], v[158:161], v[190:193], v[12:15]
	s_nop 0
	v_mfma_f32_16x16x32_bf16 v[12:15], v[162:165], v[194:197], v[12:15]
	v_mfma_f32_16x16x32_bf16 v[8:11], v[166:169], v[190:193], v[8:11]
	s_nop 0
	v_mfma_f32_16x16x32_bf16 v[8:11], v[170:173], v[194:197], v[8:11]
	v_mfma_f32_16x16x32_bf16 v[4:7], v[158:161], v[234:237], v[4:7]
	s_nop 0
	v_mfma_f32_16x16x32_bf16 v[4:7], v[162:165], v[238:241], v[4:7]
	v_mfma_f32_16x16x32_bf16 v[0:3], v[166:169], v[234:237], v[0:3]
	s_nop 0
	v_mfma_f32_16x16x32_bf16 v[0:3], v[170:173], v[238:241], v[0:3]
	s_setprio 0
	s_barrier
	s_bitcmp0_b32 s42, 0
	s_waitcnt vmcnt(15)
	v_mul_f32_e32 v128, 0x42800000, v128
	s_waitcnt vmcnt(14)
	v_mul_f32_e32 v132, 0x42800000, v132
	v_mul_f32_e32 v129, 0x42800000, v129
	v_mul_f32_e32 v133, 0x42800000, v133
	v_mul_f32_e32 v130, 0x42800000, v130
	v_mul_f32_e32 v134, 0x42800000, v134
	v_mul_f32_e32 v131, 0x42800000, v131
	v_mul_f32_e32 v135, 0x42800000, v135
	s_mov_b64 s[42:43], -1
	s_cbranch_scc0 .LBB0_598
	s_andn2_b64 vcc, exec, s[42:43]
	s_cbranch_vccnz .LBB0_594
	s_branch .LBB0_599

.LBB0_920:
	s_add_i32 s3, s94, 0x100
	s_add_i32 s16, s36, 0x100
	s_waitcnt lgkmcnt(4)
	s_barrier
	s_setprio 1
	v_mfma_scale_f32_16x16x128_f8f6f4 v[188:191], v[24:31], v[56:63], 0, v213, v213 op_sel_hi:[0,0,0]
	v_mfma_scale_f32_16x16x128_f8f6f4 v[184:187], v[16:23], v[56:63], 0, v213, v213 op_sel_hi:[0,0,0]
	v_mfma_scale_f32_16x16x128_f8f6f4 v[180:183], v[24:31], v[48:55], 0, v213, v213 op_sel_hi:[0,0,0]
	v_mfma_scale_f32_16x16x128_f8f6f4 v[176:179], v[16:23], v[48:55], 0, v213, v213 op_sel_hi:[0,0,0]
	v_mfma_scale_f32_16x16x128_f8f6f4 v[172:175], v[24:31], v[40:47], 0, v213, v213 op_sel_hi:[0,0,0]
	v_mfma_scale_f32_16x16x128_f8f6f4 v[168:171], v[16:23], v[40:47], 0, v213, v213 op_sel_hi:[0,0,0]
	v_mfma_scale_f32_16x16x128_f8f6f4 v[164:167], v[24:31], v[32:39], 0, v213, v213 op_sel_hi:[0,0,0]
	v_mfma_scale_f32_16x16x128_f8f6f4 v[160:163], v[16:23], v[32:39], 0, v213, v213 op_sel_hi:[0,0,0]
	s_setprio 0
	s_setprio 1
	s_waitcnt lgkmcnt(2)
	v_mfma_scale_f32_16x16x128_f8f6f4 v[156:159], v[8:15], v[56:63], 0, v213, v213 op_sel_hi:[0,0,0]
	s_waitcnt lgkmcnt(0)
	v_mfma_scale_f32_16x16x128_f8f6f4 v[152:155], v[0:7], v[56:63], 0, v213, v213 op_sel_hi:[0,0,0]
	v_mfma_scale_f32_16x16x128_f8f6f4 v[148:151], v[8:15], v[48:55], 0, v213, v213 op_sel_hi:[0,0,0]
	v_mfma_scale_f32_16x16x128_f8f6f4 v[144:147], v[0:7], v[48:55], 0, v213, v213 op_sel_hi:[0,0,0]
	v_mfma_scale_f32_16x16x128_f8f6f4 v[140:143], v[8:15], v[40:47], 0, v213, v213 op_sel_hi:[0,0,0]
	v_mfma_scale_f32_16x16x128_f8f6f4 v[136:139], v[0:7], v[40:47], 0, v213, v213 op_sel_hi:[0,0,0]
	v_mfma_scale_f32_16x16x128_f8f6f4 v[132:135], v[8:15], v[32:39], 0, v213, v213 op_sel_hi:[0,0,0]
	v_mfma_scale_f32_16x16x128_f8f6f4 v[128:131], v[0:7], v[32:39], 0, v213, v213 op_sel_hi:[0,0,0]
	s_setprio 0
	s_barrier
	s_mov_b32 m0, s71
	s_mov_b32 s10, s14
	s_mov_b32 s11, s15
	ds_read_b128 v[56:59], v216 offset:0x4000
	ds_read_b128 v[60:63], v216 offset:0x4400
	ds_read_b128 v[48:51], v216 offset:0x4800
	ds_read_b128 v[52:55], v216 offset:0x4c00
	ds_read_b128 v[40:43], v216 offset:0x5000
	ds_read_b128 v[44:47], v216 offset:0x5400
	ds_read_b128 v[32:35], v216 offset:0x5800
	ds_read_b128 v[36:39], v216 offset:0x5c00
	buffer_load_dwordx4 v215, s[8:11], s16 offen lds
	s_add_i32 s16, s36, 0x80100
	s_mov_b32 m0, s72
	s_and_b64 vcc, exec, s[4:5]
	buffer_load_dwordx4 v215, s[8:11], s16 offen lds
	s_add_i32 s16, s36, 0x8100
	s_mov_b32 m0, s73
	s_nop 0
	buffer_load_dwordx4 v215, s[8:11], s16 offen lds
	s_add_i32 s16, s36, 0x88100
	s_mov_b32 m0, s74
	s_nop 0
	buffer_load_dwordx4 v215, s[8:11], s16 offen lds
	s_mov_b32 m0, s70
	s_nop 0
	buffer_load_dwordx4 v214, s[12:15], s3 offen lds
	s_add_i32 s3, s94, 0x40100
	s_mov_b32 m0, s75
	s_nop 0
	buffer_load_dwordx4 v214, s[12:15], s3 offen lds
	s_cbranch_vccz .LBB0_938
	s_waitcnt vmcnt(54)
	s_cbranch_execnz .LBB0_923

.LBB0_923:
	s_add_i32 s3, s94, 0x180
	s_add_i32 s4, s36, 0x180
	s_waitcnt lgkmcnt(0)
	s_barrier
	s_setprio 1
	v_mfma_scale_f32_16x16x128_f8f6f4 v[124:127], v[24:31], v[56:63], 0, v213, v213 op_sel_hi:[0,0,0]
	v_mfma_scale_f32_16x16x128_f8f6f4 v[120:123], v[16:23], v[56:63], 0, v213, v213 op_sel_hi:[0,0,0]
	v_mfma_scale_f32_16x16x128_f8f6f4 v[116:119], v[24:31], v[48:55], 0, v213, v213 op_sel_hi:[0,0,0]
	v_mfma_scale_f32_16x16x128_f8f6f4 v[112:115], v[16:23], v[48:55], 0, v213, v213 op_sel_hi:[0,0,0]
	v_mfma_scale_f32_16x16x128_f8f6f4 v[108:111], v[24:31], v[40:47], 0, v213, v213 op_sel_hi:[0,0,0]
	v_mfma_scale_f32_16x16x128_f8f6f4 v[104:107], v[16:23], v[40:47], 0, v213, v213 op_sel_hi:[0,0,0]
	v_mfma_scale_f32_16x16x128_f8f6f4 v[100:103], v[24:31], v[32:39], 0, v213, v213 op_sel_hi:[0,0,0]
	v_mfma_scale_f32_16x16x128_f8f6f4 v[96:99], v[16:23], v[32:39], 0, v213, v213 op_sel_hi:[0,0,0]
	s_setprio 0
	s_setprio 1
	v_mfma_scale_f32_16x16x128_f8f6f4 v[92:95], v[8:15], v[56:63], 0, v213, v213 op_sel_hi:[0,0,0]
	v_mfma_scale_f32_16x16x128_f8f6f4 v[88:91], v[0:7], v[56:63], 0, v213, v213 op_sel_hi:[0,0,0]
	v_mfma_scale_f32_16x16x128_f8f6f4 v[84:87], v[8:15], v[48:55], 0, v213, v213 op_sel_hi:[0,0,0]
	v_mfma_scale_f32_16x16x128_f8f6f4 v[80:83], v[0:7], v[48:55], 0, v213, v213 op_sel_hi:[0,0,0]
	v_mfma_scale_f32_16x16x128_f8f6f4 v[76:79], v[8:15], v[40:47], 0, v213, v213 op_sel_hi:[0,0,0]
	v_mfma_scale_f32_16x16x128_f8f6f4 v[72:75], v[0:7], v[40:47], 0, v213, v213 op_sel_hi:[0,0,0]
	v_mfma_scale_f32_16x16x128_f8f6f4 v[68:71], v[8:15], v[32:39], 0, v213, v213 op_sel_hi:[0,0,0]
	v_mfma_scale_f32_16x16x128_f8f6f4 v[64:67], v[0:7], v[32:39], 0, v213, v213 op_sel_hi:[0,0,0]
	s_setprio 0
	s_barrier
	ds_read_b128 v[24:27], v217 offset:0x8000
	ds_read_b128 v[28:31], v217 offset:0x8400
	ds_read_b128 v[16:19], v217 offset:0x8800
	ds_read_b128 v[20:23], v217 offset:0x8c00
	s_mov_b32 m0, s76
	s_add_i32 s5, s94, 0x80100
	ds_read_b128 v[32:35], v216 offset:0x8000
	ds_read_b128 v[36:39], v216 offset:0x8400
	ds_read_b128 v[40:43], v216 offset:0x8800
	ds_read_b128 v[44:47], v216 offset:0x8c00
	ds_read_b128 v[48:51], v216 offset:0x9000
	ds_read_b128 v[52:55], v216 offset:0x9400
	ds_read_b128 v[56:59], v216 offset:0x9800
	ds_read_b128 v[60:63], v216 offset:0x9c00
	ds_read_b128 v[8:11], v217 offset:0xc000
	ds_read_b128 v[12:15], v217 offset:0xc400
	ds_read_b128 v[0:3], v217 offset:0xc800
	ds_read_b128 v[4:7], v217 offset:0xcc00
	buffer_load_dwordx4 v214, s[12:15], s5 offen lds
	s_add_i32 s5, s94, 0xc0100
	s_mov_b32 m0, s77
	s_nop 0
	buffer_load_dwordx4 v214, s[12:15], s5 offen lds
	s_waitcnt vmcnt(10)
	s_waitcnt lgkmcnt(4)
	s_barrier
	s_setprio 1
	v_mfma_scale_f32_16x16x128_f8f6f4 v[188:191], v[24:31], v[32:39], v[188:191], v213, v213 op_sel_hi:[0,0,0]
	v_mfma_scale_f32_16x16x128_f8f6f4 v[184:187], v[16:23], v[32:39], v[184:187], v213, v213 op_sel_hi:[0,0,0]
	v_mfma_scale_f32_16x16x128_f8f6f4 v[180:183], v[24:31], v[40:47], v[180:183], v213, v213 op_sel_hi:[0,0,0]
	v_mfma_scale_f32_16x16x128_f8f6f4 v[176:179], v[16:23], v[40:47], v[176:179], v213, v213 op_sel_hi:[0,0,0]
	v_mfma_scale_f32_16x16x128_f8f6f4 v[172:175], v[24:31], v[48:55], v[172:175], v213, v213 op_sel_hi:[0,0,0]
	v_mfma_scale_f32_16x16x128_f8f6f4 v[168:171], v[16:23], v[48:55], v[168:171], v213, v213 op_sel_hi:[0,0,0]
	v_mfma_scale_f32_16x16x128_f8f6f4 v[164:167], v[24:31], v[56:63], v[164:167], v213, v213 op_sel_hi:[0,0,0]
	v_mfma_scale_f32_16x16x128_f8f6f4 v[160:163], v[16:23], v[56:63], v[160:163], v213, v213 op_sel_hi:[0,0,0]
	s_setprio 0
	s_setprio 1
	s_waitcnt lgkmcnt(2)
	v_mfma_scale_f32_16x16x128_f8f6f4 v[156:159], v[8:15], v[32:39], v[156:159], v213, v213 op_sel_hi:[0,0,0]
	s_waitcnt lgkmcnt(0)
	v_mfma_scale_f32_16x16x128_f8f6f4 v[152:155], v[0:7], v[32:39], v[152:155], v213, v213 op_sel_hi:[0,0,0]
	v_mfma_scale_f32_16x16x128_f8f6f4 v[148:151], v[8:15], v[40:47], v[148:151], v213, v213 op_sel_hi:[0,0,0]
	v_mfma_scale_f32_16x16x128_f8f6f4 v[144:147], v[0:7], v[40:47], v[144:147], v213, v213 op_sel_hi:[0,0,0]
	v_mfma_scale_f32_16x16x128_f8f6f4 v[140:143], v[8:15], v[48:55], v[140:143], v213, v213 op_sel_hi:[0,0,0]
	v_mfma_scale_f32_16x16x128_f8f6f4 v[136:139], v[0:7], v[48:55], v[136:139], v213, v213 op_sel_hi:[0,0,0]
	v_mfma_scale_f32_16x16x128_f8f6f4 v[132:135], v[8:15], v[56:63], v[132:135], v213, v213 op_sel_hi:[0,0,0]
	v_mfma_scale_f32_16x16x128_f8f6f4 v[128:131], v[0:7], v[56:63], v[128:131], v213, v213 op_sel_hi:[0,0,0]
	s_setprio 0
	s_barrier
	s_mov_b32 m0, s80
	s_mov_b32 s10, s14
	s_mov_b32 s11, s15
	ds_read_b128 v[32:35], v216 offset:0xc000
	ds_read_b128 v[36:39], v216 offset:0xc400
	ds_read_b128 v[40:43], v216 offset:0xc800
	ds_read_b128 v[44:47], v216 offset:0xcc00
	ds_read_b128 v[48:51], v216 offset:0xd000
	ds_read_b128 v[52:55], v216 offset:0xd400
	ds_read_b128 v[56:59], v216 offset:0xd800
	ds_read_b128 v[60:63], v216 offset:0xdc00
	buffer_load_dwordx4 v215, s[8:11], s4 offen lds
	s_add_i32 s4, s36, 0x80180
	s_mov_b32 m0, s81
	s_nop 0
	buffer_load_dwordx4 v215, s[8:11], s4 offen lds
	s_add_i32 s4, s36, 0x8180
	s_mov_b32 m0, s84
	s_nop 0
	buffer_load_dwordx4 v215, s[8:11], s4 offen lds
	s_add_i32 s4, s36, 0x88180
	s_mov_b32 m0, s85
	s_nop 0
	buffer_load_dwordx4 v215, s[8:11], s4 offen lds
	s_mov_b32 m0, s82
	s_nop 0
	buffer_load_dwordx4 v214, s[12:15], s3 offen lds
	s_add_i32 s3, s94, 0x40180
	s_mov_b32 m0, s83
	s_nop 0
	buffer_load_dwordx4 v214, s[12:15], s3 offen lds
	s_waitcnt vmcnt(8)
	s_waitcnt lgkmcnt(0)
	s_barrier
	s_setprio 1
	v_mfma_scale_f32_16x16x128_f8f6f4 v[124:127], v[24:31], v[32:39], v[124:127], v213, v213 op_sel_hi:[0,0,0]
	v_mfma_scale_f32_16x16x128_f8f6f4 v[120:123], v[16:23], v[32:39], v[120:123], v213, v213 op_sel_hi:[0,0,0]
	v_mfma_scale_f32_16x16x128_f8f6f4 v[116:119], v[24:31], v[40:47], v[116:119], v213, v213 op_sel_hi:[0,0,0]
	v_mfma_scale_f32_16x16x128_f8f6f4 v[112:115], v[16:23], v[40:47], v[112:115], v213, v213 op_sel_hi:[0,0,0]
	v_mfma_scale_f32_16x16x128_f8f6f4 v[108:111], v[24:31], v[48:55], v[108:111], v213, v213 op_sel_hi:[0,0,0]
	v_mfma_scale_f32_16x16x128_f8f6f4 v[104:107], v[16:23], v[48:55], v[104:107], v213, v213 op_sel_hi:[0,0,0]
	v_mfma_scale_f32_16x16x128_f8f6f4 v[100:103], v[24:31], v[56:63], v[100:103], v213, v213 op_sel_hi:[0,0,0]
	v_mfma_scale_f32_16x16x128_f8f6f4 v[96:99], v[16:23], v[56:63], v[96:99], v213, v213 op_sel_hi:[0,0,0]
	s_setprio 0
	s_setprio 1
	v_mfma_scale_f32_16x16x128_f8f6f4 v[92:95], v[8:15], v[32:39], v[92:95], v213, v213 op_sel_hi:[0,0,0]
	v_mfma_scale_f32_16x16x128_f8f6f4 v[88:91], v[0:7], v[32:39], v[88:91], v213, v213 op_sel_hi:[0,0,0]
	v_mfma_scale_f32_16x16x128_f8f6f4 v[84:87], v[8:15], v[40:47], v[84:87], v213, v213 op_sel_hi:[0,0,0]
	v_mfma_scale_f32_16x16x128_f8f6f4 v[80:83], v[0:7], v[40:47], v[80:83], v213, v213 op_sel_hi:[0,0,0]
	v_mfma_scale_f32_16x16x128_f8f6f4 v[76:79], v[8:15], v[48:55], v[76:79], v213, v213 op_sel_hi:[0,0,0]
	v_mfma_scale_f32_16x16x128_f8f6f4 v[72:75], v[0:7], v[48:55], v[72:75], v213, v213 op_sel_hi:[0,0,0]
	v_mfma_scale_f32_16x16x128_f8f6f4 v[68:71], v[8:15], v[56:63], v[68:71], v213, v213 op_sel_hi:[0,0,0]
	v_mfma_scale_f32_16x16x128_f8f6f4 v[64:67], v[0:7], v[56:63], v[64:67], v213, v213 op_sel_hi:[0,0,0]
	s_setprio 0
	s_barrier
	s_waitcnt vmcnt(14)
	v_mul_f32_e32 v0, 0x42800000, v196
	v_mul_f32_e32 v1, 0x42800000, v192
	v_mul_f32_e32 v2, 0x42800000, v197
	v_mul_f32_e32 v3, 0x42800000, v193
	v_mul_f32_e32 v4, 0x42800000, v198
	v_mul_f32_e32 v5, 0x42800000, v194
	v_mul_f32_e32 v6, 0x42800000, v199
	v_mul_f32_e32 v7, 0x42800000, v195
	v_cvt_pk_fp8_f32 v202, v1, v0
	v_cvt_pk_fp8_f32 v219, v3, v2
	v_cvt_pk_fp8_f32 v220, v5, v4
	v_cvt_pk_fp8_f32 v221, v7, v6
	s_add_i32 s61, s36, 0x200
	s_mov_b32 s33, 0
	s_mov_b32 s79, s66
	s_mov_b32 s90, s68
	s_branch .LBB0_926

.LBB0_926:
	v_mov_b32_e32 v40, v202
	v_mov_b32_e32 v41, v219
	v_mov_b32_e32 v42, v220
	v_mov_b32_e32 v43, v221
	s_add_i32 s4, s94, s33
	s_mov_b32 s64, s90
	s_add_i32 s90, s90, 1
	s_add_i32 s3, s4, 0x200
	s_add_i32 s5, s61, s33
	ds_read_b128 v[24:27], v217 offset:0
	ds_read_b128 v[28:31], v217 offset:0x400
	ds_read_b128 v[16:19], v217 offset:0x800
	ds_read_b128 v[20:23], v217 offset:0xc00
	s_cmpk_eq_i32 s33, 0xe00
	s_cselect_b32 s65, s60, s3
	s_cselect_b32 s16, s95, s5
	s_add_i32 s3, s65, 0x80
	s_mov_b32 m0, s86
	s_add_i32 s5, s4, 0x80180
	ds_read_b128 v[46:49], v216 offset:0
	ds_read_b128 v[50:53], v216 offset:0x400
	ds_read_b128 v[54:57], v216 offset:0x800
	ds_read_b128 v[58:61], v216 offset:0xc00
	ds_read_b128 v[192:195], v216 offset:0x1000
	ds_read_b128 v[196:199], v216 offset:0x1400
	ds_read_b128 v[220:223], v216 offset:0x1800
	ds_read_b128 v[224:227], v216 offset:0x1c00
	ds_read_b128 v[8:11], v217 offset:0x4000
	ds_read_b128 v[12:15], v217 offset:0x4400
	ds_read_b128 v[0:3], v217 offset:0x4800
	ds_read_b128 v[4:7], v217 offset:0x4c00
	buffer_load_dwordx4 v214, s[12:15], s5 offen lds
	s_add_i32 s4, s4, 0xc0180
	s_mov_b32 m0, s89
	s_add_i32 s17, s16, 0x80
	buffer_load_dwordx4 v214, s[12:15], s4 offen lds
	s_lshr_b32 s4, s90, 2
	s_mul_i32 s5, s4, s34
	s_add_i32 s36, s5, s2
	s_cmp_lt_i32 s4, s47
	s_cselect_b64 s[4:5], -1, 0
	s_and_b64 s[62:63], s[4:5], exec
	s_cselect_b32 s67, s36, 0
	s_ashr_i32 s62, s67, 7
	s_bfe_u32 s36, s90, 0x10001
	s_ashr_i32 s63, s62, 31
	s_or_b32 s78, s36, s87
	s_bfe_u32 s36, s67, 0x20005
	s_lshl_b64 vcc, s[62:63], 23
	s_add_u32 vcc_lo, s28, vcc_lo
	s_addc_u32 vcc_hi, s29, vcc_hi
	s_lshl_b32 s38, s36, 21
	s_add_u32 s38, vcc_lo, s38
	s_addc_u32 s39, vcc_hi, 0
	s_lshl_b32 s67, s67, 7
	s_and_b32 s67, s67, 0xf80
	s_lshl_b32 vcc_lo, s67, 2
	s_add_u32 vcc_lo, s38, vcc_lo
	v_and_or_b32 v202, s79, 2, v200
	s_addc_u32 vcc_hi, s39, 0
	v_lshl_or_b32 v44, s78, 5, v218
	v_lshlrev_b64 v[32:33], 14, v[202:203]
	v_lshl_add_u64 v[32:33], vcc, 0, v[32:33]
	v_lshlrev_b32_e32 v202, 2, v44
	v_lshl_add_u64 v[32:33], v[32:33], 0, v[202:203]
	s_movk_i32 s38, 0x4000
	v_add_co_u32_e32 v36, vcc, s38, v32
	s_nop 1
	v_addc_co_u32_e32 v37, vcc, 0, v33, vcc
	global_load_dwordx4 v[32:35], v[32:33], off nt
	s_nop 0
	global_load_dwordx4 v[36:39], v[36:37], off nt
	s_waitcnt vmcnt(10)
	s_waitcnt lgkmcnt(4)
	s_barrier
	s_setprio 1
	v_mfma_scale_f32_16x16x128_f8f6f4 v[188:191], v[24:31], v[46:53], v[188:191], v213, v213 op_sel_hi:[0,0,0]
	v_mfma_scale_f32_16x16x128_f8f6f4 v[184:187], v[16:23], v[46:53], v[184:187], v213, v213 op_sel_hi:[0,0,0]
	v_mfma_scale_f32_16x16x128_f8f6f4 v[180:183], v[24:31], v[54:61], v[180:183], v213, v213 op_sel_hi:[0,0,0]
	v_mfma_scale_f32_16x16x128_f8f6f4 v[176:179], v[16:23], v[54:61], v[176:179], v213, v213 op_sel_hi:[0,0,0]
	v_mfma_scale_f32_16x16x128_f8f6f4 v[172:175], v[24:31], v[192:199], v[172:175], v213, v213 op_sel_hi:[0,0,0]
	v_mfma_scale_f32_16x16x128_f8f6f4 v[168:171], v[16:23], v[192:199], v[168:171], v213, v213 op_sel_hi:[0,0,0]
	v_mfma_scale_f32_16x16x128_f8f6f4 v[164:167], v[24:31], v[220:227], v[164:167], v213, v213 op_sel_hi:[0,0,0]
	v_mfma_scale_f32_16x16x128_f8f6f4 v[160:163], v[16:23], v[220:227], v[160:163], v213, v213 op_sel_hi:[0,0,0]
	s_setprio 0
	s_setprio 1
	s_waitcnt lgkmcnt(2)
	v_mfma_scale_f32_16x16x128_f8f6f4 v[156:159], v[8:15], v[46:53], v[156:159], v213, v213 op_sel_hi:[0,0,0]
	s_waitcnt lgkmcnt(0)
	v_mfma_scale_f32_16x16x128_f8f6f4 v[152:155], v[0:7], v[46:53], v[152:155], v213, v213 op_sel_hi:[0,0,0]
	v_mfma_scale_f32_16x16x128_f8f6f4 v[148:151], v[8:15], v[54:61], v[148:151], v213, v213 op_sel_hi:[0,0,0]
	v_mfma_scale_f32_16x16x128_f8f6f4 v[144:147], v[0:7], v[54:61], v[144:147], v213, v213 op_sel_hi:[0,0,0]
	v_mfma_scale_f32_16x16x128_f8f6f4 v[140:143], v[8:15], v[192:199], v[140:143], v213, v213 op_sel_hi:[0,0,0]
	v_mfma_scale_f32_16x16x128_f8f6f4 v[136:139], v[0:7], v[192:199], v[136:139], v213, v213 op_sel_hi:[0,0,0]
	v_mfma_scale_f32_16x16x128_f8f6f4 v[132:135], v[8:15], v[220:227], v[132:135], v213, v213 op_sel_hi:[0,0,0]
	v_mfma_scale_f32_16x16x128_f8f6f4 v[128:131], v[0:7], v[220:227], v[128:131], v213, v213 op_sel_hi:[0,0,0]
	s_setprio 0
	s_barrier
	s_mov_b32 m0, s71
	ds_read_b128 v[46:49], v216 offset:0x4000
	ds_read_b128 v[50:53], v216 offset:0x4400
	ds_read_b128 v[54:57], v216 offset:0x4800
	ds_read_b128 v[58:61], v216 offset:0x4c00
	ds_read_b128 v[192:195], v216 offset:0x5000
	ds_read_b128 v[196:199], v216 offset:0x5400
	ds_read_b128 v[220:223], v216 offset:0x5800
	ds_read_b128 v[224:227], v216 offset:0x5c00
	s_nop 0
	buffer_load_dwordx4 v215, s[8:11], s16 offen lds
	s_add_i32 s38, s16, 0x80000
	s_mov_b32 m0, s72
	s_nop 0
	buffer_load_dwordx4 v215, s[8:11], s38 offen lds
	s_add_i32 s38, s16, 0x8000
	s_mov_b32 m0, s73
	s_nop 0
	buffer_load_dwordx4 v215, s[8:11], s38 offen lds
	s_add_i32 s38, s16, 0x88000
	s_mov_b32 m0, s74
	s_nop 0
	buffer_load_dwordx4 v215, s[8:11], s38 offen lds
	s_mov_b32 m0, s70
	s_add_i32 s38, s65, 0x40000
	buffer_load_dwordx4 v214, s[12:15], s65 offen lds
	s_mov_b32 m0, s75
	s_nop 0
	buffer_load_dwordx4 v214, s[12:15], s38 offen lds
	s_waitcnt vmcnt(10)
	s_waitcnt lgkmcnt(0)
	s_barrier
	s_setprio 1
	v_mfma_scale_f32_16x16x128_f8f6f4 v[124:127], v[24:31], v[46:53], v[124:127], v213, v213 op_sel_hi:[0,0,0]
	v_mfma_scale_f32_16x16x128_f8f6f4 v[120:123], v[16:23], v[46:53], v[120:123], v213, v213 op_sel_hi:[0,0,0]
	v_mfma_scale_f32_16x16x128_f8f6f4 v[116:119], v[24:31], v[54:61], v[116:119], v213, v213 op_sel_hi:[0,0,0]
	v_mfma_scale_f32_16x16x128_f8f6f4 v[112:115], v[16:23], v[54:61], v[112:115], v213, v213 op_sel_hi:[0,0,0]
	v_mfma_scale_f32_16x16x128_f8f6f4 v[108:111], v[24:31], v[192:199], v[108:111], v213, v213 op_sel_hi:[0,0,0]
	v_mfma_scale_f32_16x16x128_f8f6f4 v[104:107], v[16:23], v[192:199], v[104:107], v213, v213 op_sel_hi:[0,0,0]
	v_mfma_scale_f32_16x16x128_f8f6f4 v[100:103], v[24:31], v[220:227], v[100:103], v213, v213 op_sel_hi:[0,0,0]
	v_mfma_scale_f32_16x16x128_f8f6f4 v[96:99], v[16:23], v[220:227], v[96:99], v213, v213 op_sel_hi:[0,0,0]
	s_setprio 0
	s_setprio 1
	v_mfma_scale_f32_16x16x128_f8f6f4 v[92:95], v[8:15], v[46:53], v[92:95], v213, v213 op_sel_hi:[0,0,0]
	v_mfma_scale_f32_16x16x128_f8f6f4 v[88:91], v[0:7], v[46:53], v[88:91], v213, v213 op_sel_hi:[0,0,0]
	v_mfma_scale_f32_16x16x128_f8f6f4 v[84:87], v[8:15], v[54:61], v[84:87], v213, v213 op_sel_hi:[0,0,0]
	v_mfma_scale_f32_16x16x128_f8f6f4 v[80:83], v[0:7], v[54:61], v[80:83], v213, v213 op_sel_hi:[0,0,0]
	v_mfma_scale_f32_16x16x128_f8f6f4 v[76:79], v[8:15], v[192:199], v[76:79], v213, v213 op_sel_hi:[0,0,0]
	v_mfma_scale_f32_16x16x128_f8f6f4 v[72:75], v[0:7], v[192:199], v[72:75], v213, v213 op_sel_hi:[0,0,0]
	v_mfma_scale_f32_16x16x128_f8f6f4 v[68:71], v[8:15], v[220:227], v[68:71], v213, v213 op_sel_hi:[0,0,0]
	v_mfma_scale_f32_16x16x128_f8f6f4 v[64:67], v[0:7], v[220:227], v[64:67], v213, v213 op_sel_hi:[0,0,0]
	s_setprio 0
	s_barrier
	ds_read_b128 v[16:19], v217 offset:0x8000
	ds_read_b128 v[20:23], v217 offset:0x8400
	ds_read_b128 v[24:27], v217 offset:0x8800
	ds_read_b128 v[28:31], v217 offset:0x8c00
	s_mov_b32 m0, s76
	s_add_i32 s38, s65, 0x80000
	ds_read_b128 v[46:49], v216 offset:0x8000
	ds_read_b128 v[50:53], v216 offset:0x8400
	ds_read_b128 v[54:57], v216 offset:0x8800
	ds_read_b128 v[58:61], v216 offset:0x8c00
	ds_read_b128 v[192:195], v216 offset:0x9000
	ds_read_b128 v[196:199], v216 offset:0x9400
	ds_read_b128 v[220:223], v216 offset:0x9800
	ds_read_b128 v[224:227], v216 offset:0x9c00
	ds_read_b128 v[8:11], v217 offset:0xc000
	ds_read_b128 v[12:15], v217 offset:0xc400
	ds_read_b128 v[0:3], v217 offset:0xc800
	ds_read_b128 v[4:7], v217 offset:0xcc00
	buffer_load_dwordx4 v214, s[12:15], s38 offen lds
	s_add_i32 s38, s65, 0xc0000
	s_mov_b32 m0, s77
	s_nop 0
	buffer_load_dwordx4 v214, s[12:15], s38 offen lds
	s_waitcnt vmcnt(10)
	s_waitcnt lgkmcnt(4)
	s_barrier
	s_setprio 1
	v_mfma_scale_f32_16x16x128_f8f6f4 v[188:191], v[16:23], v[46:53], v[188:191], v213, v213 op_sel_hi:[0,0,0]
	v_mfma_scale_f32_16x16x128_f8f6f4 v[184:187], v[24:31], v[46:53], v[184:187], v213, v213 op_sel_hi:[0,0,0]
	v_mfma_scale_f32_16x16x128_f8f6f4 v[180:183], v[16:23], v[54:61], v[180:183], v213, v213 op_sel_hi:[0,0,0]
	v_mfma_scale_f32_16x16x128_f8f6f4 v[176:179], v[24:31], v[54:61], v[176:179], v213, v213 op_sel_hi:[0,0,0]
	v_mfma_scale_f32_16x16x128_f8f6f4 v[172:175], v[16:23], v[192:199], v[172:175], v213, v213 op_sel_hi:[0,0,0]
	v_mfma_scale_f32_16x16x128_f8f6f4 v[168:171], v[24:31], v[192:199], v[168:171], v213, v213 op_sel_hi:[0,0,0]
	v_mfma_scale_f32_16x16x128_f8f6f4 v[164:167], v[16:23], v[220:227], v[164:167], v213, v213 op_sel_hi:[0,0,0]
	v_mfma_scale_f32_16x16x128_f8f6f4 v[160:163], v[24:31], v[220:227], v[160:163], v213, v213 op_sel_hi:[0,0,0]
	s_setprio 0
	s_setprio 1
	s_waitcnt lgkmcnt(2)
	v_mfma_scale_f32_16x16x128_f8f6f4 v[156:159], v[8:15], v[46:53], v[156:159], v213, v213 op_sel_hi:[0,0,0]
	s_waitcnt lgkmcnt(0)
	v_mfma_scale_f32_16x16x128_f8f6f4 v[152:155], v[0:7], v[46:53], v[152:155], v213, v213 op_sel_hi:[0,0,0]
	v_mfma_scale_f32_16x16x128_f8f6f4 v[148:151], v[8:15], v[54:61], v[148:151], v213, v213 op_sel_hi:[0,0,0]
	v_mfma_scale_f32_16x16x128_f8f6f4 v[144:147], v[0:7], v[54:61], v[144:147], v213, v213 op_sel_hi:[0,0,0]
	v_mfma_scale_f32_16x16x128_f8f6f4 v[140:143], v[8:15], v[192:199], v[140:143], v213, v213 op_sel_hi:[0,0,0]
	v_mfma_scale_f32_16x16x128_f8f6f4 v[136:139], v[0:7], v[192:199], v[136:139], v213, v213 op_sel_hi:[0,0,0]
	v_mfma_scale_f32_16x16x128_f8f6f4 v[132:135], v[8:15], v[220:227], v[132:135], v213, v213 op_sel_hi:[0,0,0]
	v_mfma_scale_f32_16x16x128_f8f6f4 v[128:131], v[0:7], v[220:227], v[128:131], v213, v213 op_sel_hi:[0,0,0]
	s_setprio 0
	s_barrier
	s_mov_b32 m0, s80
	ds_read_b128 v[46:49], v216 offset:0xc000
	ds_read_b128 v[50:53], v216 offset:0xc400
	ds_read_b128 v[54:57], v216 offset:0xc800
	ds_read_b128 v[58:61], v216 offset:0xcc00
	ds_read_b128 v[192:195], v216 offset:0xd000
	ds_read_b128 v[196:199], v216 offset:0xd400
	ds_read_b128 v[220:223], v216 offset:0xd800
	ds_read_b128 v[224:227], v216 offset:0xdc00
	s_nop 0
	buffer_load_dwordx4 v215, s[8:11], s17 offen lds
	s_add_i32 s17, s16, 0x80080
	s_mov_b32 m0, s81
	s_add_i32 s65, s65, 0x40080
	buffer_load_dwordx4 v215, s[8:11], s17 offen lds
	s_add_i32 s17, s16, 0x8080
	s_mov_b32 m0, s84
	s_add_i32 s16, s16, 0x88080
	buffer_load_dwordx4 v215, s[8:11], s17 offen lds
	s_mov_b32 m0, s85
	s_nop 0
	buffer_load_dwordx4 v215, s[8:11], s16 offen lds
	s_mov_b32 m0, s82
	s_nop 0
	buffer_load_dwordx4 v214, s[12:15], s3 offen lds
	s_mov_b32 m0, s83
	s_nop 0
	buffer_load_dwordx4 v214, s[12:15], s65 offen lds
	s_waitcnt vmcnt(8)
	s_waitcnt lgkmcnt(0)
	s_barrier
	s_setprio 1
	v_mfma_scale_f32_16x16x128_f8f6f4 v[124:127], v[16:23], v[46:53], v[124:127], v213, v213 op_sel_hi:[0,0,0]
	v_mfma_scale_f32_16x16x128_f8f6f4 v[120:123], v[24:31], v[46:53], v[120:123], v213, v213 op_sel_hi:[0,0,0]
	v_mfma_scale_f32_16x16x128_f8f6f4 v[116:119], v[16:23], v[54:61], v[116:119], v213, v213 op_sel_hi:[0,0,0]
	v_mfma_scale_f32_16x16x128_f8f6f4 v[112:115], v[24:31], v[54:61], v[112:115], v213, v213 op_sel_hi:[0,0,0]
	v_mfma_scale_f32_16x16x128_f8f6f4 v[108:111], v[16:23], v[192:199], v[108:111], v213, v213 op_sel_hi:[0,0,0]
	v_mfma_scale_f32_16x16x128_f8f6f4 v[104:107], v[24:31], v[192:199], v[104:107], v213, v213 op_sel_hi:[0,0,0]
	v_mfma_scale_f32_16x16x128_f8f6f4 v[100:103], v[16:23], v[220:227], v[100:103], v213, v213 op_sel_hi:[0,0,0]
	v_mfma_scale_f32_16x16x128_f8f6f4 v[96:99], v[24:31], v[220:227], v[96:99], v213, v213 op_sel_hi:[0,0,0]
	s_setprio 0
	s_setprio 1
	v_mfma_scale_f32_16x16x128_f8f6f4 v[92:95], v[8:15], v[46:53], v[92:95], v213, v213 op_sel_hi:[0,0,0]
	v_mfma_scale_f32_16x16x128_f8f6f4 v[88:91], v[0:7], v[46:53], v[88:91], v213, v213 op_sel_hi:[0,0,0]
	v_mfma_scale_f32_16x16x128_f8f6f4 v[84:87], v[8:15], v[54:61], v[84:87], v213, v213 op_sel_hi:[0,0,0]
	v_mfma_scale_f32_16x16x128_f8f6f4 v[80:83], v[0:7], v[54:61], v[80:83], v213, v213 op_sel_hi:[0,0,0]
	v_mfma_scale_f32_16x16x128_f8f6f4 v[76:79], v[8:15], v[192:199], v[76:79], v213, v213 op_sel_hi:[0,0,0]
	v_mfma_scale_f32_16x16x128_f8f6f4 v[72:75], v[0:7], v[192:199], v[72:75], v213, v213 op_sel_hi:[0,0,0]
	v_mfma_scale_f32_16x16x128_f8f6f4 v[68:71], v[8:15], v[220:227], v[68:71], v213, v213 op_sel_hi:[0,0,0]
	v_mfma_scale_f32_16x16x128_f8f6f4 v[64:67], v[0:7], v[220:227], v[64:67], v213, v213 op_sel_hi:[0,0,0]
	s_setprio 0
	s_barrier
	s_bitcmp0_b32 s64, 0
	s_waitcnt vmcnt(15)
	v_mul_f32_e32 v0, 0x42800000, v32
	s_waitcnt vmcnt(14)
	v_mul_f32_e32 v4, 0x42800000, v36
	v_mul_f32_e32 v1, 0x42800000, v33
	v_mul_f32_e32 v5, 0x42800000, v37
	v_mul_f32_e32 v2, 0x42800000, v34
	v_mul_f32_e32 v6, 0x42800000, v38
	v_mul_f32_e32 v3, 0x42800000, v35
	v_mul_f32_e32 v7, 0x42800000, v39
	s_mov_b64 s[64:65], -1
	s_cbranch_scc0 .LBB0_929
	s_andn2_b64 vcc, exec, s[64:65]
	s_cbranch_vccnz .LBB0_925
	s_branch .LBB0_930

.LBB0_1228:
	s_add_i32 s28, s61, 0x180
	s_add_i32 s29, s60, 0x180
	s_waitcnt lgkmcnt(0)
	s_barrier
	s_setprio 1
	v_mfma_scale_f32_16x16x128_f8f6f4 v[128:131], v[24:31], v[56:63], 0, v201, v201 op_sel_hi:[0,0,0]
	v_mfma_scale_f32_16x16x128_f8f6f4 v[124:127], v[16:23], v[56:63], 0, v201, v201 op_sel_hi:[0,0,0]
	v_mfma_scale_f32_16x16x128_f8f6f4 v[120:123], v[24:31], v[48:55], 0, v201, v201 op_sel_hi:[0,0,0]
	v_mfma_scale_f32_16x16x128_f8f6f4 v[116:119], v[16:23], v[48:55], 0, v201, v201 op_sel_hi:[0,0,0]
	v_mfma_scale_f32_16x16x128_f8f6f4 v[112:115], v[24:31], v[40:47], 0, v201, v201 op_sel_hi:[0,0,0]
	v_mfma_scale_f32_16x16x128_f8f6f4 v[108:111], v[16:23], v[40:47], 0, v201, v201 op_sel_hi:[0,0,0]
	v_mfma_scale_f32_16x16x128_f8f6f4 v[104:107], v[24:31], v[32:39], 0, v201, v201 op_sel_hi:[0,0,0]
	v_mfma_scale_f32_16x16x128_f8f6f4 v[100:103], v[16:23], v[32:39], 0, v201, v201 op_sel_hi:[0,0,0]
	s_setprio 0
	s_setprio 1
	v_mfma_scale_f32_16x16x128_f8f6f4 v[96:99], v[8:15], v[56:63], 0, v201, v201 op_sel_hi:[0,0,0]
	v_mfma_scale_f32_16x16x128_f8f6f4 v[92:95], v[0:7], v[56:63], 0, v201, v201 op_sel_hi:[0,0,0]
	v_mfma_scale_f32_16x16x128_f8f6f4 v[88:91], v[8:15], v[48:55], 0, v201, v201 op_sel_hi:[0,0,0]
	v_mfma_scale_f32_16x16x128_f8f6f4 v[84:87], v[0:7], v[48:55], 0, v201, v201 op_sel_hi:[0,0,0]
	v_mfma_scale_f32_16x16x128_f8f6f4 v[80:83], v[8:15], v[40:47], 0, v201, v201 op_sel_hi:[0,0,0]
	v_mfma_scale_f32_16x16x128_f8f6f4 v[76:79], v[0:7], v[40:47], 0, v201, v201 op_sel_hi:[0,0,0]
	v_mfma_scale_f32_16x16x128_f8f6f4 v[72:75], v[8:15], v[32:39], 0, v201, v201 op_sel_hi:[0,0,0]
	v_mfma_scale_f32_16x16x128_f8f6f4 v[68:71], v[0:7], v[32:39], 0, v201, v201 op_sel_hi:[0,0,0]
	s_setprio 0
	s_barrier
	ds_read_b128 v[24:27], v205 offset:0x8000
	ds_read_b128 v[28:31], v205 offset:0x8400
	ds_read_b128 v[16:19], v205 offset:0x8800
	ds_read_b128 v[20:23], v205 offset:0x8c00
	s_mov_b32 m0, s44
	ds_read_b128 v[32:35], v204 offset:0x8000
	ds_read_b128 v[36:39], v204 offset:0x8400
	ds_read_b128 v[40:43], v204 offset:0x8800
	ds_read_b128 v[44:47], v204 offset:0x8c00
	ds_read_b128 v[48:51], v204 offset:0x9000
	ds_read_b128 v[52:55], v204 offset:0x9400
	ds_read_b128 v[56:59], v204 offset:0x9800
	ds_read_b128 v[60:63], v204 offset:0x9c00
	ds_read_b128 v[8:11], v205 offset:0xc000
	ds_read_b128 v[12:15], v205 offset:0xc400
	ds_read_b128 v[0:3], v205 offset:0xc800
	ds_read_b128 v[4:7], v205 offset:0xcc00
	s_nop 0
	buffer_load_dwordx4 v216, s[4:7], s33 offen lds
	s_mov_b32 m0, s45
	s_nop 0
	buffer_load_dwordx4 v215, s[4:7], s33 offen lds
	s_waitcnt vmcnt(8)
	s_waitcnt lgkmcnt(4)
	s_barrier
	s_setprio 1
	v_mfma_scale_f32_16x16x128_f8f6f4 v[192:195], v[24:31], v[32:39], v[192:195], v201, v201 op_sel_hi:[0,0,0]
	v_mfma_scale_f32_16x16x128_f8f6f4 v[188:191], v[16:23], v[32:39], v[188:191], v201, v201 op_sel_hi:[0,0,0]
	v_mfma_scale_f32_16x16x128_f8f6f4 v[184:187], v[24:31], v[40:47], v[184:187], v201, v201 op_sel_hi:[0,0,0]
	v_mfma_scale_f32_16x16x128_f8f6f4 v[180:183], v[16:23], v[40:47], v[180:183], v201, v201 op_sel_hi:[0,0,0]
	v_mfma_scale_f32_16x16x128_f8f6f4 v[176:179], v[24:31], v[48:55], v[176:179], v201, v201 op_sel_hi:[0,0,0]
	v_mfma_scale_f32_16x16x128_f8f6f4 v[172:175], v[16:23], v[48:55], v[172:175], v201, v201 op_sel_hi:[0,0,0]
	v_mfma_scale_f32_16x16x128_f8f6f4 v[168:171], v[24:31], v[56:63], v[168:171], v201, v201 op_sel_hi:[0,0,0]
	v_mfma_scale_f32_16x16x128_f8f6f4 v[164:167], v[16:23], v[56:63], v[164:167], v201, v201 op_sel_hi:[0,0,0]
	s_setprio 0
	s_setprio 1
	s_waitcnt lgkmcnt(2)
	v_mfma_scale_f32_16x16x128_f8f6f4 v[160:163], v[8:15], v[32:39], v[160:163], v201, v201 op_sel_hi:[0,0,0]
	s_waitcnt lgkmcnt(0)
	v_mfma_scale_f32_16x16x128_f8f6f4 v[156:159], v[0:7], v[32:39], v[156:159], v201, v201 op_sel_hi:[0,0,0]
	v_mfma_scale_f32_16x16x128_f8f6f4 v[152:155], v[8:15], v[40:47], v[152:155], v201, v201 op_sel_hi:[0,0,0]
	v_mfma_scale_f32_16x16x128_f8f6f4 v[148:151], v[0:7], v[40:47], v[148:151], v201, v201 op_sel_hi:[0,0,0]
	v_mfma_scale_f32_16x16x128_f8f6f4 v[144:147], v[8:15], v[48:55], v[144:147], v201, v201 op_sel_hi:[0,0,0]
	v_mfma_scale_f32_16x16x128_f8f6f4 v[140:143], v[0:7], v[48:55], v[140:143], v201, v201 op_sel_hi:[0,0,0]
	v_mfma_scale_f32_16x16x128_f8f6f4 v[136:139], v[8:15], v[56:63], v[136:139], v201, v201 op_sel_hi:[0,0,0]
	v_mfma_scale_f32_16x16x128_f8f6f4 v[132:135], v[0:7], v[56:63], v[132:135], v201, v201 op_sel_hi:[0,0,0]
	s_setprio 0
	s_barrier
	s_mov_b32 m0, s48
	s_mov_b32 s10, s6
	s_mov_b32 s11, s7
	ds_read_b128 v[32:35], v204 offset:0xc000
	ds_read_b128 v[36:39], v204 offset:0xc400
	ds_read_b128 v[40:43], v204 offset:0xc800
	ds_read_b128 v[44:47], v204 offset:0xcc00
	ds_read_b128 v[48:51], v204 offset:0xd000
	ds_read_b128 v[52:55], v204 offset:0xd400
	ds_read_b128 v[56:59], v204 offset:0xd800
	ds_read_b128 v[60:63], v204 offset:0xdc00
	buffer_load_dwordx4 v203, s[8:11], s29 offen lds
	s_add_i32 s29, s60, 0x80180
	s_mov_b32 m0, s49
	s_nop 0
	buffer_load_dwordx4 v203, s[8:11], s29 offen lds
	s_add_i32 s29, s60, 0x8180
	s_mov_b32 m0, s62
	s_nop 0
	buffer_load_dwordx4 v203, s[8:11], s29 offen lds
	s_add_i32 s29, s60, 0x88180
	s_mov_b32 m0, s63
	s_nop 0
	buffer_load_dwordx4 v203, s[8:11], s29 offen lds
	s_mov_b32 m0, s50
	s_nop 0
	buffer_load_dwordx4 v214, s[4:7], s28 offen lds
	s_mov_b32 m0, s51
	s_nop 0
	buffer_load_dwordx4 v217, s[4:7], s28 offen lds
	s_waitcnt vmcnt(8)
	s_waitcnt lgkmcnt(0)
	s_barrier
	s_setprio 1
	v_mfma_scale_f32_16x16x128_f8f6f4 v[128:131], v[24:31], v[32:39], v[128:131], v201, v201 op_sel_hi:[0,0,0]
	v_mfma_scale_f32_16x16x128_f8f6f4 v[124:127], v[16:23], v[32:39], v[124:127], v201, v201 op_sel_hi:[0,0,0]
	v_mfma_scale_f32_16x16x128_f8f6f4 v[120:123], v[24:31], v[40:47], v[120:123], v201, v201 op_sel_hi:[0,0,0]
	v_mfma_scale_f32_16x16x128_f8f6f4 v[116:119], v[16:23], v[40:47], v[116:119], v201, v201 op_sel_hi:[0,0,0]
	v_mfma_scale_f32_16x16x128_f8f6f4 v[112:115], v[24:31], v[48:55], v[112:115], v201, v201 op_sel_hi:[0,0,0]
	v_mfma_scale_f32_16x16x128_f8f6f4 v[108:111], v[16:23], v[48:55], v[108:111], v201, v201 op_sel_hi:[0,0,0]
	v_mfma_scale_f32_16x16x128_f8f6f4 v[104:107], v[24:31], v[56:63], v[104:107], v201, v201 op_sel_hi:[0,0,0]
	v_mfma_scale_f32_16x16x128_f8f6f4 v[100:103], v[16:23], v[56:63], v[100:103], v201, v201 op_sel_hi:[0,0,0]
	s_setprio 0
	s_setprio 1
	v_mfma_scale_f32_16x16x128_f8f6f4 v[96:99], v[8:15], v[32:39], v[96:99], v201, v201 op_sel_hi:[0,0,0]
	v_mfma_scale_f32_16x16x128_f8f6f4 v[92:95], v[0:7], v[32:39], v[92:95], v201, v201 op_sel_hi:[0,0,0]
	v_mfma_scale_f32_16x16x128_f8f6f4 v[88:91], v[8:15], v[40:47], v[88:91], v201, v201 op_sel_hi:[0,0,0]
	v_mfma_scale_f32_16x16x128_f8f6f4 v[84:87], v[0:7], v[40:47], v[84:87], v201, v201 op_sel_hi:[0,0,0]
	v_mfma_scale_f32_16x16x128_f8f6f4 v[80:83], v[8:15], v[48:55], v[80:83], v201, v201 op_sel_hi:[0,0,0]
	v_mfma_scale_f32_16x16x128_f8f6f4 v[76:79], v[0:7], v[48:55], v[76:79], v201, v201 op_sel_hi:[0,0,0]
	v_mfma_scale_f32_16x16x128_f8f6f4 v[72:75], v[8:15], v[56:63], v[72:75], v201, v201 op_sel_hi:[0,0,0]
	v_mfma_scale_f32_16x16x128_f8f6f4 v[68:71], v[0:7], v[56:63], v[68:71], v201, v201 op_sel_hi:[0,0,0]
	s_setprio 0
	s_barrier
	s_waitcnt vmcnt(16)
	v_mbcnt_lo_u32_b32 v0, -1, 0
	v_mbcnt_hi_u32_b32 v0, -1, v0
	s_add_i32 s29, s60, 0x200
	v_lshl_add_u32 v0, v0, 4, s37
	v_ashrrev_i32_e32 v1, 31, v0
	v_lshrrev_b32_e32 v1, 22, v1
	v_add_u32_e32 v1, v0, v1
	v_ashrrev_i32_e32 v1, 10, v1
	v_mul_i32_i24_e32 v2, 0x400, v1
	v_sub_u32_e32 v2, v0, v2
	v_lshrrev_b32_e32 v3, 4, v2
	v_bitop3_b32 v3, v3, v2, 32 bitop3:0x6c
	v_ashrrev_i32_e32 v2, 31, v2
	v_lshrrev_b32_e32 v2, 26, v2
	v_add_u32_e32 v2, v3, v2
	v_and_b32_e32 v2, 0xc0, v2
	v_add_u32_e32 v0, 0x2000, v0
	v_sub_u32_e32 v2, v3, v2
	v_ashrrev_i32_e32 v3, 31, v0
	v_lshrrev_b32_e32 v3, 22, v3
	v_add_u32_e32 v3, v0, v3
	v_ashrrev_i32_e32 v3, 10, v3
	v_mul_i32_i24_e32 v4, 0x400, v3
	v_sub_u32_e32 v0, v0, v4
	v_lshrrev_b32_e32 v4, 4, v0
	v_bitop3_b32 v4, v4, v0, 32 bitop3:0x6c
	v_ashrrev_i32_e32 v0, 31, v0
	v_lshrrev_b32_e32 v0, 26, v0
	v_add_u32_e32 v0, v4, v0
	v_and_b32_e32 v0, 0xffc0, v0
	v_sub_u32_e32 v0, v4, v0
	v_lshrrev_b16_e32 v4, 7, v0
	v_and_b32_e32 v4, 1, v4
	v_add_u16_e32 v0, v0, v4
	v_lshlrev_b32_e32 v1, 5, v1
	v_ashrrev_i16_sdwa v2, v202, sext(v2) dst_sel:DWORD dst_unused:UNUSED_PAD src0_sel:DWORD src1_sel:BYTE_0
	v_lshlrev_b32_e32 v3, 5, v3
	v_ashrrev_i16_sdwa v0, v202, sext(v0) dst_sel:DWORD dst_unused:UNUSED_PAD src0_sel:DWORD src1_sel:BYTE_0
	v_and_b32_e32 v1, 32, v1
	v_bfe_i32 v2, v2, 0, 16
	v_and_b32_e32 v3, 32, v3
	v_bfe_i32 v0, v0, 0, 16
	v_add_lshl_u32 v1, v1, v2, 1
	v_add_lshl_u32 v0, v3, v0, 1
	v_lshl_add_u32 v32, v231, 12, v1
	v_lshl_add_u32 v33, v228, 12, v0
	v_lshl_add_u32 v34, v229, 12, v1
	v_lshl_add_u32 v35, v230, 12, v0
	s_mov_b32 s33, 0
.LBB0_1229:
	s_add_i32 s66, s28, 0x80
	s_cmp_eq_u32 s33, 28
	s_cselect_b64 vcc, -1, 0
	ds_read_b128 v[16:19], v205 offset:0
	ds_read_b128 v[20:23], v205 offset:0x400
	ds_read_b128 v[24:27], v205 offset:0x800
	ds_read_b128 v[28:31], v205 offset:0xc00
	s_and_b64 s[60:61], vcc, exec
	s_cselect_b32 s66, s72, s66
	s_cselect_b32 s61, s73, s29
	s_add_i32 s60, s66, 0x80
	s_mov_b32 m0, s65
	ds_read_b128 v[36:39], v204 offset:0
	ds_read_b128 v[40:43], v204 offset:0x400
	ds_read_b128 v[44:47], v204 offset:0x800
	ds_read_b128 v[48:51], v204 offset:0xc00
	ds_read_b128 v[52:55], v204 offset:0x1000
	ds_read_b128 v[56:59], v204 offset:0x1400
	ds_read_b128 v[228:231], v204 offset:0x1800
	ds_read_b128 v[232:235], v204 offset:0x1c00
	ds_read_b128 v[8:11], v205 offset:0x4000
	ds_read_b128 v[12:15], v205 offset:0x4400
	ds_read_b128 v[0:3], v205 offset:0x4800
	ds_read_b128 v[4:7], v205 offset:0x4c00
	s_nop 0
	buffer_load_dwordx4 v216, s[4:7], s28 offen lds
	s_mov_b32 m0, s68
	s_nop 0
	buffer_load_dwordx4 v215, s[4:7], s28 offen lds
	s_waitcnt vmcnt(8)
	s_waitcnt lgkmcnt(4)
	s_barrier
	s_setprio 1
	v_mfma_scale_f32_16x16x128_f8f6f4 v[192:195], v[16:23], v[36:43], v[192:195], v201, v201 op_sel_hi:[0,0,0]
	v_mfma_scale_f32_16x16x128_f8f6f4 v[188:191], v[24:31], v[36:43], v[188:191], v201, v201 op_sel_hi:[0,0,0]
	v_mfma_scale_f32_16x16x128_f8f6f4 v[184:187], v[16:23], v[44:51], v[184:187], v201, v201 op_sel_hi:[0,0,0]
	v_mfma_scale_f32_16x16x128_f8f6f4 v[180:183], v[24:31], v[44:51], v[180:183], v201, v201 op_sel_hi:[0,0,0]
	v_mfma_scale_f32_16x16x128_f8f6f4 v[176:179], v[16:23], v[52:59], v[176:179], v201, v201 op_sel_hi:[0,0,0]
	v_mfma_scale_f32_16x16x128_f8f6f4 v[172:175], v[24:31], v[52:59], v[172:175], v201, v201 op_sel_hi:[0,0,0]
	v_mfma_scale_f32_16x16x128_f8f6f4 v[168:171], v[16:23], v[228:235], v[168:171], v201, v201 op_sel_hi:[0,0,0]
	v_mfma_scale_f32_16x16x128_f8f6f4 v[164:167], v[24:31], v[228:235], v[164:167], v201, v201 op_sel_hi:[0,0,0]
	s_setprio 0
	s_setprio 1
	s_waitcnt lgkmcnt(2)
	v_mfma_scale_f32_16x16x128_f8f6f4 v[160:163], v[8:15], v[36:43], v[160:163], v201, v201 op_sel_hi:[0,0,0]
	s_waitcnt lgkmcnt(0)
	v_mfma_scale_f32_16x16x128_f8f6f4 v[156:159], v[0:7], v[36:43], v[156:159], v201, v201 op_sel_hi:[0,0,0]
	v_mfma_scale_f32_16x16x128_f8f6f4 v[152:155], v[8:15], v[44:51], v[152:155], v201, v201 op_sel_hi:[0,0,0]
	v_mfma_scale_f32_16x16x128_f8f6f4 v[148:151], v[0:7], v[44:51], v[148:151], v201, v201 op_sel_hi:[0,0,0]
	v_mfma_scale_f32_16x16x128_f8f6f4 v[144:147], v[8:15], v[52:59], v[144:147], v201, v201 op_sel_hi:[0,0,0]
	v_mfma_scale_f32_16x16x128_f8f6f4 v[140:143], v[0:7], v[52:59], v[140:143], v201, v201 op_sel_hi:[0,0,0]
	v_mfma_scale_f32_16x16x128_f8f6f4 v[136:139], v[8:15], v[228:235], v[136:139], v201, v201 op_sel_hi:[0,0,0]
	v_mfma_scale_f32_16x16x128_f8f6f4 v[132:135], v[0:7], v[228:235], v[132:135], v201, v201 op_sel_hi:[0,0,0]
	s_setprio 0
	s_barrier
	s_mov_b32 m0, s39
	ds_read_b128 v[36:39], v204 offset:0x4000
	ds_read_b128 v[40:43], v204 offset:0x4400
	ds_read_b128 v[44:47], v204 offset:0x4800
	ds_read_b128 v[48:51], v204 offset:0x4c00
	ds_read_b128 v[52:55], v204 offset:0x5000
	ds_read_b128 v[56:59], v204 offset:0x5400
	ds_read_b128 v[228:231], v204 offset:0x5800
	ds_read_b128 v[232:235], v204 offset:0x5c00
	s_nop 0
	buffer_load_dwordx4 v203, s[8:11], s61 offen lds
	s_add_i32 s67, s61, 0x80000
	s_mov_b32 m0, s40
	v_cndmask_b32_e32 v60, v214, v32, vcc
	buffer_load_dwordx4 v203, s[8:11], s67 offen lds
	s_add_i32 s67, s61, 0x8000
	s_mov_b32 m0, s41
	v_cndmask_b32_e32 v61, v217, v33, vcc
	buffer_load_dwordx4 v203, s[8:11], s67 offen lds
	s_add_i32 s67, s61, 0x88000
	s_mov_b32 m0, s42
	s_nop 0
	buffer_load_dwordx4 v203, s[8:11], s67 offen lds
	s_mov_b32 m0, s38
	s_nop 0
	buffer_load_dwordx4 v60, s[4:7], s66 offen lds
	s_mov_b32 m0, s43
	s_nop 0
	buffer_load_dwordx4 v61, s[4:7], s66 offen lds
	s_waitcnt vmcnt(8)
	s_waitcnt lgkmcnt(0)
	s_barrier
	s_setprio 1
	v_mfma_scale_f32_16x16x128_f8f6f4 v[128:131], v[16:23], v[36:43], v[128:131], v201, v201 op_sel_hi:[0,0,0]
	v_mfma_scale_f32_16x16x128_f8f6f4 v[124:127], v[24:31], v[36:43], v[124:127], v201, v201 op_sel_hi:[0,0,0]
	v_mfma_scale_f32_16x16x128_f8f6f4 v[120:123], v[16:23], v[44:51], v[120:123], v201, v201 op_sel_hi:[0,0,0]
	v_mfma_scale_f32_16x16x128_f8f6f4 v[116:119], v[24:31], v[44:51], v[116:119], v201, v201 op_sel_hi:[0,0,0]
	v_mfma_scale_f32_16x16x128_f8f6f4 v[112:115], v[16:23], v[52:59], v[112:115], v201, v201 op_sel_hi:[0,0,0]
	v_mfma_scale_f32_16x16x128_f8f6f4 v[108:111], v[24:31], v[52:59], v[108:111], v201, v201 op_sel_hi:[0,0,0]
	v_mfma_scale_f32_16x16x128_f8f6f4 v[104:107], v[16:23], v[228:235], v[104:107], v201, v201 op_sel_hi:[0,0,0]
	v_mfma_scale_f32_16x16x128_f8f6f4 v[100:103], v[24:31], v[228:235], v[100:103], v201, v201 op_sel_hi:[0,0,0]
	s_setprio 0
	s_setprio 1
	v_mfma_scale_f32_16x16x128_f8f6f4 v[96:99], v[8:15], v[36:43], v[96:99], v201, v201 op_sel_hi:[0,0,0]
	v_mfma_scale_f32_16x16x128_f8f6f4 v[92:95], v[0:7], v[36:43], v[92:95], v201, v201 op_sel_hi:[0,0,0]
	v_mfma_scale_f32_16x16x128_f8f6f4 v[88:91], v[8:15], v[44:51], v[88:91], v201, v201 op_sel_hi:[0,0,0]
	v_mfma_scale_f32_16x16x128_f8f6f4 v[84:87], v[0:7], v[44:51], v[84:87], v201, v201 op_sel_hi:[0,0,0]
	v_mfma_scale_f32_16x16x128_f8f6f4 v[80:83], v[8:15], v[52:59], v[80:83], v201, v201 op_sel_hi:[0,0,0]
	v_mfma_scale_f32_16x16x128_f8f6f4 v[76:79], v[0:7], v[52:59], v[76:79], v201, v201 op_sel_hi:[0,0,0]
	v_mfma_scale_f32_16x16x128_f8f6f4 v[72:75], v[8:15], v[228:235], v[72:75], v201, v201 op_sel_hi:[0,0,0]
	v_mfma_scale_f32_16x16x128_f8f6f4 v[68:71], v[0:7], v[228:235], v[68:71], v201, v201 op_sel_hi:[0,0,0]
	s_setprio 0
	s_barrier
	ds_read_b128 v[24:27], v205 offset:0x8000
	ds_read_b128 v[28:31], v205 offset:0x8400
	ds_read_b128 v[16:19], v205 offset:0x8800
	ds_read_b128 v[20:23], v205 offset:0x8c00
	s_mov_b32 m0, s44
	v_cndmask_b32_e32 v62, v216, v34, vcc
	ds_read_b128 v[36:39], v204 offset:0x8000
	ds_read_b128 v[40:43], v204 offset:0x8400
	ds_read_b128 v[44:47], v204 offset:0x8800
	ds_read_b128 v[48:51], v204 offset:0x8c00
	ds_read_b128 v[52:55], v204 offset:0x9000
	ds_read_b128 v[56:59], v204 offset:0x9400
	ds_read_b128 v[228:231], v204 offset:0x9800
	ds_read_b128 v[232:235], v204 offset:0x9c00
	ds_read_b128 v[8:11], v205 offset:0xc000
	ds_read_b128 v[12:15], v205 offset:0xc400
	ds_read_b128 v[0:3], v205 offset:0xc800
	ds_read_b128 v[4:7], v205 offset:0xcc00
	buffer_load_dwordx4 v62, s[4:7], s66 offen lds
	v_cndmask_b32_e32 v62, v215, v35, vcc
	s_mov_b32 m0, s45
	s_nop 0
	buffer_load_dwordx4 v62, s[4:7], s66 offen lds
	s_waitcnt vmcnt(8)
	s_waitcnt lgkmcnt(4)
	s_barrier
	s_setprio 1
	v_mfma_scale_f32_16x16x128_f8f6f4 v[192:195], v[24:31], v[36:43], v[192:195], v201, v201 op_sel_hi:[0,0,0]
	v_mfma_scale_f32_16x16x128_f8f6f4 v[188:191], v[16:23], v[36:43], v[188:191], v201, v201 op_sel_hi:[0,0,0]
	v_mfma_scale_f32_16x16x128_f8f6f4 v[184:187], v[24:31], v[44:51], v[184:187], v201, v201 op_sel_hi:[0,0,0]
	v_mfma_scale_f32_16x16x128_f8f6f4 v[180:183], v[16:23], v[44:51], v[180:183], v201, v201 op_sel_hi:[0,0,0]
	v_mfma_scale_f32_16x16x128_f8f6f4 v[176:179], v[24:31], v[52:59], v[176:179], v201, v201 op_sel_hi:[0,0,0]
	v_mfma_scale_f32_16x16x128_f8f6f4 v[172:175], v[16:23], v[52:59], v[172:175], v201, v201 op_sel_hi:[0,0,0]
	v_mfma_scale_f32_16x16x128_f8f6f4 v[168:171], v[24:31], v[228:235], v[168:171], v201, v201 op_sel_hi:[0,0,0]
	v_mfma_scale_f32_16x16x128_f8f6f4 v[164:167], v[16:23], v[228:235], v[164:167], v201, v201 op_sel_hi:[0,0,0]
	s_setprio 0
	s_setprio 1
	s_waitcnt lgkmcnt(2)
	v_mfma_scale_f32_16x16x128_f8f6f4 v[160:163], v[8:15], v[36:43], v[160:163], v201, v201 op_sel_hi:[0,0,0]
	s_waitcnt lgkmcnt(0)
	v_mfma_scale_f32_16x16x128_f8f6f4 v[156:159], v[0:7], v[36:43], v[156:159], v201, v201 op_sel_hi:[0,0,0]
	v_mfma_scale_f32_16x16x128_f8f6f4 v[152:155], v[8:15], v[44:51], v[152:155], v201, v201 op_sel_hi:[0,0,0]
	v_mfma_scale_f32_16x16x128_f8f6f4 v[148:151], v[0:7], v[44:51], v[148:151], v201, v201 op_sel_hi:[0,0,0]
	v_mfma_scale_f32_16x16x128_f8f6f4 v[144:147], v[8:15], v[52:59], v[144:147], v201, v201 op_sel_hi:[0,0,0]
	v_mfma_scale_f32_16x16x128_f8f6f4 v[140:143], v[0:7], v[52:59], v[140:143], v201, v201 op_sel_hi:[0,0,0]
	v_mfma_scale_f32_16x16x128_f8f6f4 v[136:139], v[8:15], v[228:235], v[136:139], v201, v201 op_sel_hi:[0,0,0]
	v_mfma_scale_f32_16x16x128_f8f6f4 v[132:135], v[0:7], v[228:235], v[132:135], v201, v201 op_sel_hi:[0,0,0]
	s_setprio 0
	s_barrier
	s_mov_b32 m0, s48
	s_add_i32 s66, s61, 0x80
	ds_read_b128 v[36:39], v204 offset:0xc000
	ds_read_b128 v[40:43], v204 offset:0xc400
	ds_read_b128 v[44:47], v204 offset:0xc800
	ds_read_b128 v[48:51], v204 offset:0xcc00
	ds_read_b128 v[52:55], v204 offset:0xd000
	ds_read_b128 v[56:59], v204 offset:0xd400
	ds_read_b128 v[228:231], v204 offset:0xd800
	ds_read_b128 v[232:235], v204 offset:0xdc00
	buffer_load_dwordx4 v203, s[8:11], s66 offen lds
	s_add_i32 s66, s61, 0x80080
	s_mov_b32 m0, s49
	s_nop 0
	buffer_load_dwordx4 v203, s[8:11], s66 offen lds
	s_add_i32 s66, s61, 0x8080
	s_mov_b32 m0, s62
	s_add_i32 s61, s61, 0x88080
	buffer_load_dwordx4 v203, s[8:11], s66 offen lds
	s_mov_b32 m0, s63
	s_nop 0
	buffer_load_dwordx4 v203, s[8:11], s61 offen lds
	s_mov_b32 m0, s50
	s_nop 0
	buffer_load_dwordx4 v60, s[4:7], s60 offen lds
	s_mov_b32 m0, s51
	s_nop 0
	buffer_load_dwordx4 v61, s[4:7], s60 offen lds
	s_waitcnt vmcnt(8)
	s_waitcnt lgkmcnt(0)
	s_barrier
	s_setprio 1
	v_mfma_scale_f32_16x16x128_f8f6f4 v[128:131], v[24:31], v[36:43], v[128:131], v201, v201 op_sel_hi:[0,0,0]
	v_mfma_scale_f32_16x16x128_f8f6f4 v[124:127], v[16:23], v[36:43], v[124:127], v201, v201 op_sel_hi:[0,0,0]
	v_mfma_scale_f32_16x16x128_f8f6f4 v[120:123], v[24:31], v[44:51], v[120:123], v201, v201 op_sel_hi:[0,0,0]
	v_mfma_scale_f32_16x16x128_f8f6f4 v[116:119], v[16:23], v[44:51], v[116:119], v201, v201 op_sel_hi:[0,0,0]
	v_mfma_scale_f32_16x16x128_f8f6f4 v[112:115], v[24:31], v[52:59], v[112:115], v201, v201 op_sel_hi:[0,0,0]
	v_mfma_scale_f32_16x16x128_f8f6f4 v[108:111], v[16:23], v[52:59], v[108:111], v201, v201 op_sel_hi:[0,0,0]
	v_mfma_scale_f32_16x16x128_f8f6f4 v[104:107], v[24:31], v[228:235], v[104:107], v201, v201 op_sel_hi:[0,0,0]
	v_mfma_scale_f32_16x16x128_f8f6f4 v[100:103], v[16:23], v[228:235], v[100:103], v201, v201 op_sel_hi:[0,0,0]
	s_setprio 0
	s_setprio 1
	v_mfma_scale_f32_16x16x128_f8f6f4 v[96:99], v[8:15], v[36:43], v[96:99], v201, v201 op_sel_hi:[0,0,0]
	v_mfma_scale_f32_16x16x128_f8f6f4 v[92:95], v[0:7], v[36:43], v[92:95], v201, v201 op_sel_hi:[0,0,0]
	v_mfma_scale_f32_16x16x128_f8f6f4 v[88:91], v[8:15], v[44:51], v[88:91], v201, v201 op_sel_hi:[0,0,0]
	v_mfma_scale_f32_16x16x128_f8f6f4 v[84:87], v[0:7], v[44:51], v[84:87], v201, v201 op_sel_hi:[0,0,0]
	v_mfma_scale_f32_16x16x128_f8f6f4 v[80:83], v[8:15], v[52:59], v[80:83], v201, v201 op_sel_hi:[0,0,0]
	v_mfma_scale_f32_16x16x128_f8f6f4 v[76:79], v[0:7], v[52:59], v[76:79], v201, v201 op_sel_hi:[0,0,0]
	v_mfma_scale_f32_16x16x128_f8f6f4 v[72:75], v[8:15], v[228:235], v[72:75], v201, v201 op_sel_hi:[0,0,0]
	v_mfma_scale_f32_16x16x128_f8f6f4 v[68:71], v[0:7], v[228:235], v[68:71], v201, v201 op_sel_hi:[0,0,0]
	s_setprio 0
	s_barrier
	s_add_i32 s33, s33, 2
	s_addk_i32 s28, 0x100
	s_addk_i32 s29, 0x100
	s_cmp_gt_u32 s33, 29
	s_cbranch_scc0 .LBB0_1229
	s_and_b64 vcc, exec, s[18:19]
	s_cbranch_vccz .LBB0_1232
	s_barrier

.LBB0_1329:
	s_add_i32 s36, s89, 0x180
	s_add_i32 s37, s61, 0x180
	s_waitcnt lgkmcnt(0)
	s_barrier
	s_setprio 1
	v_mfma_scale_f32_16x16x128_f8f6f4 v[128:131], v[24:31], v[56:63], 0, v198, v198 op_sel_hi:[0,0,0]
	v_mfma_scale_f32_16x16x128_f8f6f4 v[124:127], v[16:23], v[56:63], 0, v198, v198 op_sel_hi:[0,0,0]
	v_mfma_scale_f32_16x16x128_f8f6f4 v[120:123], v[24:31], v[48:55], 0, v198, v198 op_sel_hi:[0,0,0]
	v_mfma_scale_f32_16x16x128_f8f6f4 v[116:119], v[16:23], v[48:55], 0, v198, v198 op_sel_hi:[0,0,0]
	v_mfma_scale_f32_16x16x128_f8f6f4 v[112:115], v[24:31], v[40:47], 0, v198, v198 op_sel_hi:[0,0,0]
	v_mfma_scale_f32_16x16x128_f8f6f4 v[108:111], v[16:23], v[40:47], 0, v198, v198 op_sel_hi:[0,0,0]
	v_mfma_scale_f32_16x16x128_f8f6f4 v[104:107], v[24:31], v[32:39], 0, v198, v198 op_sel_hi:[0,0,0]
	v_mfma_scale_f32_16x16x128_f8f6f4 v[100:103], v[16:23], v[32:39], 0, v198, v198 op_sel_hi:[0,0,0]
	s_setprio 0
	s_setprio 1
	v_mfma_scale_f32_16x16x128_f8f6f4 v[96:99], v[8:15], v[56:63], 0, v198, v198 op_sel_hi:[0,0,0]
	v_mfma_scale_f32_16x16x128_f8f6f4 v[92:95], v[0:7], v[56:63], 0, v198, v198 op_sel_hi:[0,0,0]
	v_mfma_scale_f32_16x16x128_f8f6f4 v[88:91], v[8:15], v[48:55], 0, v198, v198 op_sel_hi:[0,0,0]
	v_mfma_scale_f32_16x16x128_f8f6f4 v[84:87], v[0:7], v[48:55], 0, v198, v198 op_sel_hi:[0,0,0]
	v_mfma_scale_f32_16x16x128_f8f6f4 v[80:83], v[8:15], v[40:47], 0, v198, v198 op_sel_hi:[0,0,0]
	v_mfma_scale_f32_16x16x128_f8f6f4 v[76:79], v[0:7], v[40:47], 0, v198, v198 op_sel_hi:[0,0,0]
	v_mfma_scale_f32_16x16x128_f8f6f4 v[72:75], v[8:15], v[32:39], 0, v198, v198 op_sel_hi:[0,0,0]
	v_mfma_scale_f32_16x16x128_f8f6f4 v[68:71], v[0:7], v[32:39], 0, v198, v198 op_sel_hi:[0,0,0]
	s_setprio 0
	s_barrier
	ds_read_b128 v[24:27], v202 offset:0x8000
	ds_read_b128 v[28:31], v202 offset:0x8400
	ds_read_b128 v[16:19], v202 offset:0x8800
	ds_read_b128 v[20:23], v202 offset:0x8c00
	s_mov_b32 m0, s50
	ds_read_b128 v[32:35], v201 offset:0x8000
	ds_read_b128 v[36:39], v201 offset:0x8400
	ds_read_b128 v[40:43], v201 offset:0x8800
	ds_read_b128 v[44:47], v201 offset:0x8c00
	ds_read_b128 v[48:51], v201 offset:0x9000
	ds_read_b128 v[52:55], v201 offset:0x9400
	ds_read_b128 v[56:59], v201 offset:0x9800
	ds_read_b128 v[60:63], v201 offset:0x9c00
	ds_read_b128 v[8:11], v202 offset:0xc000
	ds_read_b128 v[12:15], v202 offset:0xc400
	ds_read_b128 v[0:3], v202 offset:0xc800
	ds_read_b128 v[4:7], v202 offset:0xcc00
	s_nop 0
	buffer_load_dwordx4 v207, s[4:7], s33 offen lds
	s_mov_b32 m0, s51
	s_nop 0
	buffer_load_dwordx4 v206, s[4:7], s33 offen lds
	s_waitcnt vmcnt(8)
	s_waitcnt lgkmcnt(4)
	s_barrier
	s_setprio 1
	v_mfma_scale_f32_16x16x128_f8f6f4 v[192:195], v[24:31], v[32:39], v[192:195], v198, v198 op_sel_hi:[0,0,0]
	v_mfma_scale_f32_16x16x128_f8f6f4 v[188:191], v[16:23], v[32:39], v[188:191], v198, v198 op_sel_hi:[0,0,0]
	v_mfma_scale_f32_16x16x128_f8f6f4 v[184:187], v[24:31], v[40:47], v[184:187], v198, v198 op_sel_hi:[0,0,0]
	v_mfma_scale_f32_16x16x128_f8f6f4 v[180:183], v[16:23], v[40:47], v[180:183], v198, v198 op_sel_hi:[0,0,0]
	v_mfma_scale_f32_16x16x128_f8f6f4 v[176:179], v[24:31], v[48:55], v[176:179], v198, v198 op_sel_hi:[0,0,0]
	v_mfma_scale_f32_16x16x128_f8f6f4 v[172:175], v[16:23], v[48:55], v[172:175], v198, v198 op_sel_hi:[0,0,0]
	v_mfma_scale_f32_16x16x128_f8f6f4 v[168:171], v[24:31], v[56:63], v[168:171], v198, v198 op_sel_hi:[0,0,0]
	v_mfma_scale_f32_16x16x128_f8f6f4 v[164:167], v[16:23], v[56:63], v[164:167], v198, v198 op_sel_hi:[0,0,0]
	s_setprio 0
	s_setprio 1
	s_waitcnt lgkmcnt(2)
	v_mfma_scale_f32_16x16x128_f8f6f4 v[160:163], v[8:15], v[32:39], v[160:163], v198, v198 op_sel_hi:[0,0,0]
	s_waitcnt lgkmcnt(0)
	v_mfma_scale_f32_16x16x128_f8f6f4 v[156:159], v[0:7], v[32:39], v[156:159], v198, v198 op_sel_hi:[0,0,0]
	v_mfma_scale_f32_16x16x128_f8f6f4 v[152:155], v[8:15], v[40:47], v[152:155], v198, v198 op_sel_hi:[0,0,0]
	v_mfma_scale_f32_16x16x128_f8f6f4 v[148:151], v[0:7], v[40:47], v[148:151], v198, v198 op_sel_hi:[0,0,0]
	v_mfma_scale_f32_16x16x128_f8f6f4 v[144:147], v[8:15], v[48:55], v[144:147], v198, v198 op_sel_hi:[0,0,0]
	v_mfma_scale_f32_16x16x128_f8f6f4 v[140:143], v[0:7], v[48:55], v[140:143], v198, v198 op_sel_hi:[0,0,0]
	v_mfma_scale_f32_16x16x128_f8f6f4 v[136:139], v[8:15], v[56:63], v[136:139], v198, v198 op_sel_hi:[0,0,0]
	v_mfma_scale_f32_16x16x128_f8f6f4 v[132:135], v[0:7], v[56:63], v[132:135], v198, v198 op_sel_hi:[0,0,0]
	s_setprio 0
	s_barrier
	s_mov_b32 m0, s64
	s_mov_b32 s10, s6
	s_mov_b32 s11, s7
	ds_read_b128 v[32:35], v201 offset:0xc000
	ds_read_b128 v[36:39], v201 offset:0xc400
	ds_read_b128 v[40:43], v201 offset:0xc800
	ds_read_b128 v[44:47], v201 offset:0xcc00
	ds_read_b128 v[48:51], v201 offset:0xd000
	ds_read_b128 v[52:55], v201 offset:0xd400
	ds_read_b128 v[56:59], v201 offset:0xd800
	ds_read_b128 v[60:63], v201 offset:0xdc00
	buffer_load_dwordx4 v200, s[8:11], s37 offen lds
	s_add_i32 s33, s61, 0x80180
	s_mov_b32 m0, s65
	s_nop 0
	buffer_load_dwordx4 v200, s[8:11], s33 offen lds
	s_add_i32 s33, s61, 0x8180
	s_mov_b32 m0, s70
	s_nop 0
	buffer_load_dwordx4 v200, s[8:11], s33 offen lds
	s_add_i32 s33, s61, 0x88180
	s_mov_b32 m0, s71
	s_nop 0
	buffer_load_dwordx4 v200, s[8:11], s33 offen lds
	s_mov_b32 m0, s68
	s_nop 0
	buffer_load_dwordx4 v205, s[4:7], s36 offen lds
	s_mov_b32 m0, s69
	s_nop 0
	buffer_load_dwordx4 v208, s[4:7], s36 offen lds
	s_waitcnt vmcnt(8)
	s_waitcnt lgkmcnt(0)
	s_barrier
	s_setprio 1
	v_mfma_scale_f32_16x16x128_f8f6f4 v[128:131], v[24:31], v[32:39], v[128:131], v198, v198 op_sel_hi:[0,0,0]
	v_mfma_scale_f32_16x16x128_f8f6f4 v[124:127], v[16:23], v[32:39], v[124:127], v198, v198 op_sel_hi:[0,0,0]
	v_mfma_scale_f32_16x16x128_f8f6f4 v[120:123], v[24:31], v[40:47], v[120:123], v198, v198 op_sel_hi:[0,0,0]
	v_mfma_scale_f32_16x16x128_f8f6f4 v[116:119], v[16:23], v[40:47], v[116:119], v198, v198 op_sel_hi:[0,0,0]
	v_mfma_scale_f32_16x16x128_f8f6f4 v[112:115], v[24:31], v[48:55], v[112:115], v198, v198 op_sel_hi:[0,0,0]
	v_mfma_scale_f32_16x16x128_f8f6f4 v[108:111], v[16:23], v[48:55], v[108:111], v198, v198 op_sel_hi:[0,0,0]
	v_mfma_scale_f32_16x16x128_f8f6f4 v[104:107], v[24:31], v[56:63], v[104:107], v198, v198 op_sel_hi:[0,0,0]
	v_mfma_scale_f32_16x16x128_f8f6f4 v[100:103], v[16:23], v[56:63], v[100:103], v198, v198 op_sel_hi:[0,0,0]
	s_setprio 0
	s_setprio 1
	v_mfma_scale_f32_16x16x128_f8f6f4 v[96:99], v[8:15], v[32:39], v[96:99], v198, v198 op_sel_hi:[0,0,0]
	v_mfma_scale_f32_16x16x128_f8f6f4 v[92:95], v[0:7], v[32:39], v[92:95], v198, v198 op_sel_hi:[0,0,0]
	v_mfma_scale_f32_16x16x128_f8f6f4 v[88:91], v[8:15], v[40:47], v[88:91], v198, v198 op_sel_hi:[0,0,0]
	v_mfma_scale_f32_16x16x128_f8f6f4 v[84:87], v[0:7], v[40:47], v[84:87], v198, v198 op_sel_hi:[0,0,0]
	v_mfma_scale_f32_16x16x128_f8f6f4 v[80:83], v[8:15], v[48:55], v[80:83], v198, v198 op_sel_hi:[0,0,0]
	v_mfma_scale_f32_16x16x128_f8f6f4 v[76:79], v[0:7], v[48:55], v[76:79], v198, v198 op_sel_hi:[0,0,0]
	v_mfma_scale_f32_16x16x128_f8f6f4 v[72:75], v[8:15], v[56:63], v[72:75], v198, v198 op_sel_hi:[0,0,0]
	v_mfma_scale_f32_16x16x128_f8f6f4 v[68:71], v[0:7], v[56:63], v[68:71], v198, v198 op_sel_hi:[0,0,0]
	s_setprio 0
	s_barrier
	s_waitcnt vmcnt(16)
	v_mbcnt_lo_u32_b32 v0, -1, 0
	v_mbcnt_hi_u32_b32 v0, -1, v0
	s_add_i32 s33, s61, 0x200
	v_lshl_add_u32 v0, v0, 4, s40
	v_ashrrev_i32_e32 v1, 31, v0
	v_lshrrev_b32_e32 v1, 22, v1
	v_add_u32_e32 v1, v0, v1
	v_ashrrev_i32_e32 v1, 10, v1
	v_mul_i32_i24_e32 v2, 0x400, v1
	v_sub_u32_e32 v2, v0, v2
	v_lshrrev_b32_e32 v3, 4, v2
	v_bitop3_b32 v3, v3, v2, 32 bitop3:0x6c
	v_ashrrev_i32_e32 v2, 31, v2
	v_lshrrev_b32_e32 v2, 26, v2
	v_add_u32_e32 v2, v3, v2
	v_and_b32_e32 v2, 0xc0, v2
	v_add_u32_e32 v0, 0x2000, v0
	v_sub_u32_e32 v2, v3, v2
	v_ashrrev_i32_e32 v3, 31, v0
	v_lshrrev_b32_e32 v3, 22, v3
	v_add_u32_e32 v3, v0, v3
	v_ashrrev_i32_e32 v3, 10, v3
	v_mul_i32_i24_e32 v4, 0x400, v3
	v_sub_u32_e32 v0, v0, v4
	v_lshrrev_b32_e32 v4, 4, v0
	v_bitop3_b32 v4, v4, v0, 32 bitop3:0x6c
	v_ashrrev_i32_e32 v0, 31, v0
	v_lshrrev_b32_e32 v0, 26, v0
	v_add_u32_e32 v0, v4, v0
	v_and_b32_e32 v0, 0xffc0, v0
	v_sub_u32_e32 v0, v4, v0
	v_lshrrev_b16_e32 v4, 7, v0
	v_and_b32_e32 v4, 1, v4
	v_add_u16_e32 v0, v0, v4
	v_lshlrev_b32_e32 v1, 5, v1
	v_ashrrev_i16_sdwa v2, v199, sext(v2) dst_sel:DWORD dst_unused:UNUSED_PAD src0_sel:DWORD src1_sel:BYTE_0
	v_lshlrev_b32_e32 v3, 5, v3
	v_ashrrev_i16_sdwa v0, v199, sext(v0) dst_sel:DWORD dst_unused:UNUSED_PAD src0_sel:DWORD src1_sel:BYTE_0
	v_and_b32_e32 v1, 32, v1
	v_bfe_i32 v2, v2, 0, 16
	v_and_b32_e32 v3, 32, v3
	v_bfe_i32 v0, v0, 0, 16
	v_add_lshl_u32 v1, v1, v2, 1
	v_add_lshl_u32 v0, v3, v0, 1
	v_lshl_add_u32 v32, v220, 12, v1
	v_lshl_add_u32 v33, v217, 12, v0
	v_lshl_add_u32 v34, v218, 12, v1
	v_lshl_add_u32 v35, v219, 12, v0
	s_mov_b32 s37, 0
.LBB0_1330:
	s_add_i32 s61, s36, 0x80
	s_cmp_eq_u32 s37, 28
	s_cselect_b64 vcc, -1, 0
	ds_read_b128 v[16:19], v202 offset:0
	ds_read_b128 v[20:23], v202 offset:0x400
	ds_read_b128 v[24:27], v202 offset:0x800
	ds_read_b128 v[28:31], v202 offset:0xc00
	s_and_b64 s[66:67], vcc, exec
	s_cselect_b32 s67, s85, s61
	s_cselect_b32 s66, s86, s33
	s_add_i32 s61, s67, 0x80
	s_mov_b32 m0, s73
	ds_read_b128 v[36:39], v201 offset:0
	ds_read_b128 v[40:43], v201 offset:0x400
	ds_read_b128 v[44:47], v201 offset:0x800
	ds_read_b128 v[48:51], v201 offset:0xc00
	ds_read_b128 v[52:55], v201 offset:0x1000
	ds_read_b128 v[56:59], v201 offset:0x1400
	ds_read_b128 v[218:221], v201 offset:0x1800
	ds_read_b128 v[222:225], v201 offset:0x1c00
	ds_read_b128 v[8:11], v202 offset:0x4000
	ds_read_b128 v[12:15], v202 offset:0x4400
	ds_read_b128 v[0:3], v202 offset:0x4800
	ds_read_b128 v[4:7], v202 offset:0x4c00
	s_nop 0
	buffer_load_dwordx4 v207, s[4:7], s36 offen lds
	s_mov_b32 m0, s74
	s_nop 0
	buffer_load_dwordx4 v206, s[4:7], s36 offen lds
	s_waitcnt vmcnt(8)
	s_waitcnt lgkmcnt(4)
	s_barrier
	s_setprio 1
	v_mfma_scale_f32_16x16x128_f8f6f4 v[192:195], v[16:23], v[36:43], v[192:195], v198, v198 op_sel_hi:[0,0,0]
	v_mfma_scale_f32_16x16x128_f8f6f4 v[188:191], v[24:31], v[36:43], v[188:191], v198, v198 op_sel_hi:[0,0,0]
	v_mfma_scale_f32_16x16x128_f8f6f4 v[184:187], v[16:23], v[44:51], v[184:187], v198, v198 op_sel_hi:[0,0,0]
	v_mfma_scale_f32_16x16x128_f8f6f4 v[180:183], v[24:31], v[44:51], v[180:183], v198, v198 op_sel_hi:[0,0,0]
	v_mfma_scale_f32_16x16x128_f8f6f4 v[176:179], v[16:23], v[52:59], v[176:179], v198, v198 op_sel_hi:[0,0,0]
	v_mfma_scale_f32_16x16x128_f8f6f4 v[172:175], v[24:31], v[52:59], v[172:175], v198, v198 op_sel_hi:[0,0,0]
	v_mfma_scale_f32_16x16x128_f8f6f4 v[168:171], v[16:23], v[218:225], v[168:171], v198, v198 op_sel_hi:[0,0,0]
	v_mfma_scale_f32_16x16x128_f8f6f4 v[164:167], v[24:31], v[218:225], v[164:167], v198, v198 op_sel_hi:[0,0,0]
	s_setprio 0
	s_setprio 1
	s_waitcnt lgkmcnt(2)
	v_mfma_scale_f32_16x16x128_f8f6f4 v[160:163], v[8:15], v[36:43], v[160:163], v198, v198 op_sel_hi:[0,0,0]
	s_waitcnt lgkmcnt(0)
	v_mfma_scale_f32_16x16x128_f8f6f4 v[156:159], v[0:7], v[36:43], v[156:159], v198, v198 op_sel_hi:[0,0,0]
	v_mfma_scale_f32_16x16x128_f8f6f4 v[152:155], v[8:15], v[44:51], v[152:155], v198, v198 op_sel_hi:[0,0,0]
	v_mfma_scale_f32_16x16x128_f8f6f4 v[148:151], v[0:7], v[44:51], v[148:151], v198, v198 op_sel_hi:[0,0,0]
	v_mfma_scale_f32_16x16x128_f8f6f4 v[144:147], v[8:15], v[52:59], v[144:147], v198, v198 op_sel_hi:[0,0,0]
	v_mfma_scale_f32_16x16x128_f8f6f4 v[140:143], v[0:7], v[52:59], v[140:143], v198, v198 op_sel_hi:[0,0,0]
	v_mfma_scale_f32_16x16x128_f8f6f4 v[136:139], v[8:15], v[218:225], v[136:139], v198, v198 op_sel_hi:[0,0,0]
	v_mfma_scale_f32_16x16x128_f8f6f4 v[132:135], v[0:7], v[218:225], v[132:135], v198, v198 op_sel_hi:[0,0,0]
	s_setprio 0
	s_barrier
	s_mov_b32 m0, s45
	ds_read_b128 v[36:39], v201 offset:0x4000
	ds_read_b128 v[40:43], v201 offset:0x4400
	ds_read_b128 v[44:47], v201 offset:0x4800
	ds_read_b128 v[48:51], v201 offset:0x4c00
	ds_read_b128 v[52:55], v201 offset:0x5000
	ds_read_b128 v[56:59], v201 offset:0x5400
	ds_read_b128 v[218:221], v201 offset:0x5800
	ds_read_b128 v[222:225], v201 offset:0x5c00
	s_nop 0
	buffer_load_dwordx4 v200, s[8:11], s66 offen lds
	s_add_i32 s89, s66, 0x80000
	s_mov_b32 m0, s46
	v_cndmask_b32_e32 v60, v205, v32, vcc
	buffer_load_dwordx4 v200, s[8:11], s89 offen lds
	s_add_i32 s89, s66, 0x8000
	s_mov_b32 m0, s47
	v_cndmask_b32_e32 v61, v208, v33, vcc
	buffer_load_dwordx4 v200, s[8:11], s89 offen lds
	s_add_i32 s89, s66, 0x88000
	s_mov_b32 m0, s48
	s_nop 0
	buffer_load_dwordx4 v200, s[8:11], s89 offen lds
	s_mov_b32 m0, s44
	s_nop 0
	buffer_load_dwordx4 v60, s[4:7], s67 offen lds
	s_mov_b32 m0, s49
	s_nop 0
	buffer_load_dwordx4 v61, s[4:7], s67 offen lds
	s_waitcnt vmcnt(8)
	s_waitcnt lgkmcnt(0)
	s_barrier
	s_setprio 1
	v_mfma_scale_f32_16x16x128_f8f6f4 v[128:131], v[16:23], v[36:43], v[128:131], v198, v198 op_sel_hi:[0,0,0]
	v_mfma_scale_f32_16x16x128_f8f6f4 v[124:127], v[24:31], v[36:43], v[124:127], v198, v198 op_sel_hi:[0,0,0]
	v_mfma_scale_f32_16x16x128_f8f6f4 v[120:123], v[16:23], v[44:51], v[120:123], v198, v198 op_sel_hi:[0,0,0]
	v_mfma_scale_f32_16x16x128_f8f6f4 v[116:119], v[24:31], v[44:51], v[116:119], v198, v198 op_sel_hi:[0,0,0]
	v_mfma_scale_f32_16x16x128_f8f6f4 v[112:115], v[16:23], v[52:59], v[112:115], v198, v198 op_sel_hi:[0,0,0]
	v_mfma_scale_f32_16x16x128_f8f6f4 v[108:111], v[24:31], v[52:59], v[108:111], v198, v198 op_sel_hi:[0,0,0]
	v_mfma_scale_f32_16x16x128_f8f6f4 v[104:107], v[16:23], v[218:225], v[104:107], v198, v198 op_sel_hi:[0,0,0]
	v_mfma_scale_f32_16x16x128_f8f6f4 v[100:103], v[24:31], v[218:225], v[100:103], v198, v198 op_sel_hi:[0,0,0]
	s_setprio 0
	s_setprio 1
	v_mfma_scale_f32_16x16x128_f8f6f4 v[96:99], v[8:15], v[36:43], v[96:99], v198, v198 op_sel_hi:[0,0,0]
	v_mfma_scale_f32_16x16x128_f8f6f4 v[92:95], v[0:7], v[36:43], v[92:95], v198, v198 op_sel_hi:[0,0,0]
	v_mfma_scale_f32_16x16x128_f8f6f4 v[88:91], v[8:15], v[44:51], v[88:91], v198, v198 op_sel_hi:[0,0,0]
	v_mfma_scale_f32_16x16x128_f8f6f4 v[84:87], v[0:7], v[44:51], v[84:87], v198, v198 op_sel_hi:[0,0,0]
	v_mfma_scale_f32_16x16x128_f8f6f4 v[80:83], v[8:15], v[52:59], v[80:83], v198, v198 op_sel_hi:[0,0,0]
	v_mfma_scale_f32_16x16x128_f8f6f4 v[76:79], v[0:7], v[52:59], v[76:79], v198, v198 op_sel_hi:[0,0,0]
	v_mfma_scale_f32_16x16x128_f8f6f4 v[72:75], v[8:15], v[218:225], v[72:75], v198, v198 op_sel_hi:[0,0,0]
	v_mfma_scale_f32_16x16x128_f8f6f4 v[68:71], v[0:7], v[218:225], v[68:71], v198, v198 op_sel_hi:[0,0,0]
	s_setprio 0
	s_barrier
	ds_read_b128 v[24:27], v202 offset:0x8000
	ds_read_b128 v[28:31], v202 offset:0x8400
	ds_read_b128 v[16:19], v202 offset:0x8800
	ds_read_b128 v[20:23], v202 offset:0x8c00
	s_mov_b32 m0, s50
	v_cndmask_b32_e32 v62, v207, v34, vcc
	ds_read_b128 v[36:39], v201 offset:0x8000
	ds_read_b128 v[40:43], v201 offset:0x8400
	ds_read_b128 v[44:47], v201 offset:0x8800
	ds_read_b128 v[48:51], v201 offset:0x8c00
	ds_read_b128 v[52:55], v201 offset:0x9000
	ds_read_b128 v[56:59], v201 offset:0x9400
	ds_read_b128 v[218:221], v201 offset:0x9800
	ds_read_b128 v[222:225], v201 offset:0x9c00
	ds_read_b128 v[8:11], v202 offset:0xc000
	ds_read_b128 v[12:15], v202 offset:0xc400
	ds_read_b128 v[0:3], v202 offset:0xc800
	ds_read_b128 v[4:7], v202 offset:0xcc00
	buffer_load_dwordx4 v62, s[4:7], s67 offen lds
	v_cndmask_b32_e32 v62, v206, v35, vcc
	s_mov_b32 m0, s51
	s_nop 0
	buffer_load_dwordx4 v62, s[4:7], s67 offen lds
	s_waitcnt vmcnt(8)
	s_waitcnt lgkmcnt(4)
	s_barrier
	s_setprio 1
	v_mfma_scale_f32_16x16x128_f8f6f4 v[192:195], v[24:31], v[36:43], v[192:195], v198, v198 op_sel_hi:[0,0,0]
	v_mfma_scale_f32_16x16x128_f8f6f4 v[188:191], v[16:23], v[36:43], v[188:191], v198, v198 op_sel_hi:[0,0,0]
	v_mfma_scale_f32_16x16x128_f8f6f4 v[184:187], v[24:31], v[44:51], v[184:187], v198, v198 op_sel_hi:[0,0,0]
	v_mfma_scale_f32_16x16x128_f8f6f4 v[180:183], v[16:23], v[44:51], v[180:183], v198, v198 op_sel_hi:[0,0,0]
	v_mfma_scale_f32_16x16x128_f8f6f4 v[176:179], v[24:31], v[52:59], v[176:179], v198, v198 op_sel_hi:[0,0,0]
	v_mfma_scale_f32_16x16x128_f8f6f4 v[172:175], v[16:23], v[52:59], v[172:175], v198, v198 op_sel_hi:[0,0,0]
	v_mfma_scale_f32_16x16x128_f8f6f4 v[168:171], v[24:31], v[218:225], v[168:171], v198, v198 op_sel_hi:[0,0,0]
	v_mfma_scale_f32_16x16x128_f8f6f4 v[164:167], v[16:23], v[218:225], v[164:167], v198, v198 op_sel_hi:[0,0,0]
	s_setprio 0
	s_setprio 1
	s_waitcnt lgkmcnt(2)
	v_mfma_scale_f32_16x16x128_f8f6f4 v[160:163], v[8:15], v[36:43], v[160:163], v198, v198 op_sel_hi:[0,0,0]
	s_waitcnt lgkmcnt(0)
	v_mfma_scale_f32_16x16x128_f8f6f4 v[156:159], v[0:7], v[36:43], v[156:159], v198, v198 op_sel_hi:[0,0,0]
	v_mfma_scale_f32_16x16x128_f8f6f4 v[152:155], v[8:15], v[44:51], v[152:155], v198, v198 op_sel_hi:[0,0,0]
	v_mfma_scale_f32_16x16x128_f8f6f4 v[148:151], v[0:7], v[44:51], v[148:151], v198, v198 op_sel_hi:[0,0,0]
	v_mfma_scale_f32_16x16x128_f8f6f4 v[144:147], v[8:15], v[52:59], v[144:147], v198, v198 op_sel_hi:[0,0,0]
	v_mfma_scale_f32_16x16x128_f8f6f4 v[140:143], v[0:7], v[52:59], v[140:143], v198, v198 op_sel_hi:[0,0,0]
	v_mfma_scale_f32_16x16x128_f8f6f4 v[136:139], v[8:15], v[218:225], v[136:139], v198, v198 op_sel_hi:[0,0,0]
	v_mfma_scale_f32_16x16x128_f8f6f4 v[132:135], v[0:7], v[218:225], v[132:135], v198, v198 op_sel_hi:[0,0,0]
	s_setprio 0
	s_barrier
	s_mov_b32 m0, s64
	s_add_i32 s67, s66, 0x80
	ds_read_b128 v[36:39], v201 offset:0xc000
	ds_read_b128 v[40:43], v201 offset:0xc400
	ds_read_b128 v[44:47], v201 offset:0xc800
	ds_read_b128 v[48:51], v201 offset:0xcc00
	ds_read_b128 v[52:55], v201 offset:0xd000
	ds_read_b128 v[56:59], v201 offset:0xd400
	ds_read_b128 v[218:221], v201 offset:0xd800
	ds_read_b128 v[222:225], v201 offset:0xdc00
	buffer_load_dwordx4 v200, s[8:11], s67 offen lds
	s_add_i32 s67, s66, 0x80080
	s_mov_b32 m0, s65
	s_nop 0
	buffer_load_dwordx4 v200, s[8:11], s67 offen lds
	s_add_i32 s67, s66, 0x8080
	s_mov_b32 m0, s70
	s_add_i32 s66, s66, 0x88080
	buffer_load_dwordx4 v200, s[8:11], s67 offen lds
	s_mov_b32 m0, s71
	s_nop 0
	buffer_load_dwordx4 v200, s[8:11], s66 offen lds
	s_mov_b32 m0, s68
	s_nop 0
	buffer_load_dwordx4 v60, s[4:7], s61 offen lds
	s_mov_b32 m0, s69
	s_nop 0
	buffer_load_dwordx4 v61, s[4:7], s61 offen lds
	s_waitcnt vmcnt(8)
	s_waitcnt lgkmcnt(0)
	s_barrier
	s_setprio 1
	v_mfma_scale_f32_16x16x128_f8f6f4 v[128:131], v[24:31], v[36:43], v[128:131], v198, v198 op_sel_hi:[0,0,0]
	v_mfma_scale_f32_16x16x128_f8f6f4 v[124:127], v[16:23], v[36:43], v[124:127], v198, v198 op_sel_hi:[0,0,0]
	v_mfma_scale_f32_16x16x128_f8f6f4 v[120:123], v[24:31], v[44:51], v[120:123], v198, v198 op_sel_hi:[0,0,0]
	v_mfma_scale_f32_16x16x128_f8f6f4 v[116:119], v[16:23], v[44:51], v[116:119], v198, v198 op_sel_hi:[0,0,0]
	v_mfma_scale_f32_16x16x128_f8f6f4 v[112:115], v[24:31], v[52:59], v[112:115], v198, v198 op_sel_hi:[0,0,0]
	v_mfma_scale_f32_16x16x128_f8f6f4 v[108:111], v[16:23], v[52:59], v[108:111], v198, v198 op_sel_hi:[0,0,0]
	v_mfma_scale_f32_16x16x128_f8f6f4 v[104:107], v[24:31], v[218:225], v[104:107], v198, v198 op_sel_hi:[0,0,0]
	v_mfma_scale_f32_16x16x128_f8f6f4 v[100:103], v[16:23], v[218:225], v[100:103], v198, v198 op_sel_hi:[0,0,0]
	s_setprio 0
	s_setprio 1
	v_mfma_scale_f32_16x16x128_f8f6f4 v[96:99], v[8:15], v[36:43], v[96:99], v198, v198 op_sel_hi:[0,0,0]
	v_mfma_scale_f32_16x16x128_f8f6f4 v[92:95], v[0:7], v[36:43], v[92:95], v198, v198 op_sel_hi:[0,0,0]
	v_mfma_scale_f32_16x16x128_f8f6f4 v[88:91], v[8:15], v[44:51], v[88:91], v198, v198 op_sel_hi:[0,0,0]
	v_mfma_scale_f32_16x16x128_f8f6f4 v[84:87], v[0:7], v[44:51], v[84:87], v198, v198 op_sel_hi:[0,0,0]
	v_mfma_scale_f32_16x16x128_f8f6f4 v[80:83], v[8:15], v[52:59], v[80:83], v198, v198 op_sel_hi:[0,0,0]
	v_mfma_scale_f32_16x16x128_f8f6f4 v[76:79], v[0:7], v[52:59], v[76:79], v198, v198 op_sel_hi:[0,0,0]
	v_mfma_scale_f32_16x16x128_f8f6f4 v[72:75], v[8:15], v[218:225], v[72:75], v198, v198 op_sel_hi:[0,0,0]
	v_mfma_scale_f32_16x16x128_f8f6f4 v[68:71], v[0:7], v[218:225], v[68:71], v198, v198 op_sel_hi:[0,0,0]
	s_setprio 0
	s_barrier
	s_add_i32 s37, s37, 2
	s_addk_i32 s36, 0x100
	s_addk_i32 s33, 0x100
	s_cmp_gt_u32 s37, 29
	s_cbranch_scc0 .LBB0_1330
	s_and_b64 vcc, exec, s[28:29]
	s_cbranch_vccz .LBB0_1333
	s_barrier

.LBB0_1369:
	s_add_i32 s33, s88, 0x180
	s_add_i32 s40, s89, 0x180
	s_waitcnt lgkmcnt(0)
	s_barrier
	s_setprio 1
	v_mfma_scale_f32_16x16x128_f8f6f4 v[128:131], v[24:31], v[56:63], 0, v235, v235 op_sel_hi:[0,0,0]
	v_mfma_scale_f32_16x16x128_f8f6f4 v[124:127], v[16:23], v[56:63], 0, v235, v235 op_sel_hi:[0,0,0]
	v_mfma_scale_f32_16x16x128_f8f6f4 v[120:123], v[24:31], v[48:55], 0, v235, v235 op_sel_hi:[0,0,0]
	v_mfma_scale_f32_16x16x128_f8f6f4 v[116:119], v[16:23], v[48:55], 0, v235, v235 op_sel_hi:[0,0,0]
	v_mfma_scale_f32_16x16x128_f8f6f4 v[112:115], v[24:31], v[40:47], 0, v235, v235 op_sel_hi:[0,0,0]
	v_mfma_scale_f32_16x16x128_f8f6f4 v[108:111], v[16:23], v[40:47], 0, v235, v235 op_sel_hi:[0,0,0]
	v_mfma_scale_f32_16x16x128_f8f6f4 v[104:107], v[24:31], v[32:39], 0, v235, v235 op_sel_hi:[0,0,0]
	v_mfma_scale_f32_16x16x128_f8f6f4 v[100:103], v[16:23], v[32:39], 0, v235, v235 op_sel_hi:[0,0,0]
	s_setprio 0
	s_setprio 1
	v_mfma_scale_f32_16x16x128_f8f6f4 v[96:99], v[8:15], v[56:63], 0, v235, v235 op_sel_hi:[0,0,0]
	v_mfma_scale_f32_16x16x128_f8f6f4 v[92:95], v[0:7], v[56:63], 0, v235, v235 op_sel_hi:[0,0,0]
	v_mfma_scale_f32_16x16x128_f8f6f4 v[88:91], v[8:15], v[48:55], 0, v235, v235 op_sel_hi:[0,0,0]
	v_mfma_scale_f32_16x16x128_f8f6f4 v[84:87], v[0:7], v[48:55], 0, v235, v235 op_sel_hi:[0,0,0]
	v_mfma_scale_f32_16x16x128_f8f6f4 v[80:83], v[8:15], v[40:47], 0, v235, v235 op_sel_hi:[0,0,0]
	v_mfma_scale_f32_16x16x128_f8f6f4 v[76:79], v[0:7], v[40:47], 0, v235, v235 op_sel_hi:[0,0,0]
	v_mfma_scale_f32_16x16x128_f8f6f4 v[72:75], v[8:15], v[32:39], 0, v235, v235 op_sel_hi:[0,0,0]
	v_mfma_scale_f32_16x16x128_f8f6f4 v[68:71], v[0:7], v[32:39], 0, v235, v235 op_sel_hi:[0,0,0]
	s_setprio 0
	s_barrier
	ds_read_b128 v[16:19], v233 offset:0x8000
	ds_read_b128 v[20:23], v233 offset:0x8400
	ds_read_b128 v[24:27], v233 offset:0x8800
	ds_read_b128 v[28:31], v233 offset:0x8c00
	s_mov_b32 m0, s62
	s_add_i32 s10, s88, 0x10100
	ds_read_b128 v[32:35], v232 offset:0x8000
	ds_read_b128 v[36:39], v232 offset:0x8400
	ds_read_b128 v[40:43], v232 offset:0x8800
	ds_read_b128 v[44:47], v232 offset:0x8c00
	ds_read_b128 v[48:51], v232 offset:0x9000
	ds_read_b128 v[52:55], v232 offset:0x9400
	ds_read_b128 v[56:59], v232 offset:0x9800
	ds_read_b128 v[60:63], v232 offset:0x9c00
	ds_read_b128 v[8:11], v233 offset:0xc000
	ds_read_b128 v[12:15], v233 offset:0xc400
	ds_read_b128 v[0:3], v233 offset:0xc800
	ds_read_b128 v[4:7], v233 offset:0xcc00
	buffer_load_dwordx4 v230, s[4:7], s10 offen lds
	s_add_i32 s10, s88, 0x18100
	s_mov_b32 m0, s63
	s_nop 0
	buffer_load_dwordx4 v230, s[4:7], s10 offen lds
	s_waitcnt vmcnt(8)
	s_waitcnt lgkmcnt(4)
	s_barrier
	s_setprio 1
	v_mfma_scale_f32_16x16x128_f8f6f4 v[192:195], v[16:23], v[32:39], v[192:195], v235, v235 op_sel_hi:[0,0,0]
	v_mfma_scale_f32_16x16x128_f8f6f4 v[188:191], v[24:31], v[32:39], v[188:191], v235, v235 op_sel_hi:[0,0,0]
	v_mfma_scale_f32_16x16x128_f8f6f4 v[184:187], v[16:23], v[40:47], v[184:187], v235, v235 op_sel_hi:[0,0,0]
	v_mfma_scale_f32_16x16x128_f8f6f4 v[180:183], v[24:31], v[40:47], v[180:183], v235, v235 op_sel_hi:[0,0,0]
	v_mfma_scale_f32_16x16x128_f8f6f4 v[176:179], v[16:23], v[48:55], v[176:179], v235, v235 op_sel_hi:[0,0,0]
	v_mfma_scale_f32_16x16x128_f8f6f4 v[172:175], v[24:31], v[48:55], v[172:175], v235, v235 op_sel_hi:[0,0,0]
	v_mfma_scale_f32_16x16x128_f8f6f4 v[168:171], v[16:23], v[56:63], v[168:171], v235, v235 op_sel_hi:[0,0,0]
	v_mfma_scale_f32_16x16x128_f8f6f4 v[164:167], v[24:31], v[56:63], v[164:167], v235, v235 op_sel_hi:[0,0,0]
	s_setprio 0
	s_setprio 1
	s_waitcnt lgkmcnt(2)
	v_mfma_scale_f32_16x16x128_f8f6f4 v[160:163], v[8:15], v[32:39], v[160:163], v235, v235 op_sel_hi:[0,0,0]
	s_waitcnt lgkmcnt(0)
	v_mfma_scale_f32_16x16x128_f8f6f4 v[156:159], v[0:7], v[32:39], v[156:159], v235, v235 op_sel_hi:[0,0,0]
	v_mfma_scale_f32_16x16x128_f8f6f4 v[152:155], v[8:15], v[40:47], v[152:155], v235, v235 op_sel_hi:[0,0,0]
	v_mfma_scale_f32_16x16x128_f8f6f4 v[148:151], v[0:7], v[40:47], v[148:151], v235, v235 op_sel_hi:[0,0,0]
	v_mfma_scale_f32_16x16x128_f8f6f4 v[144:147], v[8:15], v[48:55], v[144:147], v235, v235 op_sel_hi:[0,0,0]
	v_mfma_scale_f32_16x16x128_f8f6f4 v[140:143], v[0:7], v[48:55], v[140:143], v235, v235 op_sel_hi:[0,0,0]
	v_mfma_scale_f32_16x16x128_f8f6f4 v[136:139], v[8:15], v[56:63], v[136:139], v235, v235 op_sel_hi:[0,0,0]
	v_mfma_scale_f32_16x16x128_f8f6f4 v[132:135], v[0:7], v[56:63], v[132:135], v235, v235 op_sel_hi:[0,0,0]
	s_setprio 0
	s_barrier
	s_mov_b32 m0, s64
	s_mov_b32 s10, s6
	s_mov_b32 s11, s7
	ds_read_b128 v[32:35], v232 offset:0xc000
	ds_read_b128 v[36:39], v232 offset:0xc400
	ds_read_b128 v[40:43], v232 offset:0xc800
	ds_read_b128 v[44:47], v232 offset:0xcc00
	ds_read_b128 v[48:51], v232 offset:0xd000
	ds_read_b128 v[52:55], v232 offset:0xd400
	ds_read_b128 v[56:59], v232 offset:0xd800
	ds_read_b128 v[60:63], v232 offset:0xdc00
	buffer_load_dwordx4 v231, s[8:11], s40 offen lds
	s_add_i32 s40, s89, 0x10180
	s_mov_b32 m0, s65
	s_nop 0
	buffer_load_dwordx4 v231, s[8:11], s40 offen lds
	s_add_i32 s40, s89, 0x1180
	s_mov_b32 m0, s70
	s_nop 0
	buffer_load_dwordx4 v231, s[8:11], s40 offen lds
	s_add_i32 s40, s89, 0x11180
	s_mov_b32 m0, s71
	s_nop 0
	buffer_load_dwordx4 v231, s[8:11], s40 offen lds
	s_mov_b32 m0, s68
	s_nop 0
	buffer_load_dwordx4 v230, s[4:7], s33 offen lds
	s_add_i32 s33, s88, 0x8180
	s_mov_b32 m0, s69
	s_nop 0
	buffer_load_dwordx4 v230, s[4:7], s33 offen lds
	s_waitcnt vmcnt(8)
	s_waitcnt lgkmcnt(0)
	s_barrier
	s_setprio 1
	v_mfma_scale_f32_16x16x128_f8f6f4 v[128:131], v[16:23], v[32:39], v[128:131], v235, v235 op_sel_hi:[0,0,0]
	v_mfma_scale_f32_16x16x128_f8f6f4 v[124:127], v[24:31], v[32:39], v[124:127], v235, v235 op_sel_hi:[0,0,0]
	v_mfma_scale_f32_16x16x128_f8f6f4 v[120:123], v[16:23], v[40:47], v[120:123], v235, v235 op_sel_hi:[0,0,0]
	v_mfma_scale_f32_16x16x128_f8f6f4 v[116:119], v[24:31], v[40:47], v[116:119], v235, v235 op_sel_hi:[0,0,0]
	v_mfma_scale_f32_16x16x128_f8f6f4 v[112:115], v[16:23], v[48:55], v[112:115], v235, v235 op_sel_hi:[0,0,0]
	v_mfma_scale_f32_16x16x128_f8f6f4 v[108:111], v[24:31], v[48:55], v[108:111], v235, v235 op_sel_hi:[0,0,0]
	v_mfma_scale_f32_16x16x128_f8f6f4 v[104:107], v[16:23], v[56:63], v[104:107], v235, v235 op_sel_hi:[0,0,0]
	v_mfma_scale_f32_16x16x128_f8f6f4 v[100:103], v[24:31], v[56:63], v[100:103], v235, v235 op_sel_hi:[0,0,0]
	s_setprio 0
	s_setprio 1
	v_mfma_scale_f32_16x16x128_f8f6f4 v[96:99], v[8:15], v[32:39], v[96:99], v235, v235 op_sel_hi:[0,0,0]
	v_mfma_scale_f32_16x16x128_f8f6f4 v[92:95], v[0:7], v[32:39], v[92:95], v235, v235 op_sel_hi:[0,0,0]
	v_mfma_scale_f32_16x16x128_f8f6f4 v[88:91], v[8:15], v[40:47], v[88:91], v235, v235 op_sel_hi:[0,0,0]
	v_mfma_scale_f32_16x16x128_f8f6f4 v[84:87], v[0:7], v[40:47], v[84:87], v235, v235 op_sel_hi:[0,0,0]
	v_mfma_scale_f32_16x16x128_f8f6f4 v[80:83], v[8:15], v[48:55], v[80:83], v235, v235 op_sel_hi:[0,0,0]
	v_mfma_scale_f32_16x16x128_f8f6f4 v[76:79], v[0:7], v[48:55], v[76:79], v235, v235 op_sel_hi:[0,0,0]
	v_mfma_scale_f32_16x16x128_f8f6f4 v[72:75], v[8:15], v[56:63], v[72:75], v235, v235 op_sel_hi:[0,0,0]
	v_mfma_scale_f32_16x16x128_f8f6f4 v[68:71], v[0:7], v[56:63], v[68:71], v235, v235 op_sel_hi:[0,0,0]
	s_setprio 0
	s_barrier
	ds_read_b128 v[16:19], v233 offset:0
	ds_read_b128 v[20:23], v233 offset:0x400
	ds_read_b128 v[24:27], v233 offset:0x800
	ds_read_b128 v[28:31], v233 offset:0xc00
	s_add_i32 s33, s85, 0x80
	s_mov_b32 m0, s74
	s_add_i32 s40, s88, 0x10180
	ds_read_b128 v[32:35], v232 offset:0
	ds_read_b128 v[36:39], v232 offset:0x400
	ds_read_b128 v[40:43], v232 offset:0x800
	ds_read_b128 v[44:47], v232 offset:0xc00
	ds_read_b128 v[48:51], v232 offset:0x1000
	ds_read_b128 v[52:55], v232 offset:0x1400
	ds_read_b128 v[56:59], v232 offset:0x1800
	ds_read_b128 v[60:63], v232 offset:0x1c00
	ds_read_b128 v[8:11], v233 offset:0x4000
	ds_read_b128 v[12:15], v233 offset:0x4400
	ds_read_b128 v[0:3], v233 offset:0x4800
	ds_read_b128 v[4:7], v233 offset:0x4c00
	buffer_load_dwordx4 v230, s[4:7], s40 offen lds
	s_add_i32 s40, s88, 0x18180
	s_mov_b32 m0, s76
	s_nop 0
	buffer_load_dwordx4 v230, s[4:7], s40 offen lds
	s_waitcnt vmcnt(8)
	s_waitcnt lgkmcnt(4)
	s_barrier
	s_setprio 1
	v_mfma_scale_f32_16x16x128_f8f6f4 v[192:195], v[16:23], v[32:39], v[192:195], v235, v235 op_sel_hi:[0,0,0]
	v_mfma_scale_f32_16x16x128_f8f6f4 v[188:191], v[24:31], v[32:39], v[188:191], v235, v235 op_sel_hi:[0,0,0]
	v_mfma_scale_f32_16x16x128_f8f6f4 v[184:187], v[16:23], v[40:47], v[184:187], v235, v235 op_sel_hi:[0,0,0]
	v_mfma_scale_f32_16x16x128_f8f6f4 v[180:183], v[24:31], v[40:47], v[180:183], v235, v235 op_sel_hi:[0,0,0]
	v_mfma_scale_f32_16x16x128_f8f6f4 v[176:179], v[16:23], v[48:55], v[176:179], v235, v235 op_sel_hi:[0,0,0]
	v_mfma_scale_f32_16x16x128_f8f6f4 v[172:175], v[24:31], v[48:55], v[172:175], v235, v235 op_sel_hi:[0,0,0]
	v_mfma_scale_f32_16x16x128_f8f6f4 v[168:171], v[16:23], v[56:63], v[168:171], v235, v235 op_sel_hi:[0,0,0]
	v_mfma_scale_f32_16x16x128_f8f6f4 v[164:167], v[24:31], v[56:63], v[164:167], v235, v235 op_sel_hi:[0,0,0]
	s_setprio 0
	s_setprio 1
	s_waitcnt lgkmcnt(2)
	v_mfma_scale_f32_16x16x128_f8f6f4 v[160:163], v[8:15], v[32:39], v[160:163], v235, v235 op_sel_hi:[0,0,0]
	s_waitcnt lgkmcnt(0)
	v_mfma_scale_f32_16x16x128_f8f6f4 v[156:159], v[0:7], v[32:39], v[156:159], v235, v235 op_sel_hi:[0,0,0]
	v_mfma_scale_f32_16x16x128_f8f6f4 v[152:155], v[8:15], v[40:47], v[152:155], v235, v235 op_sel_hi:[0,0,0]
	v_mfma_scale_f32_16x16x128_f8f6f4 v[148:151], v[0:7], v[40:47], v[148:151], v235, v235 op_sel_hi:[0,0,0]
	v_mfma_scale_f32_16x16x128_f8f6f4 v[144:147], v[8:15], v[48:55], v[144:147], v235, v235 op_sel_hi:[0,0,0]
	v_mfma_scale_f32_16x16x128_f8f6f4 v[140:143], v[0:7], v[48:55], v[140:143], v235, v235 op_sel_hi:[0,0,0]
	v_mfma_scale_f32_16x16x128_f8f6f4 v[136:139], v[8:15], v[56:63], v[136:139], v235, v235 op_sel_hi:[0,0,0]
	v_mfma_scale_f32_16x16x128_f8f6f4 v[132:135], v[0:7], v[56:63], v[132:135], v235, v235 op_sel_hi:[0,0,0]
	s_setprio 0
	s_barrier
	s_mov_b32 m0, s46
	ds_read_b128 v[32:35], v232 offset:0x4000
	ds_read_b128 v[36:39], v232 offset:0x4400
	ds_read_b128 v[40:43], v232 offset:0x4800
	ds_read_b128 v[44:47], v232 offset:0x4c00
	ds_read_b128 v[48:51], v232 offset:0x5000
	ds_read_b128 v[52:55], v232 offset:0x5400
	ds_read_b128 v[56:59], v232 offset:0x5800
	ds_read_b128 v[60:63], v232 offset:0x5c00
	s_nop 0
	buffer_load_dwordx4 v231, s[8:11], s86 offen lds
	s_add_i32 s40, s86, 0x10000
	s_mov_b32 m0, s47
	s_nop 0
	buffer_load_dwordx4 v231, s[8:11], s40 offen lds
	s_add_i32 s40, s86, 0x1000
	s_mov_b32 m0, s49
	s_nop 0
	buffer_load_dwordx4 v231, s[8:11], s40 offen lds
	s_add_i32 s40, s86, 0x11000
	s_mov_b32 m0, s50
	s_nop 0
	buffer_load_dwordx4 v231, s[8:11], s40 offen lds
	s_mov_b32 m0, s48
	s_add_i32 s40, s85, 0x8000
	buffer_load_dwordx4 v230, s[4:7], s85 offen lds
	s_mov_b32 m0, s51
	s_nop 0
	buffer_load_dwordx4 v230, s[4:7], s40 offen lds
	s_waitcnt vmcnt(8)
	s_waitcnt lgkmcnt(0)
	s_barrier
	s_setprio 1
	v_mfma_scale_f32_16x16x128_f8f6f4 v[128:131], v[16:23], v[32:39], v[128:131], v235, v235 op_sel_hi:[0,0,0]
	v_mfma_scale_f32_16x16x128_f8f6f4 v[124:127], v[24:31], v[32:39], v[124:127], v235, v235 op_sel_hi:[0,0,0]
	v_mfma_scale_f32_16x16x128_f8f6f4 v[120:123], v[16:23], v[40:47], v[120:123], v235, v235 op_sel_hi:[0,0,0]
	v_mfma_scale_f32_16x16x128_f8f6f4 v[116:119], v[24:31], v[40:47], v[116:119], v235, v235 op_sel_hi:[0,0,0]
	v_mfma_scale_f32_16x16x128_f8f6f4 v[112:115], v[16:23], v[48:55], v[112:115], v235, v235 op_sel_hi:[0,0,0]
	v_mfma_scale_f32_16x16x128_f8f6f4 v[108:111], v[24:31], v[48:55], v[108:111], v235, v235 op_sel_hi:[0,0,0]
	v_mfma_scale_f32_16x16x128_f8f6f4 v[104:107], v[16:23], v[56:63], v[104:107], v235, v235 op_sel_hi:[0,0,0]
	v_mfma_scale_f32_16x16x128_f8f6f4 v[100:103], v[24:31], v[56:63], v[100:103], v235, v235 op_sel_hi:[0,0,0]
	s_setprio 0
	s_setprio 1
	v_mfma_scale_f32_16x16x128_f8f6f4 v[96:99], v[8:15], v[32:39], v[96:99], v235, v235 op_sel_hi:[0,0,0]
	v_mfma_scale_f32_16x16x128_f8f6f4 v[92:95], v[0:7], v[32:39], v[92:95], v235, v235 op_sel_hi:[0,0,0]
	v_mfma_scale_f32_16x16x128_f8f6f4 v[88:91], v[8:15], v[40:47], v[88:91], v235, v235 op_sel_hi:[0,0,0]
	v_mfma_scale_f32_16x16x128_f8f6f4 v[84:87], v[0:7], v[40:47], v[84:87], v235, v235 op_sel_hi:[0,0,0]
	v_mfma_scale_f32_16x16x128_f8f6f4 v[80:83], v[8:15], v[48:55], v[80:83], v235, v235 op_sel_hi:[0,0,0]
	v_mfma_scale_f32_16x16x128_f8f6f4 v[76:79], v[0:7], v[48:55], v[76:79], v235, v235 op_sel_hi:[0,0,0]
	v_mfma_scale_f32_16x16x128_f8f6f4 v[72:75], v[8:15], v[56:63], v[72:75], v235, v235 op_sel_hi:[0,0,0]
	v_mfma_scale_f32_16x16x128_f8f6f4 v[68:71], v[0:7], v[56:63], v[68:71], v235, v235 op_sel_hi:[0,0,0]
	s_setprio 0
	s_barrier
	ds_read_b128 v[16:19], v233 offset:0x8000
	ds_read_b128 v[20:23], v233 offset:0x8400
	ds_read_b128 v[24:27], v233 offset:0x8800
	ds_read_b128 v[28:31], v233 offset:0x8c00
	s_mov_b32 m0, s62
	s_add_i32 s40, s85, 0x10000
	ds_read_b128 v[32:35], v232 offset:0x8000
	ds_read_b128 v[36:39], v232 offset:0x8400
	ds_read_b128 v[40:43], v232 offset:0x8800
	ds_read_b128 v[44:47], v232 offset:0x8c00
	ds_read_b128 v[48:51], v232 offset:0x9000
	ds_read_b128 v[52:55], v232 offset:0x9400
	ds_read_b128 v[56:59], v232 offset:0x9800
	ds_read_b128 v[60:63], v232 offset:0x9c00
	ds_read_b128 v[8:11], v233 offset:0xc000
	ds_read_b128 v[12:15], v233 offset:0xc400
	ds_read_b128 v[0:3], v233 offset:0xc800
	ds_read_b128 v[4:7], v233 offset:0xcc00
	buffer_load_dwordx4 v230, s[4:7], s40 offen lds
	s_add_i32 s40, s85, 0x18000
	s_mov_b32 m0, s63
	s_nop 0
	buffer_load_dwordx4 v230, s[4:7], s40 offen lds
	s_waitcnt vmcnt(8)
	s_waitcnt lgkmcnt(4)
	s_barrier
	s_setprio 1
	v_mfma_scale_f32_16x16x128_f8f6f4 v[192:195], v[16:23], v[32:39], v[192:195], v235, v235 op_sel_hi:[0,0,0]
	v_mfma_scale_f32_16x16x128_f8f6f4 v[188:191], v[24:31], v[32:39], v[188:191], v235, v235 op_sel_hi:[0,0,0]
	v_mfma_scale_f32_16x16x128_f8f6f4 v[184:187], v[16:23], v[40:47], v[184:187], v235, v235 op_sel_hi:[0,0,0]
	v_mfma_scale_f32_16x16x128_f8f6f4 v[180:183], v[24:31], v[40:47], v[180:183], v235, v235 op_sel_hi:[0,0,0]
	v_mfma_scale_f32_16x16x128_f8f6f4 v[176:179], v[16:23], v[48:55], v[176:179], v235, v235 op_sel_hi:[0,0,0]
	v_mfma_scale_f32_16x16x128_f8f6f4 v[172:175], v[24:31], v[48:55], v[172:175], v235, v235 op_sel_hi:[0,0,0]
	v_mfma_scale_f32_16x16x128_f8f6f4 v[168:171], v[16:23], v[56:63], v[168:171], v235, v235 op_sel_hi:[0,0,0]
	v_mfma_scale_f32_16x16x128_f8f6f4 v[164:167], v[24:31], v[56:63], v[164:167], v235, v235 op_sel_hi:[0,0,0]
	s_setprio 0
	s_setprio 1
	s_waitcnt lgkmcnt(2)
	v_mfma_scale_f32_16x16x128_f8f6f4 v[160:163], v[8:15], v[32:39], v[160:163], v235, v235 op_sel_hi:[0,0,0]
	s_waitcnt lgkmcnt(0)
	v_mfma_scale_f32_16x16x128_f8f6f4 v[156:159], v[0:7], v[32:39], v[156:159], v235, v235 op_sel_hi:[0,0,0]
	v_mfma_scale_f32_16x16x128_f8f6f4 v[152:155], v[8:15], v[40:47], v[152:155], v235, v235 op_sel_hi:[0,0,0]
	v_mfma_scale_f32_16x16x128_f8f6f4 v[148:151], v[0:7], v[40:47], v[148:151], v235, v235 op_sel_hi:[0,0,0]
	v_mfma_scale_f32_16x16x128_f8f6f4 v[144:147], v[8:15], v[48:55], v[144:147], v235, v235 op_sel_hi:[0,0,0]
	v_mfma_scale_f32_16x16x128_f8f6f4 v[140:143], v[0:7], v[48:55], v[140:143], v235, v235 op_sel_hi:[0,0,0]
	v_mfma_scale_f32_16x16x128_f8f6f4 v[136:139], v[8:15], v[56:63], v[136:139], v235, v235 op_sel_hi:[0,0,0]
	v_mfma_scale_f32_16x16x128_f8f6f4 v[132:135], v[0:7], v[56:63], v[132:135], v235, v235 op_sel_hi:[0,0,0]
	s_setprio 0
	s_barrier
	s_mov_b32 m0, s64
	s_add_i32 s40, s86, 0x80
	ds_read_b128 v[32:35], v232 offset:0xc000
	ds_read_b128 v[36:39], v232 offset:0xc400
	ds_read_b128 v[40:43], v232 offset:0xc800
	ds_read_b128 v[44:47], v232 offset:0xcc00
	ds_read_b128 v[48:51], v232 offset:0xd000
	ds_read_b128 v[52:55], v232 offset:0xd400
	ds_read_b128 v[56:59], v232 offset:0xd800
	ds_read_b128 v[60:63], v232 offset:0xdc00
	buffer_load_dwordx4 v231, s[8:11], s40 offen lds
	s_add_i32 s40, s86, 0x10080
	s_mov_b32 m0, s65
	s_nop 0
	buffer_load_dwordx4 v231, s[8:11], s40 offen lds
	s_add_i32 s40, s86, 0x1080
	s_mov_b32 m0, s70
	s_nop 0
	buffer_load_dwordx4 v231, s[8:11], s40 offen lds
	s_add_i32 s40, s86, 0x11080
	s_mov_b32 m0, s71
	s_nop 0
	buffer_load_dwordx4 v231, s[8:11], s40 offen lds
	s_mov_b32 m0, s68
	s_add_i32 s10, s85, 0x8080
	buffer_load_dwordx4 v230, s[4:7], s33 offen lds
	s_mov_b32 m0, s69
	s_nop 0
	buffer_load_dwordx4 v230, s[4:7], s10 offen lds
	s_waitcnt vmcnt(8)
	s_waitcnt lgkmcnt(0)
	s_barrier
	s_setprio 1
	v_mfma_scale_f32_16x16x128_f8f6f4 v[128:131], v[16:23], v[32:39], v[128:131], v235, v235 op_sel_hi:[0,0,0]
	v_mfma_scale_f32_16x16x128_f8f6f4 v[124:127], v[24:31], v[32:39], v[124:127], v235, v235 op_sel_hi:[0,0,0]
	v_mfma_scale_f32_16x16x128_f8f6f4 v[120:123], v[16:23], v[40:47], v[120:123], v235, v235 op_sel_hi:[0,0,0]
	v_mfma_scale_f32_16x16x128_f8f6f4 v[116:119], v[24:31], v[40:47], v[116:119], v235, v235 op_sel_hi:[0,0,0]
	v_mfma_scale_f32_16x16x128_f8f6f4 v[112:115], v[16:23], v[48:55], v[112:115], v235, v235 op_sel_hi:[0,0,0]
	v_mfma_scale_f32_16x16x128_f8f6f4 v[108:111], v[24:31], v[48:55], v[108:111], v235, v235 op_sel_hi:[0,0,0]
	v_mfma_scale_f32_16x16x128_f8f6f4 v[104:107], v[16:23], v[56:63], v[104:107], v235, v235 op_sel_hi:[0,0,0]
	v_mfma_scale_f32_16x16x128_f8f6f4 v[100:103], v[24:31], v[56:63], v[100:103], v235, v235 op_sel_hi:[0,0,0]
	s_setprio 0
	s_setprio 1
	v_mfma_scale_f32_16x16x128_f8f6f4 v[96:99], v[8:15], v[32:39], v[96:99], v235, v235 op_sel_hi:[0,0,0]
	v_mfma_scale_f32_16x16x128_f8f6f4 v[92:95], v[0:7], v[32:39], v[92:95], v235, v235 op_sel_hi:[0,0,0]
	v_mfma_scale_f32_16x16x128_f8f6f4 v[88:91], v[8:15], v[40:47], v[88:91], v235, v235 op_sel_hi:[0,0,0]
	v_mfma_scale_f32_16x16x128_f8f6f4 v[84:87], v[0:7], v[40:47], v[84:87], v235, v235 op_sel_hi:[0,0,0]
	v_mfma_scale_f32_16x16x128_f8f6f4 v[80:83], v[8:15], v[48:55], v[80:83], v235, v235 op_sel_hi:[0,0,0]
	v_mfma_scale_f32_16x16x128_f8f6f4 v[76:79], v[0:7], v[48:55], v[76:79], v235, v235 op_sel_hi:[0,0,0]
	v_mfma_scale_f32_16x16x128_f8f6f4 v[72:75], v[8:15], v[56:63], v[72:75], v235, v235 op_sel_hi:[0,0,0]
	v_mfma_scale_f32_16x16x128_f8f6f4 v[68:71], v[0:7], v[56:63], v[68:71], v235, v235 op_sel_hi:[0,0,0]
	s_setprio 0
	s_barrier
	s_andn2_b64 vcc, exec, s[20:21]
	s_cbranch_vccnz .LBB0_1371
	s_barrier

.LBB0_1452:
	s_add_i32 s33, s80, 0x180
	s_add_i32 s36, s81, 0x180
	s_waitcnt lgkmcnt(0)
	s_barrier
	s_setprio 1
	v_mfma_scale_f32_16x16x128_f8f6f4 v[128:131], v[24:31], v[56:63], 0, v235, v235 op_sel_hi:[0,0,0]
	v_mfma_scale_f32_16x16x128_f8f6f4 v[124:127], v[16:23], v[56:63], 0, v235, v235 op_sel_hi:[0,0,0]
	v_mfma_scale_f32_16x16x128_f8f6f4 v[120:123], v[24:31], v[48:55], 0, v235, v235 op_sel_hi:[0,0,0]
	v_mfma_scale_f32_16x16x128_f8f6f4 v[116:119], v[16:23], v[48:55], 0, v235, v235 op_sel_hi:[0,0,0]
	v_mfma_scale_f32_16x16x128_f8f6f4 v[112:115], v[24:31], v[40:47], 0, v235, v235 op_sel_hi:[0,0,0]
	v_mfma_scale_f32_16x16x128_f8f6f4 v[108:111], v[16:23], v[40:47], 0, v235, v235 op_sel_hi:[0,0,0]
	v_mfma_scale_f32_16x16x128_f8f6f4 v[104:107], v[24:31], v[32:39], 0, v235, v235 op_sel_hi:[0,0,0]
	v_mfma_scale_f32_16x16x128_f8f6f4 v[100:103], v[16:23], v[32:39], 0, v235, v235 op_sel_hi:[0,0,0]
	s_setprio 0
	s_setprio 1
	v_mfma_scale_f32_16x16x128_f8f6f4 v[96:99], v[8:15], v[56:63], 0, v235, v235 op_sel_hi:[0,0,0]
	v_mfma_scale_f32_16x16x128_f8f6f4 v[92:95], v[0:7], v[56:63], 0, v235, v235 op_sel_hi:[0,0,0]
	v_mfma_scale_f32_16x16x128_f8f6f4 v[88:91], v[8:15], v[48:55], 0, v235, v235 op_sel_hi:[0,0,0]
	v_mfma_scale_f32_16x16x128_f8f6f4 v[84:87], v[0:7], v[48:55], 0, v235, v235 op_sel_hi:[0,0,0]
	v_mfma_scale_f32_16x16x128_f8f6f4 v[80:83], v[8:15], v[40:47], 0, v235, v235 op_sel_hi:[0,0,0]
	v_mfma_scale_f32_16x16x128_f8f6f4 v[76:79], v[0:7], v[40:47], 0, v235, v235 op_sel_hi:[0,0,0]
	v_mfma_scale_f32_16x16x128_f8f6f4 v[72:75], v[8:15], v[32:39], 0, v235, v235 op_sel_hi:[0,0,0]
	v_mfma_scale_f32_16x16x128_f8f6f4 v[68:71], v[0:7], v[32:39], 0, v235, v235 op_sel_hi:[0,0,0]
	s_setprio 0
	s_barrier
	ds_read_b128 v[16:19], v233 offset:0x8000
	ds_read_b128 v[20:23], v233 offset:0x8400
	ds_read_b128 v[24:27], v233 offset:0x8800
	ds_read_b128 v[28:31], v233 offset:0x8c00
	s_mov_b32 m0, s62
	s_add_i32 s10, s80, 0x10100
	ds_read_b128 v[32:35], v232 offset:0x8000
	ds_read_b128 v[36:39], v232 offset:0x8400
	ds_read_b128 v[40:43], v232 offset:0x8800
	ds_read_b128 v[44:47], v232 offset:0x8c00
	ds_read_b128 v[48:51], v232 offset:0x9000
	ds_read_b128 v[52:55], v232 offset:0x9400
	ds_read_b128 v[56:59], v232 offset:0x9800
	ds_read_b128 v[60:63], v232 offset:0x9c00
	ds_read_b128 v[8:11], v233 offset:0xc000
	ds_read_b128 v[12:15], v233 offset:0xc400
	ds_read_b128 v[0:3], v233 offset:0xc800
	ds_read_b128 v[4:7], v233 offset:0xcc00
	buffer_load_dwordx4 v230, s[4:7], s10 offen lds
	s_add_i32 s10, s80, 0x18100
	s_mov_b32 m0, s63
	s_nop 0
	buffer_load_dwordx4 v230, s[4:7], s10 offen lds
	s_waitcnt vmcnt(8)
	s_waitcnt lgkmcnt(4)
	s_barrier
	s_setprio 1
	v_mfma_scale_f32_16x16x128_f8f6f4 v[192:195], v[16:23], v[32:39], v[192:195], v235, v235 op_sel_hi:[0,0,0]
	v_mfma_scale_f32_16x16x128_f8f6f4 v[188:191], v[24:31], v[32:39], v[188:191], v235, v235 op_sel_hi:[0,0,0]
	v_mfma_scale_f32_16x16x128_f8f6f4 v[184:187], v[16:23], v[40:47], v[184:187], v235, v235 op_sel_hi:[0,0,0]
	v_mfma_scale_f32_16x16x128_f8f6f4 v[180:183], v[24:31], v[40:47], v[180:183], v235, v235 op_sel_hi:[0,0,0]
	v_mfma_scale_f32_16x16x128_f8f6f4 v[176:179], v[16:23], v[48:55], v[176:179], v235, v235 op_sel_hi:[0,0,0]
	v_mfma_scale_f32_16x16x128_f8f6f4 v[172:175], v[24:31], v[48:55], v[172:175], v235, v235 op_sel_hi:[0,0,0]
	v_mfma_scale_f32_16x16x128_f8f6f4 v[168:171], v[16:23], v[56:63], v[168:171], v235, v235 op_sel_hi:[0,0,0]
	v_mfma_scale_f32_16x16x128_f8f6f4 v[164:167], v[24:31], v[56:63], v[164:167], v235, v235 op_sel_hi:[0,0,0]
	s_setprio 0
	s_setprio 1
	s_waitcnt lgkmcnt(2)
	v_mfma_scale_f32_16x16x128_f8f6f4 v[160:163], v[8:15], v[32:39], v[160:163], v235, v235 op_sel_hi:[0,0,0]
	s_waitcnt lgkmcnt(0)
	v_mfma_scale_f32_16x16x128_f8f6f4 v[156:159], v[0:7], v[32:39], v[156:159], v235, v235 op_sel_hi:[0,0,0]
	v_mfma_scale_f32_16x16x128_f8f6f4 v[152:155], v[8:15], v[40:47], v[152:155], v235, v235 op_sel_hi:[0,0,0]
	v_mfma_scale_f32_16x16x128_f8f6f4 v[148:151], v[0:7], v[40:47], v[148:151], v235, v235 op_sel_hi:[0,0,0]
	v_mfma_scale_f32_16x16x128_f8f6f4 v[144:147], v[8:15], v[48:55], v[144:147], v235, v235 op_sel_hi:[0,0,0]
	v_mfma_scale_f32_16x16x128_f8f6f4 v[140:143], v[0:7], v[48:55], v[140:143], v235, v235 op_sel_hi:[0,0,0]
	v_mfma_scale_f32_16x16x128_f8f6f4 v[136:139], v[8:15], v[56:63], v[136:139], v235, v235 op_sel_hi:[0,0,0]
	v_mfma_scale_f32_16x16x128_f8f6f4 v[132:135], v[0:7], v[56:63], v[132:135], v235, v235 op_sel_hi:[0,0,0]
	s_setprio 0
	s_barrier
	s_mov_b32 m0, s64
	s_mov_b32 s10, s6
	s_mov_b32 s11, s7
	ds_read_b128 v[32:35], v232 offset:0xc000
	ds_read_b128 v[36:39], v232 offset:0xc400
	ds_read_b128 v[40:43], v232 offset:0xc800
	ds_read_b128 v[44:47], v232 offset:0xcc00
	ds_read_b128 v[48:51], v232 offset:0xd000
	ds_read_b128 v[52:55], v232 offset:0xd400
	ds_read_b128 v[56:59], v232 offset:0xd800
	ds_read_b128 v[60:63], v232 offset:0xdc00
	buffer_load_dwordx4 v231, s[8:11], s36 offen lds
	s_add_i32 s36, s81, 0x10180
	s_mov_b32 m0, s65
	s_nop 0
	buffer_load_dwordx4 v231, s[8:11], s36 offen lds
	s_add_i32 s36, s81, 0x1180
	s_mov_b32 m0, s70
	s_nop 0
	buffer_load_dwordx4 v231, s[8:11], s36 offen lds
	s_add_i32 s36, s81, 0x11180
	s_mov_b32 m0, s71
	s_nop 0
	buffer_load_dwordx4 v231, s[8:11], s36 offen lds
	s_mov_b32 m0, s68
	s_nop 0
	buffer_load_dwordx4 v230, s[4:7], s33 offen lds
	s_add_i32 s33, s80, 0x8180
	s_mov_b32 m0, s69
	s_nop 0
	buffer_load_dwordx4 v230, s[4:7], s33 offen lds
	s_waitcnt vmcnt(8)
	s_waitcnt lgkmcnt(0)
	s_barrier
	s_setprio 1
	v_mfma_scale_f32_16x16x128_f8f6f4 v[128:131], v[16:23], v[32:39], v[128:131], v235, v235 op_sel_hi:[0,0,0]
	v_mfma_scale_f32_16x16x128_f8f6f4 v[124:127], v[24:31], v[32:39], v[124:127], v235, v235 op_sel_hi:[0,0,0]
	v_mfma_scale_f32_16x16x128_f8f6f4 v[120:123], v[16:23], v[40:47], v[120:123], v235, v235 op_sel_hi:[0,0,0]
	v_mfma_scale_f32_16x16x128_f8f6f4 v[116:119], v[24:31], v[40:47], v[116:119], v235, v235 op_sel_hi:[0,0,0]
	v_mfma_scale_f32_16x16x128_f8f6f4 v[112:115], v[16:23], v[48:55], v[112:115], v235, v235 op_sel_hi:[0,0,0]
	v_mfma_scale_f32_16x16x128_f8f6f4 v[108:111], v[24:31], v[48:55], v[108:111], v235, v235 op_sel_hi:[0,0,0]
	v_mfma_scale_f32_16x16x128_f8f6f4 v[104:107], v[16:23], v[56:63], v[104:107], v235, v235 op_sel_hi:[0,0,0]
	v_mfma_scale_f32_16x16x128_f8f6f4 v[100:103], v[24:31], v[56:63], v[100:103], v235, v235 op_sel_hi:[0,0,0]
	s_setprio 0
	s_setprio 1
	v_mfma_scale_f32_16x16x128_f8f6f4 v[96:99], v[8:15], v[32:39], v[96:99], v235, v235 op_sel_hi:[0,0,0]
	v_mfma_scale_f32_16x16x128_f8f6f4 v[92:95], v[0:7], v[32:39], v[92:95], v235, v235 op_sel_hi:[0,0,0]
	v_mfma_scale_f32_16x16x128_f8f6f4 v[88:91], v[8:15], v[40:47], v[88:91], v235, v235 op_sel_hi:[0,0,0]
	v_mfma_scale_f32_16x16x128_f8f6f4 v[84:87], v[0:7], v[40:47], v[84:87], v235, v235 op_sel_hi:[0,0,0]
	v_mfma_scale_f32_16x16x128_f8f6f4 v[80:83], v[8:15], v[48:55], v[80:83], v235, v235 op_sel_hi:[0,0,0]
	v_mfma_scale_f32_16x16x128_f8f6f4 v[76:79], v[0:7], v[48:55], v[76:79], v235, v235 op_sel_hi:[0,0,0]
	v_mfma_scale_f32_16x16x128_f8f6f4 v[72:75], v[8:15], v[56:63], v[72:75], v235, v235 op_sel_hi:[0,0,0]
	v_mfma_scale_f32_16x16x128_f8f6f4 v[68:71], v[0:7], v[56:63], v[68:71], v235, v235 op_sel_hi:[0,0,0]
	s_setprio 0
	s_barrier
	ds_read_b128 v[16:19], v233 offset:0
	ds_read_b128 v[20:23], v233 offset:0x400
	ds_read_b128 v[24:27], v233 offset:0x800
	ds_read_b128 v[28:31], v233 offset:0xc00
	s_add_i32 s33, s43, 0x80
	s_mov_b32 m0, s74
	s_add_i32 s36, s80, 0x10180
	ds_read_b128 v[32:35], v232 offset:0
	ds_read_b128 v[36:39], v232 offset:0x400
	ds_read_b128 v[40:43], v232 offset:0x800
	ds_read_b128 v[44:47], v232 offset:0xc00
	ds_read_b128 v[48:51], v232 offset:0x1000
	ds_read_b128 v[52:55], v232 offset:0x1400
	ds_read_b128 v[56:59], v232 offset:0x1800
	ds_read_b128 v[60:63], v232 offset:0x1c00
	ds_read_b128 v[8:11], v233 offset:0x4000
	ds_read_b128 v[12:15], v233 offset:0x4400
	ds_read_b128 v[0:3], v233 offset:0x4800
	ds_read_b128 v[4:7], v233 offset:0x4c00
	buffer_load_dwordx4 v230, s[4:7], s36 offen lds
	s_add_i32 s36, s80, 0x18180
	s_mov_b32 m0, s76
	s_nop 0
	buffer_load_dwordx4 v230, s[4:7], s36 offen lds
	s_waitcnt vmcnt(8)
	s_waitcnt lgkmcnt(4)
	s_barrier
	s_setprio 1
	v_mfma_scale_f32_16x16x128_f8f6f4 v[192:195], v[16:23], v[32:39], v[192:195], v235, v235 op_sel_hi:[0,0,0]
	v_mfma_scale_f32_16x16x128_f8f6f4 v[188:191], v[24:31], v[32:39], v[188:191], v235, v235 op_sel_hi:[0,0,0]
	v_mfma_scale_f32_16x16x128_f8f6f4 v[184:187], v[16:23], v[40:47], v[184:187], v235, v235 op_sel_hi:[0,0,0]
	v_mfma_scale_f32_16x16x128_f8f6f4 v[180:183], v[24:31], v[40:47], v[180:183], v235, v235 op_sel_hi:[0,0,0]
	v_mfma_scale_f32_16x16x128_f8f6f4 v[176:179], v[16:23], v[48:55], v[176:179], v235, v235 op_sel_hi:[0,0,0]
	v_mfma_scale_f32_16x16x128_f8f6f4 v[172:175], v[24:31], v[48:55], v[172:175], v235, v235 op_sel_hi:[0,0,0]
	v_mfma_scale_f32_16x16x128_f8f6f4 v[168:171], v[16:23], v[56:63], v[168:171], v235, v235 op_sel_hi:[0,0,0]
	v_mfma_scale_f32_16x16x128_f8f6f4 v[164:167], v[24:31], v[56:63], v[164:167], v235, v235 op_sel_hi:[0,0,0]
	s_setprio 0
	s_setprio 1
	s_waitcnt lgkmcnt(2)
	v_mfma_scale_f32_16x16x128_f8f6f4 v[160:163], v[8:15], v[32:39], v[160:163], v235, v235 op_sel_hi:[0,0,0]
	s_waitcnt lgkmcnt(0)
	v_mfma_scale_f32_16x16x128_f8f6f4 v[156:159], v[0:7], v[32:39], v[156:159], v235, v235 op_sel_hi:[0,0,0]
	v_mfma_scale_f32_16x16x128_f8f6f4 v[152:155], v[8:15], v[40:47], v[152:155], v235, v235 op_sel_hi:[0,0,0]
	v_mfma_scale_f32_16x16x128_f8f6f4 v[148:151], v[0:7], v[40:47], v[148:151], v235, v235 op_sel_hi:[0,0,0]
	v_mfma_scale_f32_16x16x128_f8f6f4 v[144:147], v[8:15], v[48:55], v[144:147], v235, v235 op_sel_hi:[0,0,0]
	v_mfma_scale_f32_16x16x128_f8f6f4 v[140:143], v[0:7], v[48:55], v[140:143], v235, v235 op_sel_hi:[0,0,0]
	v_mfma_scale_f32_16x16x128_f8f6f4 v[136:139], v[8:15], v[56:63], v[136:139], v235, v235 op_sel_hi:[0,0,0]
	v_mfma_scale_f32_16x16x128_f8f6f4 v[132:135], v[0:7], v[56:63], v[132:135], v235, v235 op_sel_hi:[0,0,0]
	s_setprio 0
	s_barrier
	s_mov_b32 m0, s46
	ds_read_b128 v[32:35], v232 offset:0x4000
	ds_read_b128 v[36:39], v232 offset:0x4400
	ds_read_b128 v[40:43], v232 offset:0x4800
	ds_read_b128 v[44:47], v232 offset:0x4c00
	ds_read_b128 v[48:51], v232 offset:0x5000
	ds_read_b128 v[52:55], v232 offset:0x5400
	ds_read_b128 v[56:59], v232 offset:0x5800
	ds_read_b128 v[60:63], v232 offset:0x5c00
	s_nop 0
	buffer_load_dwordx4 v231, s[8:11], s78 offen lds
	s_add_i32 s36, s78, 0x10000
	s_mov_b32 m0, s47
	s_nop 0
	buffer_load_dwordx4 v231, s[8:11], s36 offen lds
	s_add_i32 s36, s78, 0x1000
	s_mov_b32 m0, s49
	s_nop 0
	buffer_load_dwordx4 v231, s[8:11], s36 offen lds
	s_add_i32 s36, s78, 0x11000
	s_mov_b32 m0, s50
	s_nop 0
	buffer_load_dwordx4 v231, s[8:11], s36 offen lds
	s_mov_b32 m0, s48
	s_add_i32 s36, s43, 0x8000
	buffer_load_dwordx4 v230, s[4:7], s43 offen lds
	s_mov_b32 m0, s51
	s_nop 0
	buffer_load_dwordx4 v230, s[4:7], s36 offen lds
	s_waitcnt vmcnt(8)
	s_waitcnt lgkmcnt(0)
	s_barrier
	s_setprio 1
	v_mfma_scale_f32_16x16x128_f8f6f4 v[128:131], v[16:23], v[32:39], v[128:131], v235, v235 op_sel_hi:[0,0,0]
	v_mfma_scale_f32_16x16x128_f8f6f4 v[124:127], v[24:31], v[32:39], v[124:127], v235, v235 op_sel_hi:[0,0,0]
	v_mfma_scale_f32_16x16x128_f8f6f4 v[120:123], v[16:23], v[40:47], v[120:123], v235, v235 op_sel_hi:[0,0,0]
	v_mfma_scale_f32_16x16x128_f8f6f4 v[116:119], v[24:31], v[40:47], v[116:119], v235, v235 op_sel_hi:[0,0,0]
	v_mfma_scale_f32_16x16x128_f8f6f4 v[112:115], v[16:23], v[48:55], v[112:115], v235, v235 op_sel_hi:[0,0,0]
	v_mfma_scale_f32_16x16x128_f8f6f4 v[108:111], v[24:31], v[48:55], v[108:111], v235, v235 op_sel_hi:[0,0,0]
	v_mfma_scale_f32_16x16x128_f8f6f4 v[104:107], v[16:23], v[56:63], v[104:107], v235, v235 op_sel_hi:[0,0,0]
	v_mfma_scale_f32_16x16x128_f8f6f4 v[100:103], v[24:31], v[56:63], v[100:103], v235, v235 op_sel_hi:[0,0,0]
	s_setprio 0
	s_setprio 1
	v_mfma_scale_f32_16x16x128_f8f6f4 v[96:99], v[8:15], v[32:39], v[96:99], v235, v235 op_sel_hi:[0,0,0]
	v_mfma_scale_f32_16x16x128_f8f6f4 v[92:95], v[0:7], v[32:39], v[92:95], v235, v235 op_sel_hi:[0,0,0]
	v_mfma_scale_f32_16x16x128_f8f6f4 v[88:91], v[8:15], v[40:47], v[88:91], v235, v235 op_sel_hi:[0,0,0]
	v_mfma_scale_f32_16x16x128_f8f6f4 v[84:87], v[0:7], v[40:47], v[84:87], v235, v235 op_sel_hi:[0,0,0]
	v_mfma_scale_f32_16x16x128_f8f6f4 v[80:83], v[8:15], v[48:55], v[80:83], v235, v235 op_sel_hi:[0,0,0]
	v_mfma_scale_f32_16x16x128_f8f6f4 v[76:79], v[0:7], v[48:55], v[76:79], v235, v235 op_sel_hi:[0,0,0]
	v_mfma_scale_f32_16x16x128_f8f6f4 v[72:75], v[8:15], v[56:63], v[72:75], v235, v235 op_sel_hi:[0,0,0]
	v_mfma_scale_f32_16x16x128_f8f6f4 v[68:71], v[0:7], v[56:63], v[68:71], v235, v235 op_sel_hi:[0,0,0]
	s_setprio 0
	s_barrier
	ds_read_b128 v[16:19], v233 offset:0x8000
	ds_read_b128 v[20:23], v233 offset:0x8400
	ds_read_b128 v[24:27], v233 offset:0x8800
	ds_read_b128 v[28:31], v233 offset:0x8c00
	s_mov_b32 m0, s62
	s_add_i32 s36, s43, 0x10000
	ds_read_b128 v[32:35], v232 offset:0x8000
	ds_read_b128 v[36:39], v232 offset:0x8400
	ds_read_b128 v[40:43], v232 offset:0x8800
	ds_read_b128 v[44:47], v232 offset:0x8c00
	ds_read_b128 v[48:51], v232 offset:0x9000
	ds_read_b128 v[52:55], v232 offset:0x9400
	ds_read_b128 v[56:59], v232 offset:0x9800
	ds_read_b128 v[60:63], v232 offset:0x9c00
	ds_read_b128 v[8:11], v233 offset:0xc000
	ds_read_b128 v[12:15], v233 offset:0xc400
	ds_read_b128 v[0:3], v233 offset:0xc800
	ds_read_b128 v[4:7], v233 offset:0xcc00
	buffer_load_dwordx4 v230, s[4:7], s36 offen lds
	s_add_i32 s36, s43, 0x18000
	s_mov_b32 m0, s63
	s_nop 0
	buffer_load_dwordx4 v230, s[4:7], s36 offen lds
	s_waitcnt vmcnt(8)
	s_waitcnt lgkmcnt(4)
	s_barrier
	s_setprio 1
	v_mfma_scale_f32_16x16x128_f8f6f4 v[192:195], v[16:23], v[32:39], v[192:195], v235, v235 op_sel_hi:[0,0,0]
	v_mfma_scale_f32_16x16x128_f8f6f4 v[188:191], v[24:31], v[32:39], v[188:191], v235, v235 op_sel_hi:[0,0,0]
	v_mfma_scale_f32_16x16x128_f8f6f4 v[184:187], v[16:23], v[40:47], v[184:187], v235, v235 op_sel_hi:[0,0,0]
	v_mfma_scale_f32_16x16x128_f8f6f4 v[180:183], v[24:31], v[40:47], v[180:183], v235, v235 op_sel_hi:[0,0,0]
	v_mfma_scale_f32_16x16x128_f8f6f4 v[176:179], v[16:23], v[48:55], v[176:179], v235, v235 op_sel_hi:[0,0,0]
	v_mfma_scale_f32_16x16x128_f8f6f4 v[172:175], v[24:31], v[48:55], v[172:175], v235, v235 op_sel_hi:[0,0,0]
	v_mfma_scale_f32_16x16x128_f8f6f4 v[168:171], v[16:23], v[56:63], v[168:171], v235, v235 op_sel_hi:[0,0,0]
	v_mfma_scale_f32_16x16x128_f8f6f4 v[164:167], v[24:31], v[56:63], v[164:167], v235, v235 op_sel_hi:[0,0,0]
	s_setprio 0
	s_setprio 1
	s_waitcnt lgkmcnt(2)
	v_mfma_scale_f32_16x16x128_f8f6f4 v[160:163], v[8:15], v[32:39], v[160:163], v235, v235 op_sel_hi:[0,0,0]
	s_waitcnt lgkmcnt(0)
	v_mfma_scale_f32_16x16x128_f8f6f4 v[156:159], v[0:7], v[32:39], v[156:159], v235, v235 op_sel_hi:[0,0,0]
	v_mfma_scale_f32_16x16x128_f8f6f4 v[152:155], v[8:15], v[40:47], v[152:155], v235, v235 op_sel_hi:[0,0,0]
	v_mfma_scale_f32_16x16x128_f8f6f4 v[148:151], v[0:7], v[40:47], v[148:151], v235, v235 op_sel_hi:[0,0,0]
	v_mfma_scale_f32_16x16x128_f8f6f4 v[144:147], v[8:15], v[48:55], v[144:147], v235, v235 op_sel_hi:[0,0,0]
	v_mfma_scale_f32_16x16x128_f8f6f4 v[140:143], v[0:7], v[48:55], v[140:143], v235, v235 op_sel_hi:[0,0,0]
	v_mfma_scale_f32_16x16x128_f8f6f4 v[136:139], v[8:15], v[56:63], v[136:139], v235, v235 op_sel_hi:[0,0,0]
	v_mfma_scale_f32_16x16x128_f8f6f4 v[132:135], v[0:7], v[56:63], v[132:135], v235, v235 op_sel_hi:[0,0,0]
	s_setprio 0
	s_barrier
	s_mov_b32 m0, s64
	s_add_i32 s36, s78, 0x80
	ds_read_b128 v[32:35], v232 offset:0xc000
	ds_read_b128 v[36:39], v232 offset:0xc400
	ds_read_b128 v[40:43], v232 offset:0xc800
	ds_read_b128 v[44:47], v232 offset:0xcc00
	ds_read_b128 v[48:51], v232 offset:0xd000
	ds_read_b128 v[52:55], v232 offset:0xd400
	ds_read_b128 v[56:59], v232 offset:0xd800
	ds_read_b128 v[60:63], v232 offset:0xdc00
	buffer_load_dwordx4 v231, s[8:11], s36 offen lds
	s_add_i32 s36, s78, 0x10080
	s_mov_b32 m0, s65
	s_nop 0
	buffer_load_dwordx4 v231, s[8:11], s36 offen lds
	s_add_i32 s36, s78, 0x1080
	s_mov_b32 m0, s70
	s_nop 0
	buffer_load_dwordx4 v231, s[8:11], s36 offen lds
	s_add_i32 s36, s78, 0x11080
	s_mov_b32 m0, s71
	s_nop 0
	buffer_load_dwordx4 v231, s[8:11], s36 offen lds
	s_mov_b32 m0, s68
	s_add_i32 s10, s43, 0x8080
	buffer_load_dwordx4 v230, s[4:7], s33 offen lds
	s_mov_b32 m0, s69
	s_nop 0
	buffer_load_dwordx4 v230, s[4:7], s10 offen lds
	s_waitcnt vmcnt(8)
	s_waitcnt lgkmcnt(0)
	s_barrier
	s_setprio 1
	v_mfma_scale_f32_16x16x128_f8f6f4 v[128:131], v[16:23], v[32:39], v[128:131], v235, v235 op_sel_hi:[0,0,0]
	v_mfma_scale_f32_16x16x128_f8f6f4 v[124:127], v[24:31], v[32:39], v[124:127], v235, v235 op_sel_hi:[0,0,0]
	v_mfma_scale_f32_16x16x128_f8f6f4 v[120:123], v[16:23], v[40:47], v[120:123], v235, v235 op_sel_hi:[0,0,0]
	v_mfma_scale_f32_16x16x128_f8f6f4 v[116:119], v[24:31], v[40:47], v[116:119], v235, v235 op_sel_hi:[0,0,0]
	v_mfma_scale_f32_16x16x128_f8f6f4 v[112:115], v[16:23], v[48:55], v[112:115], v235, v235 op_sel_hi:[0,0,0]
	v_mfma_scale_f32_16x16x128_f8f6f4 v[108:111], v[24:31], v[48:55], v[108:111], v235, v235 op_sel_hi:[0,0,0]
	v_mfma_scale_f32_16x16x128_f8f6f4 v[104:107], v[16:23], v[56:63], v[104:107], v235, v235 op_sel_hi:[0,0,0]
	v_mfma_scale_f32_16x16x128_f8f6f4 v[100:103], v[24:31], v[56:63], v[100:103], v235, v235 op_sel_hi:[0,0,0]
	s_setprio 0
	s_setprio 1
	v_mfma_scale_f32_16x16x128_f8f6f4 v[96:99], v[8:15], v[32:39], v[96:99], v235, v235 op_sel_hi:[0,0,0]
	v_mfma_scale_f32_16x16x128_f8f6f4 v[92:95], v[0:7], v[32:39], v[92:95], v235, v235 op_sel_hi:[0,0,0]
	v_mfma_scale_f32_16x16x128_f8f6f4 v[88:91], v[8:15], v[40:47], v[88:91], v235, v235 op_sel_hi:[0,0,0]
	v_mfma_scale_f32_16x16x128_f8f6f4 v[84:87], v[0:7], v[40:47], v[84:87], v235, v235 op_sel_hi:[0,0,0]
	v_mfma_scale_f32_16x16x128_f8f6f4 v[80:83], v[8:15], v[48:55], v[80:83], v235, v235 op_sel_hi:[0,0,0]
	v_mfma_scale_f32_16x16x128_f8f6f4 v[76:79], v[0:7], v[48:55], v[76:79], v235, v235 op_sel_hi:[0,0,0]
	v_mfma_scale_f32_16x16x128_f8f6f4 v[72:75], v[8:15], v[56:63], v[72:75], v235, v235 op_sel_hi:[0,0,0]
	v_mfma_scale_f32_16x16x128_f8f6f4 v[68:71], v[0:7], v[56:63], v[68:71], v235, v235 op_sel_hi:[0,0,0]
	s_setprio 0
	s_barrier
	s_andn2_b64 vcc, exec, s[20:21]
	s_cbranch_vccnz .LBB0_1454
	s_barrier
